# full back-edge rotation: loop-back branch before the barrier, barrier copy at the loop head, in the 8 GEMM K-loops
# baseline (speedup 1.0000x reference)
; template <class Epi, class Sched, bool ALIGN_EPI = false, bool SP2 = false, bool FP8 = false>
; __device__ __forceinline__ void gemm_phase(PG8_LAS unsigned char* lds, const Gemm g, const Sched& S, const Epi& E) {
;     ...
;     for (;;) {
;         const bool has_next = S.next(ui + 1, nxt);
;         const char* nA = has_next ? (const char*)g.A + (size_t)nxt.pm * tstep : cA; const char* nB = has_next ? (const char*)g.Bt + (size_t)nxt.pb * tstep : cB;
;         for (int t = 0; t < nt; t += 2) {
;             const bool last = (t == nt - 2);
;             const char* a1 = cA + (size_t)(t + 1) * kstep;
;             const char* a2 = last ? nA : cA + (size_t)(t + 2) * kstep; const char* b2 = last ? nB : cB + (size_t)(t + 2) * kstep;
;     ...
; #pragma unroll
;         for (int a = 0; a < 2; ++a)
; #pragma unroll
;             for (int b = 0; b < 2; ++b)
; #pragma unroll
;                 for (int m = 0; m < 4; ++m)
; #pragma unroll
;                     for (int n = 0; n < 2; ++n) acc[a][b][m][n] = (f32x4){0.f, 0.f, 0.f, 0.f};
;         cur = nxt; cA = nA; cB = nB; ++ui;
.LBB0_411:
	s_ashr_i32 s15, s14, 31
	s_lshl_b64 s[16:17], s[14:15], 20
	s_add_u32 s16, s28, s16
	s_addc_u32 s17, s29, s17
	s_and_b64 s[18:19], s[6:7], exec
	s_cselect_b32 s15, s17, s23
	s_cselect_b32 s48, s16, s22
	s_ashr_i32 s13, s12, 31
	s_lshl_b64 s[18:19], s[12:13], 20
	s_add_u32 s18, s30, s18
	s_addc_u32 s19, s31, s19
	s_and_b64 s[26:27], s[6:7], exec
	s_cselect_b32 s13, s19, s25
	s_cselect_b32 s49, s18, s24
	s_add_u32 s22, s22, 0x80080
	s_addc_u32 s23, s23, 0
	s_add_u32 s56, s24, 0x100
	v_mov_b32_e32 v2, 0
	s_addc_u32 s57, s25, 0
	s_mov_b32 s60, -2
	v_mov_b32_e32 v3, v2
	v_mov_b32_e32 v4, v2
	v_mov_b32_e32 v5, v2
	v_mov_b32_e32 v6, v2
	v_mov_b32_e32 v7, v2
	v_mov_b32_e32 v8, v2
	v_mov_b32_e32 v9, v2
	v_mov_b32_e32 v10, v2
	v_mov_b32_e32 v11, v2
	v_mov_b32_e32 v12, v2
	v_mov_b32_e32 v13, v2
	v_mov_b32_e32 v18, v2
	v_mov_b32_e32 v19, v2
	v_mov_b32_e32 v20, v2
	v_mov_b32_e32 v21, v2
	v_mov_b32_e32 v26, v2
	v_mov_b32_e32 v27, v2
	v_mov_b32_e32 v28, v2
	v_mov_b32_e32 v29, v2
	v_mov_b32_e32 v34, v2
	v_mov_b32_e32 v35, v2
	v_mov_b32_e32 v36, v2
	v_mov_b32_e32 v37, v2
	v_mov_b32_e32 v42, v2
	v_mov_b32_e32 v43, v2
	v_mov_b32_e32 v44, v2
	v_mov_b32_e32 v45, v2
	v_mov_b32_e32 v50, v2
	v_mov_b32_e32 v51, v2
	v_mov_b32_e32 v52, v2
	v_mov_b32_e32 v53, v2
	v_mov_b32_e32 v14, v2
	v_mov_b32_e32 v15, v2
	v_mov_b32_e32 v16, v2
	v_mov_b32_e32 v17, v2
	v_mov_b32_e32 v22, v2
	v_mov_b32_e32 v23, v2
	v_mov_b32_e32 v24, v2
	v_mov_b32_e32 v25, v2
	v_mov_b32_e32 v30, v2
	v_mov_b32_e32 v31, v2
	v_mov_b32_e32 v32, v2
	v_mov_b32_e32 v33, v2
	v_mov_b32_e32 v38, v2
	v_mov_b32_e32 v39, v2
	v_mov_b32_e32 v40, v2
	v_mov_b32_e32 v41, v2
	v_mov_b32_e32 v46, v2
	v_mov_b32_e32 v47, v2
	v_mov_b32_e32 v48, v2
	v_mov_b32_e32 v49, v2
	v_mov_b32_e32 v54, v2
	v_mov_b32_e32 v55, v2
	v_mov_b32_e32 v56, v2
	v_mov_b32_e32 v57, v2
	v_mov_b32_e32 v58, v2
	v_mov_b32_e32 v59, v2
	v_mov_b32_e32 v60, v2
	v_mov_b32_e32 v61, v2
	v_mov_b32_e32 v62, v2
	v_mov_b32_e32 v63, v2
	v_mov_b32_e32 v64, v2
	v_mov_b32_e32 v65, v2
	v_mov_b32_e32 v66, v2
	v_mov_b32_e32 v67, v2
	v_mov_b32_e32 v68, v2
	v_mov_b32_e32 v69, v2
	v_mov_b32_e32 v70, v2
	v_mov_b32_e32 v71, v2
	v_mov_b32_e32 v72, v2
	v_mov_b32_e32 v73, v2
	v_mov_b32_e32 v74, v2
	v_mov_b32_e32 v75, v2
	v_mov_b32_e32 v76, v2
	v_mov_b32_e32 v77, v2
	v_mov_b32_e32 v82, v2
	v_mov_b32_e32 v83, v2
	v_mov_b32_e32 v84, v2
	v_mov_b32_e32 v85, v2
	v_mov_b32_e32 v90, v2
	v_mov_b32_e32 v91, v2
	v_mov_b32_e32 v92, v2
	v_mov_b32_e32 v93, v2
	v_mov_b32_e32 v98, v2
	v_mov_b32_e32 v99, v2
	v_mov_b32_e32 v100, v2
	v_mov_b32_e32 v101, v2
	v_mov_b32_e32 v106, v2
	v_mov_b32_e32 v107, v2
	v_mov_b32_e32 v108, v2
	v_mov_b32_e32 v109, v2
	v_mov_b32_e32 v114, v2
	v_mov_b32_e32 v115, v2
	v_mov_b32_e32 v116, v2
	v_mov_b32_e32 v117, v2
	v_mov_b32_e32 v78, v2
	v_mov_b32_e32 v79, v2
	v_mov_b32_e32 v80, v2
	v_mov_b32_e32 v81, v2
	v_mov_b32_e32 v86, v2
	v_mov_b32_e32 v87, v2
	v_mov_b32_e32 v88, v2
	v_mov_b32_e32 v89, v2
	v_mov_b32_e32 v94, v2
	v_mov_b32_e32 v95, v2
	v_mov_b32_e32 v96, v2
	v_mov_b32_e32 v97, v2
	v_mov_b32_e32 v102, v2
	v_mov_b32_e32 v103, v2
	v_mov_b32_e32 v104, v2
	v_mov_b32_e32 v105, v2
	v_mov_b32_e32 v110, v2
	v_mov_b32_e32 v111, v2
	v_mov_b32_e32 v112, v2
	v_mov_b32_e32 v113, v2
	v_mov_b32_e32 v118, v2
	v_mov_b32_e32 v119, v2
	v_mov_b32_e32 v120, v2
	v_mov_b32_e32 v121, v2
	v_mov_b32_e32 v122, v2
	v_mov_b32_e32 v123, v2
	v_mov_b32_e32 v124, v2
	v_mov_b32_e32 v125, v2
	v_mov_b32_e32 v126, v2
	v_mov_b32_e32 v127, v2
	v_mov_b32_e32 v128, v2
	v_mov_b32_e32 v129, v2
	s_branch .LBB0_412

; #define PG8_STAGE(bufoff, gbase, voff) do { _Pragma("unroll") for (int _i = 0; _i < 2; ++_i) \
;         __builtin_amdgcn_global_load_lds((const unsigned*)((const char*)(gbase) + (voff)[_i]), (PG8_LAS unsigned*)(lds + (bufoff) + ldsw + _i * 8192), 16, 0, 0); } while (0)
; #define PG8_LDA(dst, b, h) do { _Pragma("unroll") for (int m = 0; m < 4; ++m) _Pragma("unroll") for (int k = 0; k < 2; ++k) dst[m][k] = *(const PG8_LAS bf16x8*)(lds + PG8_SA(b, h) + aoff + m * 2048 + k * 1024); } while (0)
; #define PG8_LDB(dst, b, h) do { _Pragma("unroll") for (int n = 0; n < 2; ++n) _Pragma("unroll") for (int k = 0; k < 2; ++k) dst[n][k] = *(const PG8_LAS bf16x8*)(lds + PG8_SB(b, h) + boff + n * 2048 + k * 1024); } while (0)
; #define PG8_WAIT_V(n) asm volatile("s_waitcnt vmcnt(" #n ")" ::: "memory")
; #define PG8_WAIT_L(n) asm volatile("s_waitcnt lgkmcnt(" #n ")" ::: "memory")
; #define PG8_BAR __builtin_amdgcn_s_barrier()
; #define PG8_SCHED __builtin_amdgcn_sched_barrier(0)
; template <class Epi, class Sched, bool ALIGN_EPI = false, bool SP2 = false, bool FP8 = false>
; __device__ __forceinline__ void gemm_phase(PG8_LAS unsigned char* lds, const Gemm g, const Sched& S, const Epi& E) {
;     ...
;             PG8_LDB(B0, 0, 0); PG8_LDB(B1, 0, 1); PG8_SCHED; PG8_LDA(At, 0, 0); PG8_STAGE(PG8_SA(1, 1), a1 + hstep, voffA);
;             PG8_WAIT_V(8); PG8_WAIT_L(0); PG8_BAR; PG8_MMA(0, 0, At, B0); PG8_MMA(0, 1, At, B1); PG8_BAR; PG8_SCHED;
;             PG8_LDA(At, 0, 1); PG8_STAGE(PG8_SB(0, 0), b2, voffB); PG8_STAGE(PG8_SB(0, 1), b2 + hstep, voffB); PG8_STAGE(PG8_SA(0, 0), a2, voffA);
;             PG8_WAIT_V(8); PG8_WAIT_L(0); PG8_BAR; PG8_MMA(1, 0, At, B0); PG8_MMA(1, 1, At, B1); PG8_BAR; PG8_SCHED;
.LBB0_412:
	ds_read_b128 v[146:149], v152
	ds_read_b128 v[156:159], v152 offset:1024
	ds_read_b128 v[160:163], v152 offset:2048
	ds_read_b128 v[164:167], v152 offset:3072
	ds_read_b128 v[168:171], v153
	ds_read_b128 v[172:175], v153 offset:1024
	ds_read_b128 v[176:179], v153 offset:2048
	ds_read_b128 v[180:183], v153 offset:3072
	s_add_u32 s24, s22, 0xfff80080
	s_addc_u32 s25, s23, -1
	s_cmp_eq_u32 s60, 28
	s_cselect_b32 s27, s15, s25
	s_cselect_b32 s26, s48, s24
	s_cselect_b32 s25, s13, s57
	s_cselect_b32 s24, s49, s56
	v_lshl_add_u64 v[216:217], s[22:23], 0, v[138:139]
	s_add_i32 m0, s21, 0xc000
	ds_read_b128 v[184:187], v154
	ds_read_b128 v[188:191], v154 offset:1024
	ds_read_b128 v[192:195], v154 offset:2048
	ds_read_b128 v[196:199], v154 offset:3072
	ds_read_b128 v[200:203], v154 offset:4096
	ds_read_b128 v[204:207], v154 offset:5120
	ds_read_b128 v[208:211], v154 offset:6144
	ds_read_b128 v[212:215], v154 offset:7168
	global_load_lds_dwordx4 v[216:217], off
	v_lshl_add_u64 v[216:217], s[22:23], 0, v[140:141]
	s_add_i32 m0, s21, 0xe000
	s_nop 0
	global_load_lds_dwordx4 v[216:217], off
	s_waitcnt vmcnt(8)
	s_waitcnt lgkmcnt(0)
	s_barrier
	s_setprio 1
	s_waitcnt lgkmcnt(0)
	v_mfma_f32_16x16x32_bf16 v[126:129], v[146:149], v[184:187], v[126:129]
	v_mfma_f32_16x16x32_bf16 v[122:125], v[160:163], v[184:187], v[122:125]
	v_mfma_f32_16x16x32_bf16 v[118:121], v[146:149], v[192:195], v[118:121]
	v_mfma_f32_16x16x32_bf16 v[110:113], v[160:163], v[192:195], v[110:113]
	v_mfma_f32_16x16x32_bf16 v[102:105], v[146:149], v[200:203], v[102:105]
	v_mfma_f32_16x16x32_bf16 v[94:97], v[160:163], v[200:203], v[94:97]
	v_mfma_f32_16x16x32_bf16 v[86:89], v[146:149], v[208:211], v[86:89]
	v_mfma_f32_16x16x32_bf16 v[78:81], v[160:163], v[208:211], v[78:81]
	v_mfma_f32_16x16x32_bf16 v[126:129], v[156:159], v[188:191], v[126:129]
	v_mfma_f32_16x16x32_bf16 v[122:125], v[164:167], v[188:191], v[122:125]
	v_mfma_f32_16x16x32_bf16 v[118:121], v[156:159], v[196:199], v[118:121]
	v_mfma_f32_16x16x32_bf16 v[110:113], v[164:167], v[196:199], v[110:113]
	v_mfma_f32_16x16x32_bf16 v[102:105], v[156:159], v[204:207], v[102:105]
	v_mfma_f32_16x16x32_bf16 v[94:97], v[164:167], v[204:207], v[94:97]
	v_mfma_f32_16x16x32_bf16 v[86:89], v[156:159], v[212:215], v[86:89]
	v_mfma_f32_16x16x32_bf16 v[78:81], v[164:167], v[212:215], v[78:81]
	s_setprio 0
	s_setprio 1
	v_mfma_f32_16x16x32_bf16 v[114:117], v[168:171], v[184:187], v[114:117]
	v_mfma_f32_16x16x32_bf16 v[106:109], v[176:179], v[184:187], v[106:109]
	v_mfma_f32_16x16x32_bf16 v[98:101], v[168:171], v[192:195], v[98:101]
	v_mfma_f32_16x16x32_bf16 v[90:93], v[176:179], v[192:195], v[90:93]
	v_mfma_f32_16x16x32_bf16 v[82:85], v[168:171], v[200:203], v[82:85]
	v_mfma_f32_16x16x32_bf16 v[74:77], v[176:179], v[200:203], v[74:77]
	v_mfma_f32_16x16x32_bf16 v[70:73], v[168:171], v[208:211], v[70:73]
	v_mfma_f32_16x16x32_bf16 v[66:69], v[176:179], v[208:211], v[66:69]
	v_mfma_f32_16x16x32_bf16 v[114:117], v[172:175], v[188:191], v[114:117]
	v_mfma_f32_16x16x32_bf16 v[106:109], v[180:183], v[188:191], v[106:109]
	v_mfma_f32_16x16x32_bf16 v[98:101], v[172:175], v[196:199], v[98:101]
	v_mfma_f32_16x16x32_bf16 v[90:93], v[180:183], v[196:199], v[90:93]
	v_mfma_f32_16x16x32_bf16 v[82:85], v[172:175], v[204:207], v[82:85]
	v_mfma_f32_16x16x32_bf16 v[74:77], v[180:183], v[204:207], v[74:77]
	v_mfma_f32_16x16x32_bf16 v[70:73], v[172:175], v[212:215], v[70:73]
	v_mfma_f32_16x16x32_bf16 v[66:69], v[180:183], v[212:215], v[66:69]
	s_setprio 0
	s_barrier
	s_add_i32 s61, s44, s33
	v_lshl_add_u64 v[216:217], s[24:25], 0, v[134:135]
	s_mov_b32 m0, s61
	ds_read_b128 v[184:187], v154 offset:16384
	ds_read_b128 v[188:191], v154 offset:17408
	ds_read_b128 v[192:195], v154 offset:18432
	ds_read_b128 v[196:199], v154 offset:19456
	ds_read_b128 v[200:203], v154 offset:20480
	ds_read_b128 v[204:207], v154 offset:21504
	ds_read_b128 v[208:211], v154 offset:22528
	ds_read_b128 v[212:215], v154 offset:23552
	global_load_lds_dwordx4 v[216:217], off
	s_add_i32 m0, s61, 0x2000
	s_add_u32 s62, s24, 0x80000
	v_lshl_add_u64 v[218:219], s[24:25], 0, v[130:131]
	s_addc_u32 s63, s25, 0
	s_add_i32 s61, s45, s33
	global_load_lds_dwordx4 v[218:219], off
	v_lshl_add_u64 v[220:221], s[62:63], 0, v[134:135]
	s_mov_b32 m0, s61
	v_lshl_add_u64 v[222:223], s[26:27], 0, v[132:133]
	global_load_lds_dwordx4 v[220:221], off
	v_lshl_add_u64 v[220:221], s[62:63], 0, v[130:131]
	s_add_i32 m0, s61, 0x2000
	s_nop 0
	global_load_lds_dwordx4 v[220:221], off
	v_lshl_add_u64 v[220:221], s[26:27], 0, v[136:137]
	s_mov_b32 m0, s21
	s_nop 0
	global_load_lds_dwordx4 v[220:221], off
	s_mov_b32 m0, s36
	s_nop 0
	global_load_lds_dwordx4 v[222:223], off
	s_waitcnt vmcnt(8)
	s_waitcnt lgkmcnt(0)
	s_barrier
; #define PG8_STAGE(bufoff, gbase, voff) do { _Pragma("unroll") for (int _i = 0; _i < 2; ++_i) \
;         __builtin_amdgcn_global_load_lds((const unsigned*)((const char*)(gbase) + (voff)[_i]), (PG8_LAS unsigned*)(lds + (bufoff) + ldsw + _i * 8192), 16, 0, 0); } while (0)
; #define PG8_LDA(dst, b, h) do { _Pragma("unroll") for (int m = 0; m < 4; ++m) _Pragma("unroll") for (int k = 0; k < 2; ++k) dst[m][k] = *(const PG8_LAS bf16x8*)(lds + PG8_SA(b, h) + aoff + m * 2048 + k * 1024); } while (0)
; #define PG8_LDB(dst, b, h) do { _Pragma("unroll") for (int n = 0; n < 2; ++n) _Pragma("unroll") for (int k = 0; k < 2; ++k) dst[n][k] = *(const PG8_LAS bf16x8*)(lds + PG8_SB(b, h) + boff + n * 2048 + k * 1024); } while (0)
; #define PG8_WAIT_V(n) asm volatile("s_waitcnt vmcnt(" #n ")" ::: "memory")
; #define PG8_WAIT_L(n) asm volatile("s_waitcnt lgkmcnt(" #n ")" ::: "memory")
; #define PG8_BAR __builtin_amdgcn_s_barrier()
; #define PG8_SCHED __builtin_amdgcn_sched_barrier(0)
; template <class Epi, class Sched, bool ALIGN_EPI = false, bool SP2 = false, bool FP8 = false>
; __device__ __forceinline__ void gemm_phase(PG8_LAS unsigned char* lds, const Gemm g, const Sched& S, const Epi& E) {
;     ...
;             PG8_WAIT_V(8); PG8_WAIT_L(0); PG8_BAR; PG8_MMA(1, 0, At, B0); PG8_MMA(1, 1, At, B1); PG8_BAR; PG8_SCHED;
;             PG8_LDB(B0, 1, 0); PG8_LDB(B1, 1, 1); PG8_SCHED; PG8_LDA(At, 1, 0); PG8_STAGE(PG8_SA(0, 1), a2 + hstep, voffA);
;             PG8_WAIT_V(8); PG8_WAIT_L(0); PG8_BAR; PG8_MMA(0, 0, At, B0); PG8_MMA(0, 1, At, B1); PG8_BAR; PG8_SCHED;
	s_setprio 1
	s_waitcnt lgkmcnt(0)
	v_mfma_f32_16x16x32_bf16 v[62:65], v[146:149], v[184:187], v[62:65]
	v_mfma_f32_16x16x32_bf16 v[58:61], v[160:163], v[184:187], v[58:61]
	v_mfma_f32_16x16x32_bf16 v[54:57], v[146:149], v[192:195], v[54:57]
	v_mfma_f32_16x16x32_bf16 v[46:49], v[160:163], v[192:195], v[46:49]
	v_mfma_f32_16x16x32_bf16 v[38:41], v[146:149], v[200:203], v[38:41]
	v_mfma_f32_16x16x32_bf16 v[30:33], v[160:163], v[200:203], v[30:33]
	v_mfma_f32_16x16x32_bf16 v[22:25], v[146:149], v[208:211], v[22:25]
	v_mfma_f32_16x16x32_bf16 v[14:17], v[160:163], v[208:211], v[14:17]
	v_mfma_f32_16x16x32_bf16 v[62:65], v[156:159], v[188:191], v[62:65]
	v_mfma_f32_16x16x32_bf16 v[58:61], v[164:167], v[188:191], v[58:61]
	v_mfma_f32_16x16x32_bf16 v[54:57], v[156:159], v[196:199], v[54:57]
	v_mfma_f32_16x16x32_bf16 v[46:49], v[164:167], v[196:199], v[46:49]
	v_mfma_f32_16x16x32_bf16 v[38:41], v[156:159], v[204:207], v[38:41]
	v_mfma_f32_16x16x32_bf16 v[30:33], v[164:167], v[204:207], v[30:33]
	v_mfma_f32_16x16x32_bf16 v[22:25], v[156:159], v[212:215], v[22:25]
	v_mfma_f32_16x16x32_bf16 v[14:17], v[164:167], v[212:215], v[14:17]
	s_setprio 0
	s_setprio 1
	v_mfma_f32_16x16x32_bf16 v[50:53], v[168:171], v[184:187], v[50:53]
	v_mfma_f32_16x16x32_bf16 v[42:45], v[176:179], v[184:187], v[42:45]
	v_mfma_f32_16x16x32_bf16 v[34:37], v[168:171], v[192:195], v[34:37]
	v_mfma_f32_16x16x32_bf16 v[26:29], v[176:179], v[192:195], v[26:29]
	v_mfma_f32_16x16x32_bf16 v[18:21], v[168:171], v[200:203], v[18:21]
	v_mfma_f32_16x16x32_bf16 v[10:13], v[176:179], v[200:203], v[10:13]
	v_mfma_f32_16x16x32_bf16 v[6:9], v[168:171], v[208:211], v[6:9]
	v_mfma_f32_16x16x32_bf16 v[2:5], v[176:179], v[208:211], v[2:5]
	v_mfma_f32_16x16x32_bf16 v[50:53], v[172:175], v[188:191], v[50:53]
	v_mfma_f32_16x16x32_bf16 v[42:45], v[180:183], v[188:191], v[42:45]
	v_mfma_f32_16x16x32_bf16 v[34:37], v[172:175], v[196:199], v[34:37]
	v_mfma_f32_16x16x32_bf16 v[26:29], v[180:183], v[196:199], v[26:29]
	v_mfma_f32_16x16x32_bf16 v[18:21], v[172:175], v[204:207], v[18:21]
	v_mfma_f32_16x16x32_bf16 v[10:13], v[180:183], v[204:207], v[10:13]
	v_mfma_f32_16x16x32_bf16 v[6:9], v[172:175], v[212:215], v[6:9]
	v_mfma_f32_16x16x32_bf16 v[2:5], v[180:183], v[212:215], v[2:5]
	s_setprio 0
	s_barrier
	s_add_i32 s61, 0, 0x18000
	v_add_u32_e32 v155, s61, v150
	s_add_i32 s62, 0, 0x1c000
	ds_read_b128 v[146:149], v155
	ds_read_b128 v[156:159], v155 offset:1024
	ds_read_b128 v[160:163], v155 offset:2048
	ds_read_b128 v[164:167], v155 offset:3072
	v_add_u32_e32 v155, s62, v150
	ds_read_b128 v[168:171], v155
	ds_read_b128 v[172:175], v155 offset:1024
	ds_read_b128 v[176:179], v155 offset:2048
	ds_read_b128 v[180:183], v155 offset:3072
	s_add_u32 s26, s26, 0x80000
	s_addc_u32 s27, s27, 0
	s_mov_b32 m0, s37
	v_lshl_add_u64 v[224:225], s[26:27], 0, v[136:137]
	ds_read_b128 v[184:187], v154 offset:32768
	ds_read_b128 v[188:191], v154 offset:33792
	ds_read_b128 v[192:195], v154 offset:34816
	ds_read_b128 v[196:199], v154 offset:35840
	ds_read_b128 v[200:203], v154 offset:36864
	ds_read_b128 v[204:207], v154 offset:37888
	ds_read_b128 v[208:211], v154 offset:38912
	ds_read_b128 v[212:215], v154 offset:39936
	global_load_lds_dwordx4 v[224:225], off
	v_lshl_add_u64 v[224:225], s[26:27], 0, v[132:133]
	s_mov_b32 m0, s38
	s_nop 0
	global_load_lds_dwordx4 v[224:225], off
	s_waitcnt vmcnt(8)
	s_waitcnt lgkmcnt(0)
	s_barrier
	s_setprio 1
	s_waitcnt lgkmcnt(0)
	v_mfma_f32_16x16x32_bf16 v[126:129], v[146:149], v[184:187], v[126:129]
	v_mfma_f32_16x16x32_bf16 v[122:125], v[160:163], v[184:187], v[122:125]
	v_mfma_f32_16x16x32_bf16 v[118:121], v[146:149], v[192:195], v[118:121]
	v_mfma_f32_16x16x32_bf16 v[110:113], v[160:163], v[192:195], v[110:113]
	v_mfma_f32_16x16x32_bf16 v[102:105], v[146:149], v[200:203], v[102:105]
	v_mfma_f32_16x16x32_bf16 v[94:97], v[160:163], v[200:203], v[94:97]
	v_mfma_f32_16x16x32_bf16 v[86:89], v[146:149], v[208:211], v[86:89]
	v_mfma_f32_16x16x32_bf16 v[78:81], v[160:163], v[208:211], v[78:81]
	v_mfma_f32_16x16x32_bf16 v[126:129], v[156:159], v[188:191], v[126:129]
	v_mfma_f32_16x16x32_bf16 v[122:125], v[164:167], v[188:191], v[122:125]
	v_mfma_f32_16x16x32_bf16 v[118:121], v[156:159], v[196:199], v[118:121]
	v_mfma_f32_16x16x32_bf16 v[110:113], v[164:167], v[196:199], v[110:113]
	v_mfma_f32_16x16x32_bf16 v[102:105], v[156:159], v[204:207], v[102:105]
	v_mfma_f32_16x16x32_bf16 v[94:97], v[164:167], v[204:207], v[94:97]
	v_mfma_f32_16x16x32_bf16 v[86:89], v[156:159], v[212:215], v[86:89]
	v_mfma_f32_16x16x32_bf16 v[78:81], v[164:167], v[212:215], v[78:81]
	s_setprio 0
	s_setprio 1
	v_mfma_f32_16x16x32_bf16 v[114:117], v[168:171], v[184:187], v[114:117]
	v_mfma_f32_16x16x32_bf16 v[106:109], v[176:179], v[184:187], v[106:109]
	v_mfma_f32_16x16x32_bf16 v[98:101], v[168:171], v[192:195], v[98:101]
	v_mfma_f32_16x16x32_bf16 v[90:93], v[176:179], v[192:195], v[90:93]
	v_mfma_f32_16x16x32_bf16 v[82:85], v[168:171], v[200:203], v[82:85]
	v_mfma_f32_16x16x32_bf16 v[74:77], v[176:179], v[200:203], v[74:77]
	v_mfma_f32_16x16x32_bf16 v[70:73], v[168:171], v[208:211], v[70:73]
	v_mfma_f32_16x16x32_bf16 v[66:69], v[176:179], v[208:211], v[66:69]
	v_mfma_f32_16x16x32_bf16 v[114:117], v[172:175], v[188:191], v[114:117]
	v_mfma_f32_16x16x32_bf16 v[106:109], v[180:183], v[188:191], v[106:109]
	v_mfma_f32_16x16x32_bf16 v[98:101], v[172:175], v[196:199], v[98:101]
	v_mfma_f32_16x16x32_bf16 v[90:93], v[180:183], v[196:199], v[90:93]
	v_mfma_f32_16x16x32_bf16 v[82:85], v[172:175], v[204:207], v[82:85]
	v_mfma_f32_16x16x32_bf16 v[74:77], v[180:183], v[204:207], v[74:77]
	v_mfma_f32_16x16x32_bf16 v[70:73], v[172:175], v[212:215], v[70:73]
	v_mfma_f32_16x16x32_bf16 v[66:69], v[180:183], v[212:215], v[66:69]
	s_setprio 0
	s_barrier
; #define PG8_STAGE(bufoff, gbase, voff) do { _Pragma("unroll") for (int _i = 0; _i < 2; ++_i) \
;         __builtin_amdgcn_global_load_lds((const unsigned*)((const char*)(gbase) + (voff)[_i]), (PG8_LAS unsigned*)(lds + (bufoff) + ldsw + _i * 8192), 16, 0, 0); } while (0)
; #define PG8_LDA(dst, b, h) do { _Pragma("unroll") for (int m = 0; m < 4; ++m) _Pragma("unroll") for (int k = 0; k < 2; ++k) dst[m][k] = *(const PG8_LAS bf16x8*)(lds + PG8_SA(b, h) + aoff + m * 2048 + k * 1024); } while (0)
; #define PG8_WAIT_V(n) asm volatile("s_waitcnt vmcnt(" #n ")" ::: "memory")
; #define PG8_WAIT_L(n) asm volatile("s_waitcnt lgkmcnt(" #n ")" ::: "memory")
; #define PG8_BAR __builtin_amdgcn_s_barrier()
; #define PG8_SCHED __builtin_amdgcn_sched_barrier(0)
; template <class Epi, class Sched, bool ALIGN_EPI = false, bool SP2 = false, bool FP8 = false>
; __device__ __forceinline__ void gemm_phase(PG8_LAS unsigned char* lds, const Gemm g, const Sched& S, const Epi& E) {
;     ...
;         for (int t = 0; t < nt; t += 2) {
;             const bool last = (t == nt - 2);
;             const char* a1 = cA + (size_t)(t + 1) * kstep;
;             const char* a2 = last ? nA : cA + (size_t)(t + 2) * kstep; const char* b2 = last ? nB : cB + (size_t)(t + 2) * kstep;
;     ...
;             PG8_LDA(At, 1, 1); PG8_STAGE(PG8_SB(1, 0), b3, voffB); PG8_STAGE(PG8_SB(1, 1), b3 + hstep, voffB); PG8_STAGE(PG8_SA(1, 0), a3, voffA);
;             PG8_WAIT_V(8); PG8_WAIT_L(0); PG8_BAR; PG8_MMA(1, 0, At, B0); PG8_MMA(1, 1, At, B1); PG8_BAR; PG8_SCHED;
	s_add_i32 s26, s61, s33
	v_lshl_add_u64 v[216:217], v[216:217], 0, s[8:9]
	s_mov_b32 m0, s26
	ds_read_b128 v[184:187], v154 offset:49152
	ds_read_b128 v[188:191], v154 offset:50176
	ds_read_b128 v[192:195], v154 offset:51200
	ds_read_b128 v[196:199], v154 offset:52224
	ds_read_b128 v[200:203], v154 offset:53248
	ds_read_b128 v[204:207], v154 offset:54272
	ds_read_b128 v[208:211], v154 offset:55296
	ds_read_b128 v[212:215], v154 offset:56320
	global_load_lds_dwordx4 v[216:217], off
	s_add_i32 m0, s26, 0x2000
	s_add_u32 s24, s24, 0x80080
	v_lshl_add_u64 v[216:217], v[218:219], 0, s[8:9]
	s_addc_u32 s25, s25, 0
	s_add_i32 s26, s62, s33
	global_load_lds_dwordx4 v[216:217], off
	v_lshl_add_u64 v[216:217], s[24:25], 0, v[134:135]
	s_mov_b32 m0, s26
	s_nop 0
	global_load_lds_dwordx4 v[216:217], off
	v_lshl_add_u64 v[216:217], s[24:25], 0, v[130:131]
	s_add_i32 m0, s26, 0x2000
	s_nop 0
	global_load_lds_dwordx4 v[216:217], off
	v_lshl_add_u64 v[216:217], v[220:221], 0, s[8:9]
	s_mov_b32 m0, s41
	s_nop 0
	global_load_lds_dwordx4 v[216:217], off
	v_lshl_add_u64 v[216:217], v[222:223], 0, s[8:9]
	s_mov_b32 m0, s42
	s_nop 0
	global_load_lds_dwordx4 v[216:217], off
	s_waitcnt vmcnt(8)
	s_waitcnt lgkmcnt(0)
	s_barrier
	s_setprio 1
	s_waitcnt lgkmcnt(0)
	v_mfma_f32_16x16x32_bf16 v[62:65], v[146:149], v[184:187], v[62:65]
	v_mfma_f32_16x16x32_bf16 v[58:61], v[160:163], v[184:187], v[58:61]
	v_mfma_f32_16x16x32_bf16 v[54:57], v[146:149], v[192:195], v[54:57]
	v_mfma_f32_16x16x32_bf16 v[46:49], v[160:163], v[192:195], v[46:49]
	v_mfma_f32_16x16x32_bf16 v[38:41], v[146:149], v[200:203], v[38:41]
	v_mfma_f32_16x16x32_bf16 v[30:33], v[160:163], v[200:203], v[30:33]
	v_mfma_f32_16x16x32_bf16 v[22:25], v[146:149], v[208:211], v[22:25]
	v_mfma_f32_16x16x32_bf16 v[14:17], v[160:163], v[208:211], v[14:17]
	v_mfma_f32_16x16x32_bf16 v[62:65], v[156:159], v[188:191], v[62:65]
	v_mfma_f32_16x16x32_bf16 v[58:61], v[164:167], v[188:191], v[58:61]
	v_mfma_f32_16x16x32_bf16 v[54:57], v[156:159], v[196:199], v[54:57]
	v_mfma_f32_16x16x32_bf16 v[46:49], v[164:167], v[196:199], v[46:49]
	v_mfma_f32_16x16x32_bf16 v[38:41], v[156:159], v[204:207], v[38:41]
	v_mfma_f32_16x16x32_bf16 v[30:33], v[164:167], v[204:207], v[30:33]
	v_mfma_f32_16x16x32_bf16 v[22:25], v[156:159], v[212:215], v[22:25]
	v_mfma_f32_16x16x32_bf16 v[14:17], v[164:167], v[212:215], v[14:17]
	s_setprio 0
	s_setprio 1
	v_mfma_f32_16x16x32_bf16 v[50:53], v[168:171], v[184:187], v[50:53]
	v_mfma_f32_16x16x32_bf16 v[42:45], v[176:179], v[184:187], v[42:45]
	v_mfma_f32_16x16x32_bf16 v[34:37], v[168:171], v[192:195], v[34:37]
	v_mfma_f32_16x16x32_bf16 v[26:29], v[176:179], v[192:195], v[26:29]
	v_mfma_f32_16x16x32_bf16 v[18:21], v[168:171], v[200:203], v[18:21]
	v_mfma_f32_16x16x32_bf16 v[10:13], v[176:179], v[200:203], v[10:13]
	v_mfma_f32_16x16x32_bf16 v[6:9], v[168:171], v[208:211], v[6:9]
	v_mfma_f32_16x16x32_bf16 v[2:5], v[176:179], v[208:211], v[2:5]
	v_mfma_f32_16x16x32_bf16 v[50:53], v[172:175], v[188:191], v[50:53]
	v_mfma_f32_16x16x32_bf16 v[42:45], v[180:183], v[188:191], v[42:45]
	v_mfma_f32_16x16x32_bf16 v[34:37], v[172:175], v[196:199], v[34:37]
	v_mfma_f32_16x16x32_bf16 v[26:29], v[180:183], v[196:199], v[26:29]
	v_mfma_f32_16x16x32_bf16 v[18:21], v[172:175], v[204:207], v[18:21]
	v_mfma_f32_16x16x32_bf16 v[10:13], v[180:183], v[204:207], v[10:13]
	v_mfma_f32_16x16x32_bf16 v[6:9], v[172:175], v[212:215], v[6:9]
	v_mfma_f32_16x16x32_bf16 v[2:5], v[180:183], v[212:215], v[2:5]
	s_setprio 0
	s_add_i32 s60, s60, 2
	s_add_u32 s22, s22, 0x100
	s_addc_u32 s23, s23, 0
	s_add_u32 s56, s56, 0x100
	s_addc_u32 s57, s57, 0
	s_cmp_gt_u32 s60, 29
	s_cbranch_scc0 .Lrot_head_412
	s_barrier
	s_and_b64 vcc, exec, s[10:11]
	s_cbranch_vccz .LBB0_415
	s_barrier

; template <class Epi, class Sched, bool ALIGN_EPI = false, bool SP2 = false, bool FP8 = false>
; __device__ __forceinline__ void gemm_phase(PG8_LAS unsigned char* lds, const Gemm g, const Sched& S, const Epi& E) {
;     ...
;     for (;;) {
;         const bool has_next = S.next(ui + 1, nxt);
;         const char* nA = has_next ? (const char*)g.A + (size_t)nxt.pm * tstep : cA; const char* nB = has_next ? (const char*)g.Bt + (size_t)nxt.pb * tstep : cB;
;         for (int t = 0; t < nt; t += 2) {
;             const bool last = (t == nt - 2);
;             const char* a1 = cA + (size_t)(t + 1) * kstep;
;             const char* a2 = last ? nA : cA + (size_t)(t + 2) * kstep; const char* b2 = last ? nB : cB + (size_t)(t + 2) * kstep;
;     ...
; #pragma unroll
;         for (int a = 0; a < 2; ++a)
; #pragma unroll
;             for (int b = 0; b < 2; ++b)
; #pragma unroll
;                 for (int m = 0; m < 4; ++m)
; #pragma unroll
;                     for (int n = 0; n < 2; ++n) acc[a][b][m][n] = (f32x4){0.f, 0.f, 0.f, 0.f};
;         cur = nxt; cA = nA; cB = nB; ++ui;
.LBB0_1005:
	s_ashr_i32 s15, s14, 31
	s_lshl_b64 s[16:17], s[14:15], 20
	s_add_u32 s16, s28, s16
	s_addc_u32 s17, s29, s17
	s_and_b64 s[18:19], s[6:7], exec
	s_cselect_b32 s15, s17, s23
	s_cselect_b32 s49, s16, s22
	s_ashr_i32 s13, s12, 31
	s_lshl_b64 s[18:19], s[12:13], 20
	s_add_u32 s18, s30, s18
	s_addc_u32 s19, s31, s19
	s_and_b64 s[26:27], s[6:7], exec
	s_cselect_b32 s13, s19, s25
	s_cselect_b32 s56, s18, s24
	s_add_u32 s22, s22, 0x80080
	s_addc_u32 s23, s23, 0
	s_add_u32 s57, s24, 0x100
	v_mov_b32_e32 v2, 0
	s_addc_u32 s60, s25, 0
	s_mov_b32 s61, -2
	v_mov_b32_e32 v3, v2
	v_mov_b32_e32 v4, v2
	v_mov_b32_e32 v5, v2
	v_mov_b32_e32 v6, v2
	v_mov_b32_e32 v7, v2
	v_mov_b32_e32 v8, v2
	v_mov_b32_e32 v9, v2
	v_mov_b32_e32 v18, v2
	v_mov_b32_e32 v19, v2
	v_mov_b32_e32 v20, v2
	v_mov_b32_e32 v21, v2
	v_mov_b32_e32 v22, v2
	v_mov_b32_e32 v23, v2
	v_mov_b32_e32 v24, v2
	v_mov_b32_e32 v25, v2
	v_mov_b32_e32 v34, v2
	v_mov_b32_e32 v35, v2
	v_mov_b32_e32 v36, v2
	v_mov_b32_e32 v37, v2
	v_mov_b32_e32 v38, v2
	v_mov_b32_e32 v39, v2
	v_mov_b32_e32 v40, v2
	v_mov_b32_e32 v41, v2
	v_mov_b32_e32 v50, v2
	v_mov_b32_e32 v51, v2
	v_mov_b32_e32 v52, v2
	v_mov_b32_e32 v53, v2
	v_mov_b32_e32 v54, v2
	v_mov_b32_e32 v55, v2
	v_mov_b32_e32 v56, v2
	v_mov_b32_e32 v57, v2
	v_mov_b32_e32 v10, v2
	v_mov_b32_e32 v11, v2
	v_mov_b32_e32 v12, v2
	v_mov_b32_e32 v13, v2
	v_mov_b32_e32 v14, v2
	v_mov_b32_e32 v15, v2
	v_mov_b32_e32 v16, v2
	v_mov_b32_e32 v17, v2
	v_mov_b32_e32 v26, v2
	v_mov_b32_e32 v27, v2
	v_mov_b32_e32 v28, v2
	v_mov_b32_e32 v29, v2
	v_mov_b32_e32 v30, v2
	v_mov_b32_e32 v31, v2
	v_mov_b32_e32 v32, v2
	v_mov_b32_e32 v33, v2
	v_mov_b32_e32 v42, v2
	v_mov_b32_e32 v43, v2
	v_mov_b32_e32 v44, v2
	v_mov_b32_e32 v45, v2
	v_mov_b32_e32 v46, v2
	v_mov_b32_e32 v47, v2
	v_mov_b32_e32 v48, v2
	v_mov_b32_e32 v49, v2
	v_mov_b32_e32 v58, v2
	v_mov_b32_e32 v59, v2
	v_mov_b32_e32 v60, v2
	v_mov_b32_e32 v61, v2
	v_mov_b32_e32 v62, v2
	v_mov_b32_e32 v63, v2
	v_mov_b32_e32 v64, v2
	v_mov_b32_e32 v65, v2
	v_mov_b32_e32 v66, v2
	v_mov_b32_e32 v67, v2
	v_mov_b32_e32 v68, v2
	v_mov_b32_e32 v69, v2
	v_mov_b32_e32 v70, v2
	v_mov_b32_e32 v71, v2
	v_mov_b32_e32 v72, v2
	v_mov_b32_e32 v73, v2
	v_mov_b32_e32 v82, v2
	v_mov_b32_e32 v83, v2
	v_mov_b32_e32 v84, v2
	v_mov_b32_e32 v85, v2
	v_mov_b32_e32 v86, v2
	v_mov_b32_e32 v87, v2
	v_mov_b32_e32 v88, v2
	v_mov_b32_e32 v89, v2
	v_mov_b32_e32 v98, v2
	v_mov_b32_e32 v99, v2
	v_mov_b32_e32 v100, v2
	v_mov_b32_e32 v101, v2
	v_mov_b32_e32 v102, v2
	v_mov_b32_e32 v103, v2
	v_mov_b32_e32 v104, v2
	v_mov_b32_e32 v105, v2
	v_mov_b32_e32 v114, v2
	v_mov_b32_e32 v115, v2
	v_mov_b32_e32 v116, v2
	v_mov_b32_e32 v117, v2
	v_mov_b32_e32 v118, v2
	v_mov_b32_e32 v119, v2
	v_mov_b32_e32 v120, v2
	v_mov_b32_e32 v121, v2
	v_mov_b32_e32 v74, v2
	v_mov_b32_e32 v75, v2
	v_mov_b32_e32 v76, v2
	v_mov_b32_e32 v77, v2
	v_mov_b32_e32 v78, v2
	v_mov_b32_e32 v79, v2
	v_mov_b32_e32 v80, v2
	v_mov_b32_e32 v81, v2
	v_mov_b32_e32 v90, v2
	v_mov_b32_e32 v91, v2
	v_mov_b32_e32 v92, v2
	v_mov_b32_e32 v93, v2
	v_mov_b32_e32 v94, v2
	v_mov_b32_e32 v95, v2
	v_mov_b32_e32 v96, v2
	v_mov_b32_e32 v97, v2
	v_mov_b32_e32 v106, v2
	v_mov_b32_e32 v107, v2
	v_mov_b32_e32 v108, v2
	v_mov_b32_e32 v109, v2
	v_mov_b32_e32 v110, v2
	v_mov_b32_e32 v111, v2
	v_mov_b32_e32 v112, v2
	v_mov_b32_e32 v113, v2
	v_mov_b32_e32 v122, v2
	v_mov_b32_e32 v123, v2
	v_mov_b32_e32 v124, v2
	v_mov_b32_e32 v125, v2
	v_mov_b32_e32 v126, v2
	v_mov_b32_e32 v127, v2
	v_mov_b32_e32 v128, v2
	v_mov_b32_e32 v129, v2
	s_branch .LBB0_1006

; #define PG8_STAGE(bufoff, gbase, voff) do { _Pragma("unroll") for (int _i = 0; _i < 2; ++_i) \
;         __builtin_amdgcn_global_load_lds((const unsigned*)((const char*)(gbase) + (voff)[_i]), (PG8_LAS unsigned*)(lds + (bufoff) + ldsw + _i * 8192), 16, 0, 0); } while (0)
; #define PG8_LDA(dst, b, h) do { _Pragma("unroll") for (int m = 0; m < 4; ++m) _Pragma("unroll") for (int k = 0; k < 2; ++k) dst[m][k] = *(const PG8_LAS bf16x8*)(lds + PG8_SA(b, h) + aoff + m * 2048 + k * 1024); } while (0)
; #define PG8_LDB(dst, b, h) do { _Pragma("unroll") for (int n = 0; n < 2; ++n) _Pragma("unroll") for (int k = 0; k < 2; ++k) dst[n][k] = *(const PG8_LAS bf16x8*)(lds + PG8_SB(b, h) + boff + n * 2048 + k * 1024); } while (0)
; #define PG8_WAIT_V(n) asm volatile("s_waitcnt vmcnt(" #n ")" ::: "memory")
; #define PG8_WAIT_L(n) asm volatile("s_waitcnt lgkmcnt(" #n ")" ::: "memory")
; #define PG8_BAR __builtin_amdgcn_s_barrier()
; #define PG8_SCHED __builtin_amdgcn_sched_barrier(0)
; template <class Epi, class Sched, bool ALIGN_EPI = false, bool SP2 = false, bool FP8 = false>
; __device__ __forceinline__ void gemm_phase(PG8_LAS unsigned char* lds, const Gemm g, const Sched& S, const Epi& E) {
;     ...
;             const bool last = (t == nt - 2);
;             const char* a1 = cA + (size_t)(t + 1) * kstep;
;             const char* a2 = last ? nA : cA + (size_t)(t + 2) * kstep; const char* b2 = last ? nB : cB + (size_t)(t + 2) * kstep;
;             const char* a3 = a2 + kstep; const char* b3 = b2 + kstep;
;             if (last && has_next) S.a_ready(nxt);
;             if constexpr (SP2) {
;             PG8_LDB(B0, 0, 0); PG8_LDB(B1, 0, 1); PG8_SCHED; PG8_LDA(At, 0, 0); PG8_STAGE(PG8_SA(1, 1), a1 + hstep, voffA);
;             PG8_WAIT_V(8); PG8_WAIT_L(0); PG8_BAR; PG8_MMA(0, 0, At, B0); PG8_MMA(0, 1, At, B1); PG8_BAR; PG8_SCHED;
;             PG8_LDA(At, 0, 1); PG8_STAGE(PG8_SB(0, 0), b2, voffB); PG8_STAGE(PG8_SB(0, 1), b2 + hstep, voffB); PG8_STAGE(PG8_SA(0, 0), a2, voffA);
.LBB0_1006:
	ds_read_b128 v[130:133], v194
	ds_read_b128 v[134:137], v194 offset:1024
	ds_read_b128 v[138:141], v194 offset:2048
	ds_read_b128 v[142:145], v194 offset:3072
	ds_read_b128 v[146:149], v195
	ds_read_b128 v[150:153], v195 offset:1024
	ds_read_b128 v[170:173], v195 offset:2048
	ds_read_b128 v[174:177], v195 offset:3072
	s_add_u32 s24, s22, 0xfff80080
	s_addc_u32 s25, s23, -1
	s_cmp_eq_u32 s61, 28
	s_cselect_b32 s27, s15, s25
	s_cselect_b32 s26, s49, s24
	s_cselect_b32 s25, s13, s60
	s_cselect_b32 s24, s56, s57
	v_lshl_add_u64 v[190:191], s[22:23], 0, v[162:163]
	s_add_i32 m0, s21, 0xc000
	ds_read_b128 v[178:181], v196
	ds_read_b128 v[182:185], v196 offset:1024
	ds_read_b128 v[186:189], v196 offset:2048
	ds_read_b128 v[198:201], v196 offset:3072
	ds_read_b128 v[202:205], v196 offset:4096
	ds_read_b128 v[206:209], v196 offset:5120
	ds_read_b128 v[210:213], v196 offset:6144
	ds_read_b128 v[214:217], v196 offset:7168
	global_load_lds_dwordx4 v[190:191], off
	v_lshl_add_u64 v[190:191], s[22:23], 0, v[164:165]
	s_add_i32 m0, s21, 0xe000
	s_nop 0
	global_load_lds_dwordx4 v[190:191], off
	s_waitcnt vmcnt(8)
	s_waitcnt lgkmcnt(0)
	s_barrier
	s_setprio 1
	s_waitcnt lgkmcnt(0)
	v_mfma_f32_16x16x32_bf16 v[126:129], v[130:133], v[178:181], v[126:129]
	v_mfma_f32_16x16x32_bf16 v[122:125], v[138:141], v[178:181], v[122:125]
	v_mfma_f32_16x16x32_bf16 v[110:113], v[130:133], v[186:189], v[110:113]
	v_mfma_f32_16x16x32_bf16 v[106:109], v[138:141], v[186:189], v[106:109]
	v_mfma_f32_16x16x32_bf16 v[94:97], v[130:133], v[202:205], v[94:97]
	v_mfma_f32_16x16x32_bf16 v[90:93], v[138:141], v[202:205], v[90:93]
	v_mfma_f32_16x16x32_bf16 v[78:81], v[130:133], v[210:213], v[78:81]
	v_mfma_f32_16x16x32_bf16 v[74:77], v[138:141], v[210:213], v[74:77]
	v_mfma_f32_16x16x32_bf16 v[126:129], v[134:137], v[182:185], v[126:129]
	v_mfma_f32_16x16x32_bf16 v[122:125], v[142:145], v[182:185], v[122:125]
	v_mfma_f32_16x16x32_bf16 v[110:113], v[134:137], v[198:201], v[110:113]
	v_mfma_f32_16x16x32_bf16 v[106:109], v[142:145], v[198:201], v[106:109]
	v_mfma_f32_16x16x32_bf16 v[94:97], v[134:137], v[206:209], v[94:97]
	v_mfma_f32_16x16x32_bf16 v[90:93], v[142:145], v[206:209], v[90:93]
	v_mfma_f32_16x16x32_bf16 v[78:81], v[134:137], v[214:217], v[78:81]
	v_mfma_f32_16x16x32_bf16 v[74:77], v[142:145], v[214:217], v[74:77]
	s_setprio 0
	s_setprio 1
	v_mfma_f32_16x16x32_bf16 v[118:121], v[146:149], v[178:181], v[118:121]
	v_mfma_f32_16x16x32_bf16 v[114:117], v[170:173], v[178:181], v[114:117]
	v_mfma_f32_16x16x32_bf16 v[102:105], v[146:149], v[186:189], v[102:105]
	v_mfma_f32_16x16x32_bf16 v[98:101], v[170:173], v[186:189], v[98:101]
	v_mfma_f32_16x16x32_bf16 v[86:89], v[146:149], v[202:205], v[86:89]
	v_mfma_f32_16x16x32_bf16 v[82:85], v[170:173], v[202:205], v[82:85]
	v_mfma_f32_16x16x32_bf16 v[70:73], v[146:149], v[210:213], v[70:73]
	v_mfma_f32_16x16x32_bf16 v[66:69], v[170:173], v[210:213], v[66:69]
	v_mfma_f32_16x16x32_bf16 v[118:121], v[150:153], v[182:185], v[118:121]
	v_mfma_f32_16x16x32_bf16 v[114:117], v[174:177], v[182:185], v[114:117]
	v_mfma_f32_16x16x32_bf16 v[102:105], v[150:153], v[198:201], v[102:105]
	v_mfma_f32_16x16x32_bf16 v[98:101], v[174:177], v[198:201], v[98:101]
	v_mfma_f32_16x16x32_bf16 v[86:89], v[150:153], v[206:209], v[86:89]
	v_mfma_f32_16x16x32_bf16 v[82:85], v[174:177], v[206:209], v[82:85]
	v_mfma_f32_16x16x32_bf16 v[70:73], v[150:153], v[214:217], v[70:73]
	v_mfma_f32_16x16x32_bf16 v[66:69], v[174:177], v[214:217], v[66:69]
	s_setprio 0
	s_barrier
	s_add_i32 s62, s44, s33
	v_lshl_add_u64 v[190:191], s[24:25], 0, v[156:157]
	s_mov_b32 m0, s62
	ds_read_b128 v[178:181], v196 offset:16384
	ds_read_b128 v[182:185], v196 offset:17408
	ds_read_b128 v[186:189], v196 offset:18432
	ds_read_b128 v[198:201], v196 offset:19456
	ds_read_b128 v[202:205], v196 offset:20480
	ds_read_b128 v[206:209], v196 offset:21504
	ds_read_b128 v[210:213], v196 offset:22528
	ds_read_b128 v[214:217], v196 offset:23552
	global_load_lds_dwordx4 v[190:191], off
	s_add_i32 m0, s62, 0x2000
	s_add_u32 s62, s24, 0x80000
	v_lshl_add_u64 v[218:219], s[24:25], 0, v[160:161]
	s_addc_u32 s63, s25, 0
	s_add_i32 s68, s45, s33
	global_load_lds_dwordx4 v[218:219], off
	v_lshl_add_u64 v[220:221], s[62:63], 0, v[156:157]
	s_mov_b32 m0, s68
	v_lshl_add_u64 v[222:223], s[26:27], 0, v[158:159]
	global_load_lds_dwordx4 v[220:221], off
	v_lshl_add_u64 v[220:221], s[62:63], 0, v[160:161]
	s_add_i32 m0, s68, 0x2000
	s_nop 0
	global_load_lds_dwordx4 v[220:221], off
	v_lshl_add_u64 v[220:221], s[26:27], 0, v[154:155]
	s_mov_b32 m0, s21
	s_nop 0
	global_load_lds_dwordx4 v[220:221], off
	s_mov_b32 m0, s34
	s_nop 0
	global_load_lds_dwordx4 v[222:223], off
	s_waitcnt vmcnt(8)
	s_waitcnt lgkmcnt(0)
	s_barrier
; #define PG8_STAGE(bufoff, gbase, voff) do { _Pragma("unroll") for (int _i = 0; _i < 2; ++_i) \
;         __builtin_amdgcn_global_load_lds((const unsigned*)((const char*)(gbase) + (voff)[_i]), (PG8_LAS unsigned*)(lds + (bufoff) + ldsw + _i * 8192), 16, 0, 0); } while (0)
; #define PG8_LDA(dst, b, h) do { _Pragma("unroll") for (int m = 0; m < 4; ++m) _Pragma("unroll") for (int k = 0; k < 2; ++k) dst[m][k] = *(const PG8_LAS bf16x8*)(lds + PG8_SA(b, h) + aoff + m * 2048 + k * 1024); } while (0)
; #define PG8_LDB(dst, b, h) do { _Pragma("unroll") for (int n = 0; n < 2; ++n) _Pragma("unroll") for (int k = 0; k < 2; ++k) dst[n][k] = *(const PG8_LAS bf16x8*)(lds + PG8_SB(b, h) + boff + n * 2048 + k * 1024); } while (0)
; #define PG8_WAIT_V(n) asm volatile("s_waitcnt vmcnt(" #n ")" ::: "memory")
; #define PG8_WAIT_L(n) asm volatile("s_waitcnt lgkmcnt(" #n ")" ::: "memory")
; #define PG8_BAR __builtin_amdgcn_s_barrier()
; #define PG8_SCHED __builtin_amdgcn_sched_barrier(0)
; template <class Epi, class Sched, bool ALIGN_EPI = false, bool SP2 = false, bool FP8 = false>
; __device__ __forceinline__ void gemm_phase(PG8_LAS unsigned char* lds, const Gemm g, const Sched& S, const Epi& E) {
;     ...
;             PG8_WAIT_V(8); PG8_WAIT_L(0); PG8_BAR; PG8_MMA(0, 0, At, B0); PG8_MMA(0, 1, At, B1); PG8_BAR; PG8_SCHED;
;             PG8_LDA(At, 0, 1); PG8_STAGE(PG8_SB(0, 0), b2, voffB); PG8_STAGE(PG8_SB(0, 1), b2 + hstep, voffB); PG8_STAGE(PG8_SA(0, 0), a2, voffA);
;             PG8_WAIT_V(8); PG8_WAIT_L(0); PG8_BAR; PG8_MMA(1, 0, At, B0); PG8_MMA(1, 1, At, B1); PG8_BAR; PG8_SCHED;
;             PG8_LDB(B0, 1, 0); PG8_LDB(B1, 1, 1); PG8_SCHED; PG8_LDA(At, 1, 0); PG8_STAGE(PG8_SA(0, 1), a2 + hstep, voffA);
;             PG8_WAIT_V(8); PG8_WAIT_L(0); PG8_BAR; PG8_MMA(0, 0, At, B0); PG8_MMA(0, 1, At, B1); PG8_BAR; PG8_SCHED;
	s_setprio 1
	s_waitcnt lgkmcnt(0)
	v_mfma_f32_16x16x32_bf16 v[62:65], v[130:133], v[178:181], v[62:65]
	v_mfma_f32_16x16x32_bf16 v[58:61], v[138:141], v[178:181], v[58:61]
	v_mfma_f32_16x16x32_bf16 v[46:49], v[130:133], v[186:189], v[46:49]
	v_mfma_f32_16x16x32_bf16 v[42:45], v[138:141], v[186:189], v[42:45]
	v_mfma_f32_16x16x32_bf16 v[30:33], v[130:133], v[202:205], v[30:33]
	v_mfma_f32_16x16x32_bf16 v[26:29], v[138:141], v[202:205], v[26:29]
	v_mfma_f32_16x16x32_bf16 v[14:17], v[130:133], v[210:213], v[14:17]
	v_mfma_f32_16x16x32_bf16 v[10:13], v[138:141], v[210:213], v[10:13]
	v_mfma_f32_16x16x32_bf16 v[62:65], v[134:137], v[182:185], v[62:65]
	v_mfma_f32_16x16x32_bf16 v[58:61], v[142:145], v[182:185], v[58:61]
	v_mfma_f32_16x16x32_bf16 v[46:49], v[134:137], v[198:201], v[46:49]
	v_mfma_f32_16x16x32_bf16 v[42:45], v[142:145], v[198:201], v[42:45]
	v_mfma_f32_16x16x32_bf16 v[30:33], v[134:137], v[206:209], v[30:33]
	v_mfma_f32_16x16x32_bf16 v[26:29], v[142:145], v[206:209], v[26:29]
	v_mfma_f32_16x16x32_bf16 v[14:17], v[134:137], v[214:217], v[14:17]
	v_mfma_f32_16x16x32_bf16 v[10:13], v[142:145], v[214:217], v[10:13]
	s_setprio 0
	s_setprio 1
	v_mfma_f32_16x16x32_bf16 v[54:57], v[146:149], v[178:181], v[54:57]
	v_mfma_f32_16x16x32_bf16 v[50:53], v[170:173], v[178:181], v[50:53]
	v_mfma_f32_16x16x32_bf16 v[38:41], v[146:149], v[186:189], v[38:41]
	v_mfma_f32_16x16x32_bf16 v[34:37], v[170:173], v[186:189], v[34:37]
	v_mfma_f32_16x16x32_bf16 v[22:25], v[146:149], v[202:205], v[22:25]
	v_mfma_f32_16x16x32_bf16 v[18:21], v[170:173], v[202:205], v[18:21]
	v_mfma_f32_16x16x32_bf16 v[6:9], v[146:149], v[210:213], v[6:9]
	v_mfma_f32_16x16x32_bf16 v[2:5], v[170:173], v[210:213], v[2:5]
	v_mfma_f32_16x16x32_bf16 v[54:57], v[150:153], v[182:185], v[54:57]
	v_mfma_f32_16x16x32_bf16 v[50:53], v[174:177], v[182:185], v[50:53]
	v_mfma_f32_16x16x32_bf16 v[38:41], v[150:153], v[198:201], v[38:41]
	v_mfma_f32_16x16x32_bf16 v[34:37], v[174:177], v[198:201], v[34:37]
	v_mfma_f32_16x16x32_bf16 v[22:25], v[150:153], v[206:209], v[22:25]
	v_mfma_f32_16x16x32_bf16 v[18:21], v[174:177], v[206:209], v[18:21]
	v_mfma_f32_16x16x32_bf16 v[6:9], v[150:153], v[214:217], v[6:9]
	v_mfma_f32_16x16x32_bf16 v[2:5], v[174:177], v[214:217], v[2:5]
	s_setprio 0
	s_barrier
	s_add_i32 s62, 0, 0x18000
	s_add_i32 s63, 0, 0x1c000
	v_add_u32_e32 v142, s62, v192
	v_add_u32_e32 v174, s63, v192
	ds_read_b128 v[130:133], v142
	ds_read_b128 v[134:137], v142 offset:1024
	ds_read_b128 v[138:141], v142 offset:2048
	ds_read_b128 v[142:145], v142 offset:3072
	ds_read_b128 v[146:149], v174
	ds_read_b128 v[150:153], v174 offset:1024
	ds_read_b128 v[170:173], v174 offset:2048
	ds_read_b128 v[174:177], v174 offset:3072
	s_add_u32 s26, s26, 0x80000
	s_addc_u32 s27, s27, 0
	s_mov_b32 m0, s35
	v_lshl_add_u64 v[224:225], s[26:27], 0, v[154:155]
	ds_read_b128 v[178:181], v196 offset:32768
	ds_read_b128 v[182:185], v196 offset:33792
	ds_read_b128 v[186:189], v196 offset:34816
	ds_read_b128 v[198:201], v196 offset:35840
	ds_read_b128 v[202:205], v196 offset:36864
	ds_read_b128 v[206:209], v196 offset:37888
	ds_read_b128 v[210:213], v196 offset:38912
	ds_read_b128 v[214:217], v196 offset:39936
	global_load_lds_dwordx4 v[224:225], off
	v_lshl_add_u64 v[224:225], s[26:27], 0, v[158:159]
	s_mov_b32 m0, s36
	s_nop 0
	global_load_lds_dwordx4 v[224:225], off
	s_waitcnt vmcnt(8)
	s_waitcnt lgkmcnt(0)
	s_barrier
	s_setprio 1
	s_waitcnt lgkmcnt(0)
	v_mfma_f32_16x16x32_bf16 v[126:129], v[130:133], v[178:181], v[126:129]
	v_mfma_f32_16x16x32_bf16 v[122:125], v[138:141], v[178:181], v[122:125]
	v_mfma_f32_16x16x32_bf16 v[110:113], v[130:133], v[186:189], v[110:113]
	v_mfma_f32_16x16x32_bf16 v[106:109], v[138:141], v[186:189], v[106:109]
	v_mfma_f32_16x16x32_bf16 v[94:97], v[130:133], v[202:205], v[94:97]
	v_mfma_f32_16x16x32_bf16 v[90:93], v[138:141], v[202:205], v[90:93]
	v_mfma_f32_16x16x32_bf16 v[78:81], v[130:133], v[210:213], v[78:81]
	v_mfma_f32_16x16x32_bf16 v[74:77], v[138:141], v[210:213], v[74:77]
	v_mfma_f32_16x16x32_bf16 v[126:129], v[134:137], v[182:185], v[126:129]
	v_mfma_f32_16x16x32_bf16 v[122:125], v[142:145], v[182:185], v[122:125]
	v_mfma_f32_16x16x32_bf16 v[110:113], v[134:137], v[198:201], v[110:113]
	v_mfma_f32_16x16x32_bf16 v[106:109], v[142:145], v[198:201], v[106:109]
	v_mfma_f32_16x16x32_bf16 v[94:97], v[134:137], v[206:209], v[94:97]
	v_mfma_f32_16x16x32_bf16 v[90:93], v[142:145], v[206:209], v[90:93]
	v_mfma_f32_16x16x32_bf16 v[78:81], v[134:137], v[214:217], v[78:81]
	v_mfma_f32_16x16x32_bf16 v[74:77], v[142:145], v[214:217], v[74:77]
	s_setprio 0
	s_setprio 1
	v_mfma_f32_16x16x32_bf16 v[118:121], v[146:149], v[178:181], v[118:121]
	v_mfma_f32_16x16x32_bf16 v[114:117], v[170:173], v[178:181], v[114:117]
	v_mfma_f32_16x16x32_bf16 v[102:105], v[146:149], v[186:189], v[102:105]
	v_mfma_f32_16x16x32_bf16 v[98:101], v[170:173], v[186:189], v[98:101]
	v_mfma_f32_16x16x32_bf16 v[86:89], v[146:149], v[202:205], v[86:89]
	v_mfma_f32_16x16x32_bf16 v[82:85], v[170:173], v[202:205], v[82:85]
	v_mfma_f32_16x16x32_bf16 v[70:73], v[146:149], v[210:213], v[70:73]
	v_mfma_f32_16x16x32_bf16 v[66:69], v[170:173], v[210:213], v[66:69]
	v_mfma_f32_16x16x32_bf16 v[118:121], v[150:153], v[182:185], v[118:121]
	v_mfma_f32_16x16x32_bf16 v[114:117], v[174:177], v[182:185], v[114:117]
	v_mfma_f32_16x16x32_bf16 v[102:105], v[150:153], v[198:201], v[102:105]
	v_mfma_f32_16x16x32_bf16 v[98:101], v[174:177], v[198:201], v[98:101]
	v_mfma_f32_16x16x32_bf16 v[86:89], v[150:153], v[206:209], v[86:89]
	v_mfma_f32_16x16x32_bf16 v[82:85], v[174:177], v[206:209], v[82:85]
	v_mfma_f32_16x16x32_bf16 v[70:73], v[150:153], v[214:217], v[70:73]
	v_mfma_f32_16x16x32_bf16 v[66:69], v[174:177], v[214:217], v[66:69]
	s_setprio 0
	s_barrier
; #define PG8_STAGE(bufoff, gbase, voff) do { _Pragma("unroll") for (int _i = 0; _i < 2; ++_i) \
;         __builtin_amdgcn_global_load_lds((const unsigned*)((const char*)(gbase) + (voff)[_i]), (PG8_LAS unsigned*)(lds + (bufoff) + ldsw + _i * 8192), 16, 0, 0); } while (0)
; #define PG8_LDA(dst, b, h) do { _Pragma("unroll") for (int m = 0; m < 4; ++m) _Pragma("unroll") for (int k = 0; k < 2; ++k) dst[m][k] = *(const PG8_LAS bf16x8*)(lds + PG8_SA(b, h) + aoff + m * 2048 + k * 1024); } while (0)
; #define PG8_WAIT_V(n) asm volatile("s_waitcnt vmcnt(" #n ")" ::: "memory")
; #define PG8_WAIT_L(n) asm volatile("s_waitcnt lgkmcnt(" #n ")" ::: "memory")
; #define PG8_BAR __builtin_amdgcn_s_barrier()
; #define PG8_SCHED __builtin_amdgcn_sched_barrier(0)
; template <class Epi, class Sched, bool ALIGN_EPI = false, bool SP2 = false, bool FP8 = false>
; __device__ __forceinline__ void gemm_phase(PG8_LAS unsigned char* lds, const Gemm g, const Sched& S, const Epi& E) {
;     ...
;         for (int t = 0; t < nt; t += 2) {
;     ...
;             PG8_WAIT_V(8); PG8_WAIT_L(0); PG8_BAR; PG8_MMA(0, 0, At, B0); PG8_MMA(0, 1, At, B1); PG8_BAR; PG8_SCHED;
;             PG8_LDA(At, 1, 1); PG8_STAGE(PG8_SB(1, 0), b3, voffB); PG8_STAGE(PG8_SB(1, 1), b3 + hstep, voffB); PG8_STAGE(PG8_SA(1, 0), a3, voffA);
;             PG8_WAIT_V(8); PG8_WAIT_L(0); PG8_BAR; PG8_MMA(1, 0, At, B0); PG8_MMA(1, 1, At, B1); PG8_BAR; PG8_SCHED;
	s_add_i32 s26, s62, s33
	v_lshl_add_u64 v[190:191], v[190:191], 0, s[4:5]
	s_mov_b32 m0, s26
	ds_read_b128 v[178:181], v196 offset:49152
	ds_read_b128 v[182:185], v196 offset:50176
	ds_read_b128 v[186:189], v196 offset:51200
	ds_read_b128 v[198:201], v196 offset:52224
	ds_read_b128 v[202:205], v196 offset:53248
	ds_read_b128 v[206:209], v196 offset:54272
	ds_read_b128 v[210:213], v196 offset:55296
	ds_read_b128 v[214:217], v196 offset:56320
	global_load_lds_dwordx4 v[190:191], off
	s_add_i32 m0, s26, 0x2000
	s_add_u32 s24, s24, 0x80080
	v_lshl_add_u64 v[190:191], v[218:219], 0, s[4:5]
	s_addc_u32 s25, s25, 0
	s_add_i32 s26, s63, s33
	global_load_lds_dwordx4 v[190:191], off
	v_lshl_add_u64 v[190:191], s[24:25], 0, v[156:157]
	s_mov_b32 m0, s26
	s_nop 0
	global_load_lds_dwordx4 v[190:191], off
	v_lshl_add_u64 v[190:191], s[24:25], 0, v[160:161]
	s_add_i32 m0, s26, 0x2000
	s_nop 0
	global_load_lds_dwordx4 v[190:191], off
	v_lshl_add_u64 v[190:191], v[220:221], 0, s[4:5]
	s_mov_b32 m0, s41
	s_nop 0
	global_load_lds_dwordx4 v[190:191], off
	v_lshl_add_u64 v[190:191], v[222:223], 0, s[4:5]
	s_mov_b32 m0, s42
	s_nop 0
	global_load_lds_dwordx4 v[190:191], off
	s_waitcnt vmcnt(8)
	s_waitcnt lgkmcnt(0)
	s_barrier
	s_setprio 1
	s_waitcnt lgkmcnt(0)
	v_mfma_f32_16x16x32_bf16 v[62:65], v[130:133], v[178:181], v[62:65]
	v_mfma_f32_16x16x32_bf16 v[58:61], v[138:141], v[178:181], v[58:61]
	v_mfma_f32_16x16x32_bf16 v[46:49], v[130:133], v[186:189], v[46:49]
	v_mfma_f32_16x16x32_bf16 v[42:45], v[138:141], v[186:189], v[42:45]
	v_mfma_f32_16x16x32_bf16 v[30:33], v[130:133], v[202:205], v[30:33]
	v_mfma_f32_16x16x32_bf16 v[26:29], v[138:141], v[202:205], v[26:29]
	v_mfma_f32_16x16x32_bf16 v[14:17], v[130:133], v[210:213], v[14:17]
	v_mfma_f32_16x16x32_bf16 v[10:13], v[138:141], v[210:213], v[10:13]
	v_mfma_f32_16x16x32_bf16 v[62:65], v[134:137], v[182:185], v[62:65]
	v_mfma_f32_16x16x32_bf16 v[58:61], v[142:145], v[182:185], v[58:61]
	v_mfma_f32_16x16x32_bf16 v[46:49], v[134:137], v[198:201], v[46:49]
	v_mfma_f32_16x16x32_bf16 v[42:45], v[142:145], v[198:201], v[42:45]
	v_mfma_f32_16x16x32_bf16 v[30:33], v[134:137], v[206:209], v[30:33]
	v_mfma_f32_16x16x32_bf16 v[26:29], v[142:145], v[206:209], v[26:29]
	v_mfma_f32_16x16x32_bf16 v[14:17], v[134:137], v[214:217], v[14:17]
	v_mfma_f32_16x16x32_bf16 v[10:13], v[142:145], v[214:217], v[10:13]
	s_setprio 0
	s_setprio 1
	v_mfma_f32_16x16x32_bf16 v[54:57], v[146:149], v[178:181], v[54:57]
	v_mfma_f32_16x16x32_bf16 v[50:53], v[170:173], v[178:181], v[50:53]
	v_mfma_f32_16x16x32_bf16 v[38:41], v[146:149], v[186:189], v[38:41]
	v_mfma_f32_16x16x32_bf16 v[34:37], v[170:173], v[186:189], v[34:37]
	v_mfma_f32_16x16x32_bf16 v[22:25], v[146:149], v[202:205], v[22:25]
	v_mfma_f32_16x16x32_bf16 v[18:21], v[170:173], v[202:205], v[18:21]
	v_mfma_f32_16x16x32_bf16 v[6:9], v[146:149], v[210:213], v[6:9]
	v_mfma_f32_16x16x32_bf16 v[2:5], v[170:173], v[210:213], v[2:5]
	v_mfma_f32_16x16x32_bf16 v[54:57], v[150:153], v[182:185], v[54:57]
	v_mfma_f32_16x16x32_bf16 v[50:53], v[174:177], v[182:185], v[50:53]
	v_mfma_f32_16x16x32_bf16 v[38:41], v[150:153], v[198:201], v[38:41]
	v_mfma_f32_16x16x32_bf16 v[34:37], v[174:177], v[198:201], v[34:37]
	v_mfma_f32_16x16x32_bf16 v[22:25], v[150:153], v[206:209], v[22:25]
	v_mfma_f32_16x16x32_bf16 v[18:21], v[174:177], v[206:209], v[18:21]
	v_mfma_f32_16x16x32_bf16 v[6:9], v[150:153], v[214:217], v[6:9]
	v_mfma_f32_16x16x32_bf16 v[2:5], v[174:177], v[214:217], v[2:5]
	s_setprio 0
	s_add_i32 s61, s61, 2
	s_add_u32 s22, s22, 0x100
	s_addc_u32 s23, s23, 0
	s_add_u32 s57, s57, 0x100
	s_addc_u32 s60, s60, 0
	s_cmp_gt_u32 s61, 29
	s_cbranch_scc0 .Lrot_head_1006
	s_barrier
	s_and_b64 vcc, exec, s[8:9]
	s_cbranch_vccz .LBB0_1009
	s_barrier

; template <class Epi, class Sched, bool ALIGN_EPI = false, bool SP2 = false, bool FP8 = false>
; __device__ __forceinline__ void gemm_phase(PG8_LAS unsigned char* lds, const Gemm g, const Sched& S, const Epi& E) {
;     ...
;         const bool has_next = S.next(ui + 1, nxt);
;         const char* nA = has_next ? (const char*)g.A + (size_t)nxt.pm * tstep : cA; const char* nB = has_next ? (const char*)g.Bt + (size_t)nxt.pb * tstep : cB;
;         for (int t = 0; t < nt; t += 2) {
;             const bool last = (t == nt - 2);
;             const char* a1 = cA + (size_t)(t + 1) * kstep;
;             const char* a2 = last ? nA : cA + (size_t)(t + 2) * kstep; const char* b2 = last ? nB : cB + (size_t)(t + 2) * kstep;
;             const char* a3 = a2 + kstep; const char* b3 = b2 + kstep;
;     ...
;         if (!has_next) break;
; #pragma unroll
;         for (int a = 0; a < 2; ++a)
; #pragma unroll
;             for (int b = 0; b < 2; ++b)
; #pragma unroll
;                 for (int m = 0; m < 4; ++m)
; #pragma unroll
;                     for (int n = 0; n < 2; ++n) acc[a][b][m][n] = (f32x4){0.f, 0.f, 0.f, 0.f};
;         cur = nxt; cA = nA; cB = nB; ++ui;
.LBB0_1141:
	s_ashr_i32 s17, s16, 31
	s_lshl_b64 s[18:19], s[16:17], 19
	s_add_u32 s18, s13, s18
	s_addc_u32 s19, s30, s19
	s_and_b64 s[20:21], s[6:7], exec
	s_cselect_b32 s17, s19, s25
	s_cselect_b32 s49, s18, s24
	s_ashr_i32 s15, s14, 31
	s_lshl_b64 s[20:21], s[14:15], 19
	s_add_u32 s20, s31, s20
	s_addc_u32 s21, s33, s21
	s_and_b64 s[28:29], s[6:7], exec
	s_cselect_b32 s15, s21, s27
	s_cselect_b32 s56, s20, s26
	s_add_u32 s24, s24, 0x40080
	s_addc_u32 s25, s25, 0
	s_add_u32 s57, s26, 0x100
	v_mov_b32_e32 v34, 0
	s_addc_u32 s60, s27, 0
	s_mov_b32 s61, -2
	v_mov_b32_e32 v35, v34
	v_mov_b32_e32 v36, v34
	v_mov_b32_e32 v37, v34
	v_mov_b32_e32 v42, v34
	v_mov_b32_e32 v43, v34
	v_mov_b32_e32 v44, v34
	v_mov_b32_e32 v45, v34
	v_mov_b32_e32 v50, v34
	v_mov_b32_e32 v51, v34
	v_mov_b32_e32 v52, v34
	v_mov_b32_e32 v53, v34
	v_mov_b32_e32 v58, v34
	v_mov_b32_e32 v59, v34
	v_mov_b32_e32 v60, v34
	v_mov_b32_e32 v61, v34
	v_mov_b32_e32 v66, v34
	v_mov_b32_e32 v67, v34
	v_mov_b32_e32 v68, v34
	v_mov_b32_e32 v69, v34
	v_mov_b32_e32 v74, v34
	v_mov_b32_e32 v75, v34
	v_mov_b32_e32 v76, v34
	v_mov_b32_e32 v77, v34
	v_mov_b32_e32 v82, v34
	v_mov_b32_e32 v83, v34
	v_mov_b32_e32 v84, v34
	v_mov_b32_e32 v85, v34
	v_mov_b32_e32 v90, v34
	v_mov_b32_e32 v91, v34
	v_mov_b32_e32 v92, v34
	v_mov_b32_e32 v93, v34
	v_mov_b32_e32 v38, v34
	v_mov_b32_e32 v39, v34
	v_mov_b32_e32 v40, v34
	v_mov_b32_e32 v41, v34
	v_mov_b32_e32 v46, v34
	v_mov_b32_e32 v47, v34
	v_mov_b32_e32 v48, v34
	v_mov_b32_e32 v49, v34
	v_mov_b32_e32 v54, v34
	v_mov_b32_e32 v55, v34
	v_mov_b32_e32 v56, v34
	v_mov_b32_e32 v57, v34
	v_mov_b32_e32 v62, v34
	v_mov_b32_e32 v63, v34
	v_mov_b32_e32 v64, v34
	v_mov_b32_e32 v65, v34
	v_mov_b32_e32 v70, v34
	v_mov_b32_e32 v71, v34
	v_mov_b32_e32 v72, v34
	v_mov_b32_e32 v73, v34
	v_mov_b32_e32 v78, v34
	v_mov_b32_e32 v79, v34
	v_mov_b32_e32 v80, v34
	v_mov_b32_e32 v81, v34
	v_mov_b32_e32 v86, v34
	v_mov_b32_e32 v87, v34
	v_mov_b32_e32 v88, v34
	v_mov_b32_e32 v89, v34
	v_mov_b32_e32 v94, v34
	v_mov_b32_e32 v95, v34
	v_mov_b32_e32 v96, v34
	v_mov_b32_e32 v97, v34
	v_mov_b32_e32 v98, v34
	v_mov_b32_e32 v99, v34
	v_mov_b32_e32 v100, v34
	v_mov_b32_e32 v101, v34
	v_mov_b32_e32 v106, v34
	v_mov_b32_e32 v107, v34
	v_mov_b32_e32 v108, v34
	v_mov_b32_e32 v109, v34
	v_mov_b32_e32 v114, v34
	v_mov_b32_e32 v115, v34
	v_mov_b32_e32 v116, v34
	v_mov_b32_e32 v117, v34
	v_mov_b32_e32 v122, v34
	v_mov_b32_e32 v123, v34
	v_mov_b32_e32 v124, v34
	v_mov_b32_e32 v125, v34
	v_mov_b32_e32 v130, v34
	v_mov_b32_e32 v131, v34
	v_mov_b32_e32 v132, v34
	v_mov_b32_e32 v133, v34
	v_mov_b32_e32 v138, v34
	v_mov_b32_e32 v139, v34
	v_mov_b32_e32 v140, v34
	v_mov_b32_e32 v141, v34
	v_mov_b32_e32 v146, v34
	v_mov_b32_e32 v147, v34
	v_mov_b32_e32 v148, v34
	v_mov_b32_e32 v149, v34
	v_mov_b32_e32 v154, v34
	v_mov_b32_e32 v155, v34
	v_mov_b32_e32 v156, v34
	v_mov_b32_e32 v157, v34
	v_mov_b32_e32 v102, v34
	v_mov_b32_e32 v103, v34
	v_mov_b32_e32 v104, v34
	v_mov_b32_e32 v105, v34
	v_mov_b32_e32 v110, v34
	v_mov_b32_e32 v111, v34
	v_mov_b32_e32 v112, v34
	v_mov_b32_e32 v113, v34
	v_mov_b32_e32 v118, v34
	v_mov_b32_e32 v119, v34
	v_mov_b32_e32 v120, v34
	v_mov_b32_e32 v121, v34
	v_mov_b32_e32 v126, v34
	v_mov_b32_e32 v127, v34
	v_mov_b32_e32 v128, v34
	v_mov_b32_e32 v129, v34
	v_mov_b32_e32 v134, v34
	v_mov_b32_e32 v135, v34
	v_mov_b32_e32 v136, v34
	v_mov_b32_e32 v137, v34
	v_mov_b32_e32 v142, v34
	v_mov_b32_e32 v143, v34
	v_mov_b32_e32 v144, v34
	v_mov_b32_e32 v145, v34
	v_mov_b32_e32 v150, v34
	v_mov_b32_e32 v151, v34
	v_mov_b32_e32 v152, v34
	v_mov_b32_e32 v153, v34
	v_mov_b32_e32 v158, v34
	v_mov_b32_e32 v159, v34
	v_mov_b32_e32 v160, v34
	v_mov_b32_e32 v161, v34
	s_branch .LBB0_1142

; #define PG8_STAGE(bufoff, gbase, voff) do { _Pragma("unroll") for (int _i = 0; _i < 2; ++_i) \
;         __builtin_amdgcn_global_load_lds((const unsigned*)((const char*)(gbase) + (voff)[_i]), (PG8_LAS unsigned*)(lds + (bufoff) + ldsw + _i * 8192), 16, 0, 0); } while (0)
; #define PG8_LDA(dst, b, h) do { _Pragma("unroll") for (int m = 0; m < 4; ++m) _Pragma("unroll") for (int k = 0; k < 2; ++k) dst[m][k] = *(const PG8_LAS bf16x8*)(lds + PG8_SA(b, h) + aoff + m * 2048 + k * 1024); } while (0)
; #define PG8_LDB(dst, b, h) do { _Pragma("unroll") for (int n = 0; n < 2; ++n) _Pragma("unroll") for (int k = 0; k < 2; ++k) dst[n][k] = *(const PG8_LAS bf16x8*)(lds + PG8_SB(b, h) + boff + n * 2048 + k * 1024); } while (0)
; #define PG8_WAIT_V(n) asm volatile("s_waitcnt vmcnt(" #n ")" ::: "memory")
; #define PG8_WAIT_L(n) asm volatile("s_waitcnt lgkmcnt(" #n ")" ::: "memory")
; #define PG8_BAR __builtin_amdgcn_s_barrier()
; #define PG8_SCHED __builtin_amdgcn_sched_barrier(0)
; template <class Epi, class Sched, bool ALIGN_EPI = false, bool SP2 = false, bool FP8 = false>
; __device__ __forceinline__ void gemm_phase(PG8_LAS unsigned char* lds, const Gemm g, const Sched& S, const Epi& E) {
;     ...
;             PG8_LDB(B0, 0, 0); PG8_LDB(B1, 0, 1); PG8_SCHED; PG8_LDA(At, 0, 0); PG8_STAGE(PG8_SA(1, 1), a1 + hstep, voffA);
;             PG8_WAIT_V(8); PG8_WAIT_L(0); PG8_BAR; PG8_MMA(0, 0, At, B0); PG8_MMA(0, 1, At, B1); PG8_BAR; PG8_SCHED;
;             PG8_LDA(At, 0, 1); PG8_STAGE(PG8_SB(0, 0), b2, voffB); PG8_STAGE(PG8_SB(0, 1), b2 + hstep, voffB); PG8_STAGE(PG8_SA(0, 0), a2, voffA);
;             PG8_WAIT_V(8); PG8_WAIT_L(0); PG8_BAR; PG8_MMA(1, 0, At, B0); PG8_MMA(1, 1, At, B1); PG8_BAR; PG8_SCHED;
.LBB0_1142:
	ds_read_b128 v[26:29], v188
	ds_read_b128 v[30:33], v188 offset:1024
	ds_read_b128 v[18:21], v188 offset:2048
	ds_read_b128 v[22:25], v188 offset:3072
	ds_read_b128 v[10:13], v189
	ds_read_b128 v[14:17], v189 offset:1024
	ds_read_b128 v[2:5], v189 offset:2048
	ds_read_b128 v[6:9], v189 offset:3072
	s_add_u32 s26, s24, 0xfffc0080
	s_addc_u32 s27, s25, -1
	s_cmp_eq_u32 s61, 12
	s_cselect_b32 s29, s17, s27
	s_cselect_b32 s28, s49, s26
	s_cselect_b32 s27, s15, s60
	s_cselect_b32 s26, s56, s57
	v_lshl_add_u64 v[216:217], s[24:25], 0, v[170:171]
	s_add_i32 m0, s23, 0xc000
	ds_read_b128 v[178:181], v190
	ds_read_b128 v[182:185], v190 offset:1024
	ds_read_b128 v[192:195], v190 offset:2048
	ds_read_b128 v[196:199], v190 offset:3072
	ds_read_b128 v[200:203], v190 offset:4096
	ds_read_b128 v[204:207], v190 offset:5120
	ds_read_b128 v[208:211], v190 offset:6144
	ds_read_b128 v[212:215], v190 offset:7168
	global_load_lds_dwordx4 v[216:217], off
	v_lshl_add_u64 v[216:217], s[24:25], 0, v[172:173]
	s_add_i32 m0, s23, 0xe000
	s_nop 0
	global_load_lds_dwordx4 v[216:217], off
	s_waitcnt vmcnt(8)
	s_waitcnt lgkmcnt(0)
	s_barrier
	s_setprio 1
	s_waitcnt lgkmcnt(0)
	v_mfma_f32_16x16x128_f8f6f4 v[158:161], v[26:33], v[178:185], v[158:161]
	v_mfma_f32_16x16x128_f8f6f4 v[150:153], v[18:25], v[178:185], v[150:153]
	v_mfma_f32_16x16x128_f8f6f4 v[142:145], v[26:33], v[192:199], v[142:145]
	v_mfma_f32_16x16x128_f8f6f4 v[134:137], v[18:25], v[192:199], v[134:137]
	v_mfma_f32_16x16x128_f8f6f4 v[126:129], v[26:33], v[200:207], v[126:129]
	v_mfma_f32_16x16x128_f8f6f4 v[118:121], v[18:25], v[200:207], v[118:121]
	v_mfma_f32_16x16x128_f8f6f4 v[110:113], v[26:33], v[208:215], v[110:113]
	v_mfma_f32_16x16x128_f8f6f4 v[102:105], v[18:25], v[208:215], v[102:105]
	s_setprio 0
	s_setprio 1
	v_mfma_f32_16x16x128_f8f6f4 v[154:157], v[10:17], v[178:185], v[154:157]
	v_mfma_f32_16x16x128_f8f6f4 v[146:149], v[2:9], v[178:185], v[146:149]
	v_mfma_f32_16x16x128_f8f6f4 v[138:141], v[10:17], v[192:199], v[138:141]
	v_mfma_f32_16x16x128_f8f6f4 v[130:133], v[2:9], v[192:199], v[130:133]
	v_mfma_f32_16x16x128_f8f6f4 v[122:125], v[10:17], v[200:207], v[122:125]
	v_mfma_f32_16x16x128_f8f6f4 v[114:117], v[2:9], v[200:207], v[114:117]
	v_mfma_f32_16x16x128_f8f6f4 v[106:109], v[10:17], v[208:215], v[106:109]
	v_mfma_f32_16x16x128_f8f6f4 v[98:101], v[2:9], v[208:215], v[98:101]
	s_setprio 0
	s_barrier
	s_add_i32 s62, s45, s34
	v_lshl_add_u64 v[178:179], s[26:27], 0, v[166:167]
	s_mov_b32 m0, s62
	ds_read_b128 v[192:195], v190 offset:16384
	ds_read_b128 v[196:199], v190 offset:17408
	ds_read_b128 v[200:203], v190 offset:18432
	ds_read_b128 v[204:207], v190 offset:19456
	ds_read_b128 v[208:211], v190 offset:20480
	ds_read_b128 v[212:215], v190 offset:21504
	ds_read_b128 v[216:219], v190 offset:22528
	ds_read_b128 v[220:223], v190 offset:23552
	global_load_lds_dwordx4 v[178:179], off
	s_add_i32 m0, s62, 0x2000
	s_add_u32 s62, s26, 0x40000
	v_lshl_add_u64 v[180:181], s[26:27], 0, v[162:163]
	s_addc_u32 s63, s27, 0
	s_add_i32 s68, s46, s34
	global_load_lds_dwordx4 v[180:181], off
	v_lshl_add_u64 v[182:183], s[62:63], 0, v[166:167]
	s_mov_b32 m0, s68
	v_lshl_add_u64 v[184:185], s[28:29], 0, v[164:165]
	global_load_lds_dwordx4 v[182:183], off
	v_lshl_add_u64 v[182:183], s[62:63], 0, v[162:163]
	s_add_i32 m0, s68, 0x2000
	s_nop 0
	global_load_lds_dwordx4 v[182:183], off
	v_lshl_add_u64 v[182:183], s[28:29], 0, v[168:169]
	s_mov_b32 m0, s23
	s_nop 0
	global_load_lds_dwordx4 v[182:183], off
	s_mov_b32 m0, s37
	s_nop 0
	global_load_lds_dwordx4 v[184:185], off
	s_waitcnt vmcnt(8)
	s_waitcnt lgkmcnt(0)
	s_barrier
	s_setprio 1
	s_waitcnt lgkmcnt(0)
	v_mfma_f32_16x16x128_f8f6f4 v[94:97], v[26:33], v[192:199], v[94:97]
	v_mfma_f32_16x16x128_f8f6f4 v[86:89], v[18:25], v[192:199], v[86:89]
	v_mfma_f32_16x16x128_f8f6f4 v[78:81], v[26:33], v[200:207], v[78:81]
	v_mfma_f32_16x16x128_f8f6f4 v[70:73], v[18:25], v[200:207], v[70:73]
	v_mfma_f32_16x16x128_f8f6f4 v[62:65], v[26:33], v[208:215], v[62:65]
	v_mfma_f32_16x16x128_f8f6f4 v[54:57], v[18:25], v[208:215], v[54:57]
	v_mfma_f32_16x16x128_f8f6f4 v[46:49], v[26:33], v[216:223], v[46:49]
	v_mfma_f32_16x16x128_f8f6f4 v[38:41], v[18:25], v[216:223], v[38:41]
	s_setprio 0
	s_setprio 1
	v_mfma_f32_16x16x128_f8f6f4 v[90:93], v[10:17], v[192:199], v[90:93]
	v_mfma_f32_16x16x128_f8f6f4 v[82:85], v[2:9], v[192:199], v[82:85]
	v_mfma_f32_16x16x128_f8f6f4 v[74:77], v[10:17], v[200:207], v[74:77]
	v_mfma_f32_16x16x128_f8f6f4 v[66:69], v[2:9], v[200:207], v[66:69]
	v_mfma_f32_16x16x128_f8f6f4 v[58:61], v[10:17], v[208:215], v[58:61]
	v_mfma_f32_16x16x128_f8f6f4 v[50:53], v[2:9], v[208:215], v[50:53]
	v_mfma_f32_16x16x128_f8f6f4 v[42:45], v[10:17], v[216:223], v[42:45]
	v_mfma_f32_16x16x128_f8f6f4 v[34:37], v[2:9], v[216:223], v[34:37]
	s_setprio 0
	s_barrier
; #define PG8_STAGE(bufoff, gbase, voff) do { _Pragma("unroll") for (int _i = 0; _i < 2; ++_i) \
;         __builtin_amdgcn_global_load_lds((const unsigned*)((const char*)(gbase) + (voff)[_i]), (PG8_LAS unsigned*)(lds + (bufoff) + ldsw + _i * 8192), 16, 0, 0); } while (0)
; #define PG8_LDA(dst, b, h) do { _Pragma("unroll") for (int m = 0; m < 4; ++m) _Pragma("unroll") for (int k = 0; k < 2; ++k) dst[m][k] = *(const PG8_LAS bf16x8*)(lds + PG8_SA(b, h) + aoff + m * 2048 + k * 1024); } while (0)
; #define PG8_LDB(dst, b, h) do { _Pragma("unroll") for (int n = 0; n < 2; ++n) _Pragma("unroll") for (int k = 0; k < 2; ++k) dst[n][k] = *(const PG8_LAS bf16x8*)(lds + PG8_SB(b, h) + boff + n * 2048 + k * 1024); } while (0)
; #define PG8_WAIT_V(n) asm volatile("s_waitcnt vmcnt(" #n ")" ::: "memory")
; #define PG8_WAIT_L(n) asm volatile("s_waitcnt lgkmcnt(" #n ")" ::: "memory")
; #define PG8_BAR __builtin_amdgcn_s_barrier()
; #define PG8_SCHED __builtin_amdgcn_sched_barrier(0)
; template <class Epi, class Sched, bool ALIGN_EPI = false, bool SP2 = false, bool FP8 = false>
; __device__ __forceinline__ void gemm_phase(PG8_LAS unsigned char* lds, const Gemm g, const Sched& S, const Epi& E) {
;     ...
;             PG8_WAIT_V(8); PG8_WAIT_L(0); PG8_BAR; PG8_MMA(1, 0, At, B0); PG8_MMA(1, 1, At, B1); PG8_BAR; PG8_SCHED;
;             PG8_LDB(B0, 1, 0); PG8_LDB(B1, 1, 1); PG8_SCHED; PG8_LDA(At, 1, 0); PG8_STAGE(PG8_SA(0, 1), a2 + hstep, voffA);
;             PG8_WAIT_V(8); PG8_WAIT_L(0); PG8_BAR; PG8_MMA(0, 0, At, B0); PG8_MMA(0, 1, At, B1); PG8_BAR; PG8_SCHED;
;             PG8_LDA(At, 1, 1); PG8_STAGE(PG8_SB(1, 0), b3, voffB); PG8_STAGE(PG8_SB(1, 1), b3 + hstep, voffB); PG8_STAGE(PG8_SA(1, 0), a3, voffA);
;             PG8_WAIT_V(8); PG8_WAIT_L(0); PG8_BAR; PG8_MMA(1, 0, At, B0); PG8_MMA(1, 1, At, B1); PG8_BAR; PG8_SCHED;
;     ...
;         if constexpr (FP8) asm volatile("s_nop 15\n\ts_nop 15\n\ts_nop 15\n\ts_nop 15" ::: "memory");
;         if constexpr (ALIGN_EPI) { if (wr == 0) PG8_BAR; }
	s_add_i32 s62, 0, 0x18000
	s_add_i32 s63, 0, 0x1c000
	v_add_u32_e32 v14, s62, v186
	v_add_u32_e32 v30, s63, v186
	ds_read_b128 v[2:5], v14
	ds_read_b128 v[6:9], v14 offset:1024
	ds_read_b128 v[10:13], v14 offset:2048
	ds_read_b128 v[14:17], v14 offset:3072
	ds_read_b128 v[18:21], v30
	ds_read_b128 v[22:25], v30 offset:1024
	ds_read_b128 v[26:29], v30 offset:2048
	ds_read_b128 v[30:33], v30 offset:3072
	s_add_u32 s28, s28, 0x40000
	s_addc_u32 s29, s29, 0
	s_mov_b32 m0, s38
	v_lshl_add_u64 v[224:225], s[28:29], 0, v[168:169]
	ds_read_b128 v[192:195], v190 offset:32768
	ds_read_b128 v[196:199], v190 offset:33792
	ds_read_b128 v[200:203], v190 offset:34816
	ds_read_b128 v[204:207], v190 offset:35840
	ds_read_b128 v[208:211], v190 offset:36864
	ds_read_b128 v[212:215], v190 offset:37888
	ds_read_b128 v[216:219], v190 offset:38912
	ds_read_b128 v[220:223], v190 offset:39936
	global_load_lds_dwordx4 v[224:225], off
	v_lshl_add_u64 v[224:225], s[28:29], 0, v[164:165]
	s_mov_b32 m0, s39
	s_nop 0
	global_load_lds_dwordx4 v[224:225], off
	s_waitcnt vmcnt(8)
	s_waitcnt lgkmcnt(0)
	s_barrier
	s_setprio 1
	s_waitcnt lgkmcnt(0)
	v_mfma_f32_16x16x128_f8f6f4 v[158:161], v[2:9], v[192:199], v[158:161]
	v_mfma_f32_16x16x128_f8f6f4 v[150:153], v[10:17], v[192:199], v[150:153]
	v_mfma_f32_16x16x128_f8f6f4 v[142:145], v[2:9], v[200:207], v[142:145]
	v_mfma_f32_16x16x128_f8f6f4 v[134:137], v[10:17], v[200:207], v[134:137]
	v_mfma_f32_16x16x128_f8f6f4 v[126:129], v[2:9], v[208:215], v[126:129]
	v_mfma_f32_16x16x128_f8f6f4 v[118:121], v[10:17], v[208:215], v[118:121]
	v_mfma_f32_16x16x128_f8f6f4 v[110:113], v[2:9], v[216:223], v[110:113]
	v_mfma_f32_16x16x128_f8f6f4 v[102:105], v[10:17], v[216:223], v[102:105]
	s_setprio 0
	s_setprio 1
	v_mfma_f32_16x16x128_f8f6f4 v[154:157], v[18:25], v[192:199], v[154:157]
	v_mfma_f32_16x16x128_f8f6f4 v[146:149], v[26:33], v[192:199], v[146:149]
	v_mfma_f32_16x16x128_f8f6f4 v[138:141], v[18:25], v[200:207], v[138:141]
	v_mfma_f32_16x16x128_f8f6f4 v[130:133], v[26:33], v[200:207], v[130:133]
	v_mfma_f32_16x16x128_f8f6f4 v[122:125], v[18:25], v[208:215], v[122:125]
	v_mfma_f32_16x16x128_f8f6f4 v[114:117], v[26:33], v[208:215], v[114:117]
	v_mfma_f32_16x16x128_f8f6f4 v[106:109], v[18:25], v[216:223], v[106:109]
	v_mfma_f32_16x16x128_f8f6f4 v[98:101], v[26:33], v[216:223], v[98:101]
	s_setprio 0
	s_barrier
	s_add_i32 s28, s62, s34
	v_lshl_add_u64 v[178:179], v[178:179], 0, s[8:9]
	s_mov_b32 m0, s28
	ds_read_b128 v[192:195], v190 offset:49152
	ds_read_b128 v[196:199], v190 offset:50176
	ds_read_b128 v[200:203], v190 offset:51200
	ds_read_b128 v[204:207], v190 offset:52224
	ds_read_b128 v[208:211], v190 offset:53248
	ds_read_b128 v[212:215], v190 offset:54272
	ds_read_b128 v[216:219], v190 offset:55296
	ds_read_b128 v[220:223], v190 offset:56320
	global_load_lds_dwordx4 v[178:179], off
	s_add_i32 m0, s28, 0x2000
	s_add_u32 s26, s26, 0x40080
	v_lshl_add_u64 v[178:179], v[180:181], 0, s[8:9]
	s_addc_u32 s27, s27, 0
	s_add_i32 s28, s63, s34
	global_load_lds_dwordx4 v[178:179], off
	v_lshl_add_u64 v[178:179], s[26:27], 0, v[166:167]
	s_mov_b32 m0, s28
	s_nop 0
	global_load_lds_dwordx4 v[178:179], off
	v_lshl_add_u64 v[178:179], s[26:27], 0, v[162:163]
	s_add_i32 m0, s28, 0x2000
	s_nop 0
	global_load_lds_dwordx4 v[178:179], off
	v_lshl_add_u64 v[178:179], v[182:183], 0, s[8:9]
	s_mov_b32 m0, s42
	s_nop 0
	global_load_lds_dwordx4 v[178:179], off
	v_lshl_add_u64 v[178:179], v[184:185], 0, s[8:9]
	s_mov_b32 m0, s43
	s_nop 0
	global_load_lds_dwordx4 v[178:179], off
	s_waitcnt vmcnt(8)
	s_waitcnt lgkmcnt(0)
	s_barrier
	s_setprio 1
	s_waitcnt lgkmcnt(0)
	v_mfma_f32_16x16x128_f8f6f4 v[94:97], v[2:9], v[192:199], v[94:97]
	v_mfma_f32_16x16x128_f8f6f4 v[86:89], v[10:17], v[192:199], v[86:89]
	v_mfma_f32_16x16x128_f8f6f4 v[78:81], v[2:9], v[200:207], v[78:81]
	v_mfma_f32_16x16x128_f8f6f4 v[70:73], v[10:17], v[200:207], v[70:73]
	v_mfma_f32_16x16x128_f8f6f4 v[62:65], v[2:9], v[208:215], v[62:65]
	v_mfma_f32_16x16x128_f8f6f4 v[54:57], v[10:17], v[208:215], v[54:57]
	v_mfma_f32_16x16x128_f8f6f4 v[46:49], v[2:9], v[216:223], v[46:49]
	v_mfma_f32_16x16x128_f8f6f4 v[38:41], v[10:17], v[216:223], v[38:41]
	s_setprio 0
	s_setprio 1
	v_mfma_f32_16x16x128_f8f6f4 v[90:93], v[18:25], v[192:199], v[90:93]
	v_mfma_f32_16x16x128_f8f6f4 v[82:85], v[26:33], v[192:199], v[82:85]
	v_mfma_f32_16x16x128_f8f6f4 v[74:77], v[18:25], v[200:207], v[74:77]
	v_mfma_f32_16x16x128_f8f6f4 v[66:69], v[26:33], v[200:207], v[66:69]
	v_mfma_f32_16x16x128_f8f6f4 v[58:61], v[18:25], v[208:215], v[58:61]
	v_mfma_f32_16x16x128_f8f6f4 v[50:53], v[26:33], v[208:215], v[50:53]
	v_mfma_f32_16x16x128_f8f6f4 v[42:45], v[18:25], v[216:223], v[42:45]
	v_mfma_f32_16x16x128_f8f6f4 v[34:37], v[26:33], v[216:223], v[34:37]
	s_setprio 0
	s_add_i32 s61, s61, 2
	s_add_u32 s24, s24, 0x100
	s_addc_u32 s25, s25, 0
	s_add_u32 s57, s57, 0x100
	s_addc_u32 s60, s60, 0
	s_cmp_gt_u32 s61, 13
	s_cbranch_scc0 .Lrot_head_1142
	s_barrier
	s_nop 15
	s_nop 15
	s_nop 15
	s_nop 15
	s_and_b64 vcc, exec, s[10:11]
	s_cbranch_vccz .LBB0_1145
	s_barrier

; template <class Epi, class Sched, bool ALIGN_EPI = false, bool SP2 = false, bool FP8 = false>
; __device__ __forceinline__ void gemm_phase(PG8_LAS unsigned char* lds, const Gemm g, const Sched& S, const Epi& E) {
;     ...
;         if (!has_next) break;
; #pragma unroll
;         for (int a = 0; a < 2; ++a)
; #pragma unroll
;             for (int b = 0; b < 2; ++b)
; #pragma unroll
;                 for (int m = 0; m < 4; ++m)
; #pragma unroll
;                     for (int n = 0; n < 2; ++n) acc[a][b][m][n] = (f32x4){0.f, 0.f, 0.f, 0.f};
;         cur = nxt; cA = nA; cB = nB; ++ui;
.LBB0_1224:
	s_add_u32 s28, s28, 0xb0080
	s_addc_u32 s29, s29, 0
	s_add_u32 s70, s30, 0x100
	v_mov_b32_e32 v34, 0
	s_addc_u32 s71, s31, 0
	s_mov_b32 s72, -2
	v_mov_b32_e32 v35, v34
	v_mov_b32_e32 v36, v34
	v_mov_b32_e32 v37, v34
	v_mov_b32_e32 v38, v34
	v_mov_b32_e32 v39, v34
	v_mov_b32_e32 v40, v34
	v_mov_b32_e32 v41, v34
	v_mov_b32_e32 v50, v34
	v_mov_b32_e32 v51, v34
	v_mov_b32_e32 v52, v34
	v_mov_b32_e32 v53, v34
	v_mov_b32_e32 v54, v34
	v_mov_b32_e32 v55, v34
	v_mov_b32_e32 v56, v34
	v_mov_b32_e32 v57, v34
	v_mov_b32_e32 v66, v34
	v_mov_b32_e32 v67, v34
	v_mov_b32_e32 v68, v34
	v_mov_b32_e32 v69, v34
	v_mov_b32_e32 v70, v34
	v_mov_b32_e32 v71, v34
	v_mov_b32_e32 v72, v34
	v_mov_b32_e32 v73, v34
	v_mov_b32_e32 v82, v34
	v_mov_b32_e32 v83, v34
	v_mov_b32_e32 v84, v34
	v_mov_b32_e32 v85, v34
	v_mov_b32_e32 v86, v34
	v_mov_b32_e32 v87, v34
	v_mov_b32_e32 v88, v34
	v_mov_b32_e32 v89, v34
	v_mov_b32_e32 v42, v34
	v_mov_b32_e32 v43, v34
	v_mov_b32_e32 v44, v34
	v_mov_b32_e32 v45, v34
	v_mov_b32_e32 v46, v34
	v_mov_b32_e32 v47, v34
	v_mov_b32_e32 v48, v34
	v_mov_b32_e32 v49, v34
	v_mov_b32_e32 v58, v34
	v_mov_b32_e32 v59, v34
	v_mov_b32_e32 v60, v34
	v_mov_b32_e32 v61, v34
	v_mov_b32_e32 v62, v34
	v_mov_b32_e32 v63, v34
	v_mov_b32_e32 v64, v34
	v_mov_b32_e32 v65, v34
	v_mov_b32_e32 v74, v34
	v_mov_b32_e32 v75, v34
	v_mov_b32_e32 v76, v34
	v_mov_b32_e32 v77, v34
	v_mov_b32_e32 v78, v34
	v_mov_b32_e32 v79, v34
	v_mov_b32_e32 v80, v34
	v_mov_b32_e32 v81, v34
	v_mov_b32_e32 v90, v34
	v_mov_b32_e32 v91, v34
	v_mov_b32_e32 v92, v34
	v_mov_b32_e32 v93, v34
	v_mov_b32_e32 v94, v34
	v_mov_b32_e32 v95, v34
	v_mov_b32_e32 v96, v34
	v_mov_b32_e32 v97, v34
	v_mov_b32_e32 v98, v34
	v_mov_b32_e32 v99, v34
	v_mov_b32_e32 v100, v34
	v_mov_b32_e32 v101, v34
	v_mov_b32_e32 v102, v34
	v_mov_b32_e32 v103, v34
	v_mov_b32_e32 v104, v34
	v_mov_b32_e32 v105, v34
	v_mov_b32_e32 v114, v34
	v_mov_b32_e32 v115, v34
	v_mov_b32_e32 v116, v34
	v_mov_b32_e32 v117, v34
	v_mov_b32_e32 v118, v34
	v_mov_b32_e32 v119, v34
	v_mov_b32_e32 v120, v34
	v_mov_b32_e32 v121, v34
	v_mov_b32_e32 v130, v34
	v_mov_b32_e32 v131, v34
	v_mov_b32_e32 v132, v34
	v_mov_b32_e32 v133, v34
	v_mov_b32_e32 v134, v34
	v_mov_b32_e32 v135, v34
	v_mov_b32_e32 v136, v34
	v_mov_b32_e32 v137, v34
	v_mov_b32_e32 v146, v34
	v_mov_b32_e32 v147, v34
	v_mov_b32_e32 v148, v34
	v_mov_b32_e32 v149, v34
	v_mov_b32_e32 v150, v34
	v_mov_b32_e32 v151, v34
	v_mov_b32_e32 v152, v34
	v_mov_b32_e32 v153, v34
	v_mov_b32_e32 v106, v34
	v_mov_b32_e32 v107, v34
	v_mov_b32_e32 v108, v34
	v_mov_b32_e32 v109, v34
	v_mov_b32_e32 v110, v34
	v_mov_b32_e32 v111, v34
	v_mov_b32_e32 v112, v34
	v_mov_b32_e32 v113, v34
	v_mov_b32_e32 v122, v34
	v_mov_b32_e32 v123, v34
	v_mov_b32_e32 v124, v34
	v_mov_b32_e32 v125, v34
	v_mov_b32_e32 v126, v34
	v_mov_b32_e32 v127, v34
	v_mov_b32_e32 v128, v34
	v_mov_b32_e32 v129, v34
	v_mov_b32_e32 v138, v34
	v_mov_b32_e32 v139, v34
	v_mov_b32_e32 v140, v34
	v_mov_b32_e32 v141, v34
	v_mov_b32_e32 v142, v34
	v_mov_b32_e32 v143, v34
	v_mov_b32_e32 v144, v34
	v_mov_b32_e32 v145, v34
	v_mov_b32_e32 v154, v34
	v_mov_b32_e32 v155, v34
	v_mov_b32_e32 v156, v34
	v_mov_b32_e32 v157, v34
	v_mov_b32_e32 v158, v34
	v_mov_b32_e32 v159, v34
	v_mov_b32_e32 v160, v34
	v_mov_b32_e32 v161, v34
	s_branch .LBB0_1225

; #define PG8_STAGE(bufoff, gbase, voff) do { _Pragma("unroll") for (int _i = 0; _i < 2; ++_i) \
;         __builtin_amdgcn_global_load_lds((const unsigned*)((const char*)(gbase) + (voff)[_i]), (PG8_LAS unsigned*)(lds + (bufoff) + ldsw + _i * 8192), 16, 0, 0); } while (0)
; #define PG8_LDA(dst, b, h) do { _Pragma("unroll") for (int m = 0; m < 4; ++m) _Pragma("unroll") for (int k = 0; k < 2; ++k) dst[m][k] = *(const PG8_LAS bf16x8*)(lds + PG8_SA(b, h) + aoff + m * 2048 + k * 1024); } while (0)
; #define PG8_LDB(dst, b, h) do { _Pragma("unroll") for (int n = 0; n < 2; ++n) _Pragma("unroll") for (int k = 0; k < 2; ++k) dst[n][k] = *(const PG8_LAS bf16x8*)(lds + PG8_SB(b, h) + boff + n * 2048 + k * 1024); } while (0)
; #define PG8_WAIT_V(n) asm volatile("s_waitcnt vmcnt(" #n ")" ::: "memory")
; #define PG8_WAIT_L(n) asm volatile("s_waitcnt lgkmcnt(" #n ")" ::: "memory")
; #define PG8_BAR __builtin_amdgcn_s_barrier()
; #define PG8_SCHED __builtin_amdgcn_sched_barrier(0)
; template <class Epi, class Sched, bool ALIGN_EPI = false, bool SP2 = false, bool FP8 = false>
; __device__ __forceinline__ void gemm_phase(PG8_LAS unsigned char* lds, const Gemm g, const Sched& S, const Epi& E) {
;     ...
;             PG8_LDB(B0, 0, 0); PG8_LDB(B1, 0, 1); PG8_SCHED; PG8_LDA(At, 0, 0); PG8_STAGE(PG8_SA(1, 1), a1 + hstep, voffA);
;             PG8_WAIT_V(8); PG8_WAIT_L(0); PG8_BAR; PG8_MMA(0, 0, At, B0); PG8_MMA(0, 1, At, B1); PG8_BAR; PG8_SCHED;
;             PG8_LDA(At, 0, 1); PG8_STAGE(PG8_SB(0, 0), b2, voffB); PG8_STAGE(PG8_SB(0, 1), b2 + hstep, voffB); PG8_STAGE(PG8_SA(0, 0), a2, voffA);
;             PG8_WAIT_V(8); PG8_WAIT_L(0); PG8_BAR; PG8_MMA(1, 0, At, B0); PG8_MMA(1, 1, At, B1); PG8_BAR; PG8_SCHED;
.LBB0_1225:
	ds_read_b128 v[26:29], v190
	ds_read_b128 v[30:33], v190 offset:1024
	ds_read_b128 v[18:21], v190 offset:2048
	ds_read_b128 v[22:25], v190 offset:3072
	ds_read_b128 v[10:13], v191
	ds_read_b128 v[14:17], v191 offset:1024
	ds_read_b128 v[2:5], v191 offset:2048
	ds_read_b128 v[6:9], v191 offset:3072
	s_add_u32 s30, s28, 0xfff50080
	s_addc_u32 s31, s29, -1
	s_cmp_eq_u32 s72, 40
	s_cselect_b32 s35, s9, s31
	s_cselect_b32 s34, s8, s30
	s_cselect_b32 s31, s27, s71
	s_cselect_b32 s30, s26, s70
	v_lshl_add_u64 v[186:187], s[28:29], 0, v[170:171]
	s_add_i32 m0, s39, 0xc000
	ds_read_b128 v[178:181], v192
	ds_read_b128 v[182:185], v192 offset:1024
	ds_read_b128 v[194:197], v192 offset:2048
	ds_read_b128 v[198:201], v192 offset:3072
	ds_read_b128 v[202:205], v192 offset:4096
	ds_read_b128 v[206:209], v192 offset:5120
	ds_read_b128 v[210:213], v192 offset:6144
	ds_read_b128 v[214:217], v192 offset:7168
	global_load_lds_dwordx4 v[186:187], off
	v_lshl_add_u64 v[186:187], s[28:29], 0, v[172:173]
	s_add_i32 m0, s39, 0xe000
	s_nop 0
	global_load_lds_dwordx4 v[186:187], off
	s_waitcnt vmcnt(8)
	s_waitcnt lgkmcnt(0)
	s_barrier
	s_setprio 1
	s_waitcnt lgkmcnt(0)
	v_mfma_f32_16x16x128_f8f6f4 v[158:161], v[26:33], v[178:185], v[158:161]
	v_mfma_f32_16x16x128_f8f6f4 v[154:157], v[18:25], v[178:185], v[154:157]
	v_mfma_f32_16x16x128_f8f6f4 v[142:145], v[26:33], v[194:201], v[142:145]
	v_mfma_f32_16x16x128_f8f6f4 v[138:141], v[18:25], v[194:201], v[138:141]
	v_mfma_f32_16x16x128_f8f6f4 v[126:129], v[26:33], v[202:209], v[126:129]
	v_mfma_f32_16x16x128_f8f6f4 v[122:125], v[18:25], v[202:209], v[122:125]
	v_mfma_f32_16x16x128_f8f6f4 v[110:113], v[26:33], v[210:217], v[110:113]
	v_mfma_f32_16x16x128_f8f6f4 v[106:109], v[18:25], v[210:217], v[106:109]
	s_setprio 0
	s_setprio 1
	v_mfma_f32_16x16x128_f8f6f4 v[150:153], v[10:17], v[178:185], v[150:153]
	v_mfma_f32_16x16x128_f8f6f4 v[146:149], v[2:9], v[178:185], v[146:149]
	v_mfma_f32_16x16x128_f8f6f4 v[134:137], v[10:17], v[194:201], v[134:137]
	v_mfma_f32_16x16x128_f8f6f4 v[130:133], v[2:9], v[194:201], v[130:133]
	v_mfma_f32_16x16x128_f8f6f4 v[118:121], v[10:17], v[202:209], v[118:121]
	v_mfma_f32_16x16x128_f8f6f4 v[114:117], v[2:9], v[202:209], v[114:117]
	v_mfma_f32_16x16x128_f8f6f4 v[102:105], v[10:17], v[210:217], v[102:105]
	v_mfma_f32_16x16x128_f8f6f4 v[98:101], v[2:9], v[210:217], v[98:101]
	s_setprio 0
	s_barrier
	s_add_i32 s73, s56, s38
	v_lshl_add_u64 v[178:179], s[30:31], 0, v[164:165]
	s_mov_b32 m0, s73
	ds_read_b128 v[194:197], v192 offset:16384
	ds_read_b128 v[198:201], v192 offset:17408
	ds_read_b128 v[202:205], v192 offset:18432
	ds_read_b128 v[206:209], v192 offset:19456
	ds_read_b128 v[210:213], v192 offset:20480
	ds_read_b128 v[214:217], v192 offset:21504
	ds_read_b128 v[218:221], v192 offset:22528
	ds_read_b128 v[222:225], v192 offset:23552
	global_load_lds_dwordx4 v[178:179], off
	s_add_i32 m0, s73, 0x2000
	s_add_u32 s74, s30, 0xb0000
	v_lshl_add_u64 v[180:181], s[30:31], 0, v[168:169]
	s_addc_u32 s75, s31, 0
	s_add_i32 s73, s57, s38
	global_load_lds_dwordx4 v[180:181], off
	v_lshl_add_u64 v[182:183], s[74:75], 0, v[164:165]
	s_mov_b32 m0, s73
	v_lshl_add_u64 v[184:185], s[34:35], 0, v[166:167]
	global_load_lds_dwordx4 v[182:183], off
	v_lshl_add_u64 v[182:183], s[74:75], 0, v[168:169]
	s_add_i32 m0, s73, 0x2000
	s_nop 0
	global_load_lds_dwordx4 v[182:183], off
	v_lshl_add_u64 v[182:183], s[34:35], 0, v[162:163]
	s_mov_b32 m0, s39
	s_nop 0
	global_load_lds_dwordx4 v[182:183], off
	s_mov_b32 m0, s40
	s_nop 0
	global_load_lds_dwordx4 v[184:185], off
	s_waitcnt vmcnt(8)
	s_waitcnt lgkmcnt(0)
	s_barrier
	s_setprio 1
	s_waitcnt lgkmcnt(0)
	v_mfma_f32_16x16x128_f8f6f4 v[94:97], v[26:33], v[194:201], v[94:97]
	v_mfma_f32_16x16x128_f8f6f4 v[90:93], v[18:25], v[194:201], v[90:93]
	v_mfma_f32_16x16x128_f8f6f4 v[78:81], v[26:33], v[202:209], v[78:81]
	v_mfma_f32_16x16x128_f8f6f4 v[74:77], v[18:25], v[202:209], v[74:77]
	v_mfma_f32_16x16x128_f8f6f4 v[62:65], v[26:33], v[210:217], v[62:65]
	v_mfma_f32_16x16x128_f8f6f4 v[58:61], v[18:25], v[210:217], v[58:61]
	v_mfma_f32_16x16x128_f8f6f4 v[46:49], v[26:33], v[218:225], v[46:49]
	v_mfma_f32_16x16x128_f8f6f4 v[42:45], v[18:25], v[218:225], v[42:45]
	s_setprio 0
	s_setprio 1
	v_mfma_f32_16x16x128_f8f6f4 v[86:89], v[10:17], v[194:201], v[86:89]
	v_mfma_f32_16x16x128_f8f6f4 v[82:85], v[2:9], v[194:201], v[82:85]
	v_mfma_f32_16x16x128_f8f6f4 v[70:73], v[10:17], v[202:209], v[70:73]
	v_mfma_f32_16x16x128_f8f6f4 v[66:69], v[2:9], v[202:209], v[66:69]
	v_mfma_f32_16x16x128_f8f6f4 v[54:57], v[10:17], v[210:217], v[54:57]
	v_mfma_f32_16x16x128_f8f6f4 v[50:53], v[2:9], v[210:217], v[50:53]
	v_mfma_f32_16x16x128_f8f6f4 v[38:41], v[10:17], v[218:225], v[38:41]
	v_mfma_f32_16x16x128_f8f6f4 v[34:37], v[2:9], v[218:225], v[34:37]
	s_setprio 0
	s_barrier
; #define PG8_STAGE(bufoff, gbase, voff) do { _Pragma("unroll") for (int _i = 0; _i < 2; ++_i) \
;         __builtin_amdgcn_global_load_lds((const unsigned*)((const char*)(gbase) + (voff)[_i]), (PG8_LAS unsigned*)(lds + (bufoff) + ldsw + _i * 8192), 16, 0, 0); } while (0)
; #define PG8_LDA(dst, b, h) do { _Pragma("unroll") for (int m = 0; m < 4; ++m) _Pragma("unroll") for (int k = 0; k < 2; ++k) dst[m][k] = *(const PG8_LAS bf16x8*)(lds + PG8_SA(b, h) + aoff + m * 2048 + k * 1024); } while (0)
; #define PG8_LDB(dst, b, h) do { _Pragma("unroll") for (int n = 0; n < 2; ++n) _Pragma("unroll") for (int k = 0; k < 2; ++k) dst[n][k] = *(const PG8_LAS bf16x8*)(lds + PG8_SB(b, h) + boff + n * 2048 + k * 1024); } while (0)
; #define PG8_WAIT_V(n) asm volatile("s_waitcnt vmcnt(" #n ")" ::: "memory")
; #define PG8_WAIT_L(n) asm volatile("s_waitcnt lgkmcnt(" #n ")" ::: "memory")
; #define PG8_BAR __builtin_amdgcn_s_barrier()
; #define PG8_SCHED __builtin_amdgcn_sched_barrier(0)
; template <class Epi, class Sched, bool ALIGN_EPI = false, bool SP2 = false, bool FP8 = false>
; __device__ __forceinline__ void gemm_phase(PG8_LAS unsigned char* lds, const Gemm g, const Sched& S, const Epi& E) {
;     ...
;             PG8_WAIT_V(8); PG8_WAIT_L(0); PG8_BAR; PG8_MMA(1, 0, At, B0); PG8_MMA(1, 1, At, B1); PG8_BAR; PG8_SCHED;
;             PG8_LDB(B0, 1, 0); PG8_LDB(B1, 1, 1); PG8_SCHED; PG8_LDA(At, 1, 0); PG8_STAGE(PG8_SA(0, 1), a2 + hstep, voffA);
;             PG8_WAIT_V(8); PG8_WAIT_L(0); PG8_BAR; PG8_MMA(0, 0, At, B0); PG8_MMA(0, 1, At, B1); PG8_BAR; PG8_SCHED;
;             PG8_LDA(At, 1, 1); PG8_STAGE(PG8_SB(1, 0), b3, voffB); PG8_STAGE(PG8_SB(1, 1), b3 + hstep, voffB); PG8_STAGE(PG8_SA(1, 0), a3, voffA);
;             PG8_WAIT_V(8); PG8_WAIT_L(0); PG8_BAR; PG8_MMA(1, 0, At, B0); PG8_MMA(1, 1, At, B1); PG8_BAR; PG8_SCHED;
;     ...
;         if constexpr (FP8) asm volatile("s_nop 15\n\ts_nop 15\n\ts_nop 15\n\ts_nop 15" ::: "memory");
;         if constexpr (ALIGN_EPI) { if (wr == 0) PG8_BAR; }
	s_add_i32 s73, 0, 0x18000
	s_add_i32 s74, 0, 0x1c000
	v_add_u32_e32 v14, s73, v188
	v_add_u32_e32 v30, s74, v188
	ds_read_b128 v[2:5], v14
	ds_read_b128 v[6:9], v14 offset:1024
	ds_read_b128 v[10:13], v14 offset:2048
	ds_read_b128 v[14:17], v14 offset:3072
	ds_read_b128 v[18:21], v30
	ds_read_b128 v[22:25], v30 offset:1024
	ds_read_b128 v[26:29], v30 offset:2048
	ds_read_b128 v[30:33], v30 offset:3072
	s_add_u32 s34, s34, 0xb0000
	s_addc_u32 s35, s35, 0
	s_mov_b32 m0, s41
	v_lshl_add_u64 v[186:187], s[34:35], 0, v[162:163]
	ds_read_b128 v[194:197], v192 offset:32768
	ds_read_b128 v[198:201], v192 offset:33792
	ds_read_b128 v[202:205], v192 offset:34816
	ds_read_b128 v[206:209], v192 offset:35840
	ds_read_b128 v[210:213], v192 offset:36864
	ds_read_b128 v[214:217], v192 offset:37888
	ds_read_b128 v[218:221], v192 offset:38912
	ds_read_b128 v[222:225], v192 offset:39936
	global_load_lds_dwordx4 v[186:187], off
	v_lshl_add_u64 v[186:187], s[34:35], 0, v[166:167]
	s_mov_b32 m0, s42
	s_nop 0
	global_load_lds_dwordx4 v[186:187], off
	s_waitcnt vmcnt(8)
	s_waitcnt lgkmcnt(0)
	s_barrier
	s_setprio 1
	s_waitcnt lgkmcnt(0)
	v_mfma_f32_16x16x128_f8f6f4 v[158:161], v[2:9], v[194:201], v[158:161]
	v_mfma_f32_16x16x128_f8f6f4 v[154:157], v[10:17], v[194:201], v[154:157]
	v_mfma_f32_16x16x128_f8f6f4 v[142:145], v[2:9], v[202:209], v[142:145]
	v_mfma_f32_16x16x128_f8f6f4 v[138:141], v[10:17], v[202:209], v[138:141]
	v_mfma_f32_16x16x128_f8f6f4 v[126:129], v[2:9], v[210:217], v[126:129]
	v_mfma_f32_16x16x128_f8f6f4 v[122:125], v[10:17], v[210:217], v[122:125]
	v_mfma_f32_16x16x128_f8f6f4 v[110:113], v[2:9], v[218:225], v[110:113]
	v_mfma_f32_16x16x128_f8f6f4 v[106:109], v[10:17], v[218:225], v[106:109]
	s_setprio 0
	s_setprio 1
	v_mfma_f32_16x16x128_f8f6f4 v[150:153], v[18:25], v[194:201], v[150:153]
	v_mfma_f32_16x16x128_f8f6f4 v[146:149], v[26:33], v[194:201], v[146:149]
	v_mfma_f32_16x16x128_f8f6f4 v[134:137], v[18:25], v[202:209], v[134:137]
	v_mfma_f32_16x16x128_f8f6f4 v[130:133], v[26:33], v[202:209], v[130:133]
	v_mfma_f32_16x16x128_f8f6f4 v[118:121], v[18:25], v[210:217], v[118:121]
	v_mfma_f32_16x16x128_f8f6f4 v[114:117], v[26:33], v[210:217], v[114:117]
	v_mfma_f32_16x16x128_f8f6f4 v[102:105], v[18:25], v[218:225], v[102:105]
	v_mfma_f32_16x16x128_f8f6f4 v[98:101], v[26:33], v[218:225], v[98:101]
	s_setprio 0
	s_barrier
	s_add_i32 s34, s73, s38
	v_lshl_add_u64 v[178:179], v[178:179], 0, s[12:13]
	s_mov_b32 m0, s34
	ds_read_b128 v[194:197], v192 offset:49152
	ds_read_b128 v[198:201], v192 offset:50176
	ds_read_b128 v[202:205], v192 offset:51200
	ds_read_b128 v[206:209], v192 offset:52224
	ds_read_b128 v[210:213], v192 offset:53248
	ds_read_b128 v[214:217], v192 offset:54272
	ds_read_b128 v[218:221], v192 offset:55296
	ds_read_b128 v[222:225], v192 offset:56320
	global_load_lds_dwordx4 v[178:179], off
	s_add_i32 m0, s34, 0x2000
	s_add_u32 s30, s30, 0xb0080
	v_lshl_add_u64 v[178:179], v[180:181], 0, s[12:13]
	s_addc_u32 s31, s31, 0
	s_add_i32 s34, s74, s38
	global_load_lds_dwordx4 v[178:179], off
	v_lshl_add_u64 v[178:179], s[30:31], 0, v[164:165]
	s_mov_b32 m0, s34
	s_nop 0
	global_load_lds_dwordx4 v[178:179], off
	v_lshl_add_u64 v[178:179], s[30:31], 0, v[168:169]
	s_add_i32 m0, s34, 0x2000
	s_nop 0
	global_load_lds_dwordx4 v[178:179], off
	v_lshl_add_u64 v[178:179], v[182:183], 0, s[12:13]
	s_mov_b32 m0, s47
	s_nop 0
	global_load_lds_dwordx4 v[178:179], off
	v_lshl_add_u64 v[178:179], v[184:185], 0, s[12:13]
	s_mov_b32 m0, s48
	s_nop 0
	global_load_lds_dwordx4 v[178:179], off
	s_waitcnt vmcnt(8)
	s_waitcnt lgkmcnt(0)
	s_barrier
	s_setprio 1
	s_waitcnt lgkmcnt(0)
	v_mfma_f32_16x16x128_f8f6f4 v[94:97], v[2:9], v[194:201], v[94:97]
	v_mfma_f32_16x16x128_f8f6f4 v[90:93], v[10:17], v[194:201], v[90:93]
	v_mfma_f32_16x16x128_f8f6f4 v[78:81], v[2:9], v[202:209], v[78:81]
	v_mfma_f32_16x16x128_f8f6f4 v[74:77], v[10:17], v[202:209], v[74:77]
	v_mfma_f32_16x16x128_f8f6f4 v[62:65], v[2:9], v[210:217], v[62:65]
	v_mfma_f32_16x16x128_f8f6f4 v[58:61], v[10:17], v[210:217], v[58:61]
	v_mfma_f32_16x16x128_f8f6f4 v[46:49], v[2:9], v[218:225], v[46:49]
	v_mfma_f32_16x16x128_f8f6f4 v[42:45], v[10:17], v[218:225], v[42:45]
	s_setprio 0
	s_setprio 1
	v_mfma_f32_16x16x128_f8f6f4 v[86:89], v[18:25], v[194:201], v[86:89]
	v_mfma_f32_16x16x128_f8f6f4 v[82:85], v[26:33], v[194:201], v[82:85]
	v_mfma_f32_16x16x128_f8f6f4 v[70:73], v[18:25], v[202:209], v[70:73]
	v_mfma_f32_16x16x128_f8f6f4 v[66:69], v[26:33], v[202:209], v[66:69]
	v_mfma_f32_16x16x128_f8f6f4 v[54:57], v[18:25], v[210:217], v[54:57]
	v_mfma_f32_16x16x128_f8f6f4 v[50:53], v[26:33], v[210:217], v[50:53]
	v_mfma_f32_16x16x128_f8f6f4 v[38:41], v[18:25], v[218:225], v[38:41]
	v_mfma_f32_16x16x128_f8f6f4 v[34:37], v[26:33], v[218:225], v[34:37]
	s_setprio 0
	s_add_i32 s72, s72, 2
	s_add_u32 s28, s28, 0x100
	s_addc_u32 s29, s29, 0
	s_add_u32 s70, s70, 0x100
	s_addc_u32 s71, s71, 0
	s_cmp_gt_u32 s72, 41
	s_cbranch_scc0 .Lrot_head_1225
	s_barrier
	s_nop 15
	s_nop 15
	s_nop 15
	s_nop 15
	s_and_b64 vcc, exec, s[14:15]
	s_cbranch_vccz .LBB0_1228
	s_barrier

; template <class Epi, class Sched, bool ALIGN_EPI = false, bool SP2 = false, bool FP8 = false>
; __device__ __forceinline__ void gemm_phase(PG8_LAS unsigned char* lds, const Gemm g, const Sched& S, const Epi& E) {
;     ...
;         const bool has_next = S.next(ui + 1, nxt);
;         const char* nA = has_next ? (const char*)g.A + (size_t)nxt.pm * tstep : cA; const char* nB = has_next ? (const char*)g.Bt + (size_t)nxt.pb * tstep : cB;
;         for (int t = 0; t < nt; t += 2) {
;             const bool last = (t == nt - 2);
;             const char* a1 = cA + (size_t)(t + 1) * kstep;
;             const char* a2 = last ? nA : cA + (size_t)(t + 2) * kstep; const char* b2 = last ? nB : cB + (size_t)(t + 2) * kstep;
;             const char* a3 = a2 + kstep; const char* b3 = b2 + kstep;
;     ...
;         if (!has_next) break;
; #pragma unroll
;         for (int a = 0; a < 2; ++a)
; #pragma unroll
;             for (int b = 0; b < 2; ++b)
; #pragma unroll
;                 for (int m = 0; m < 4; ++m)
; #pragma unroll
;                     for (int n = 0; n < 2; ++n) acc[a][b][m][n] = (f32x4){0.f, 0.f, 0.f, 0.f};
;         cur = nxt; cA = nA; cB = nB; ++ui;
.LBB0_1357:
	s_ashr_i32 s17, s16, 31
	s_lshl_b64 s[18:19], s[16:17], 20
	s_add_u32 s18, s30, s18
	s_addc_u32 s19, s31, s19
	s_and_b64 s[20:21], s[6:7], exec
	s_cselect_b32 s17, s19, s25
	s_cselect_b32 s56, s18, s24
	s_ashr_i32 s15, s14, 31
	s_lshl_b64 s[20:21], s[14:15], 20
	s_add_u32 s20, s33, s20
	s_addc_u32 s21, s34, s21
	s_and_b64 s[28:29], s[6:7], exec
	s_cselect_b32 s15, s21, s27
	s_cselect_b32 s57, s20, s26
	s_add_u32 s24, s24, 0x80080
	s_addc_u32 s25, s25, 0
	s_add_u32 s60, s26, 0x100
	v_mov_b32_e32 v2, 0
	s_addc_u32 s61, s27, 0
	s_mov_b32 s62, -2
	v_mov_b32_e32 v3, v2
	v_mov_b32_e32 v4, v2
	v_mov_b32_e32 v5, v2
	v_mov_b32_e32 v6, v2
	v_mov_b32_e32 v7, v2
	v_mov_b32_e32 v8, v2
	v_mov_b32_e32 v9, v2
	v_mov_b32_e32 v10, v2
	v_mov_b32_e32 v11, v2
	v_mov_b32_e32 v12, v2
	v_mov_b32_e32 v13, v2
	v_mov_b32_e32 v18, v2
	v_mov_b32_e32 v19, v2
	v_mov_b32_e32 v20, v2
	v_mov_b32_e32 v21, v2
	v_mov_b32_e32 v26, v2
	v_mov_b32_e32 v27, v2
	v_mov_b32_e32 v28, v2
	v_mov_b32_e32 v29, v2
	v_mov_b32_e32 v34, v2
	v_mov_b32_e32 v35, v2
	v_mov_b32_e32 v36, v2
	v_mov_b32_e32 v37, v2
	v_mov_b32_e32 v42, v2
	v_mov_b32_e32 v43, v2
	v_mov_b32_e32 v44, v2
	v_mov_b32_e32 v45, v2
	v_mov_b32_e32 v50, v2
	v_mov_b32_e32 v51, v2
	v_mov_b32_e32 v52, v2
	v_mov_b32_e32 v53, v2
	v_mov_b32_e32 v14, v2
	v_mov_b32_e32 v15, v2
	v_mov_b32_e32 v16, v2
	v_mov_b32_e32 v17, v2
	v_mov_b32_e32 v22, v2
	v_mov_b32_e32 v23, v2
	v_mov_b32_e32 v24, v2
	v_mov_b32_e32 v25, v2
	v_mov_b32_e32 v30, v2
	v_mov_b32_e32 v31, v2
	v_mov_b32_e32 v32, v2
	v_mov_b32_e32 v33, v2
	v_mov_b32_e32 v38, v2
	v_mov_b32_e32 v39, v2
	v_mov_b32_e32 v40, v2
	v_mov_b32_e32 v41, v2
	v_mov_b32_e32 v46, v2
	v_mov_b32_e32 v47, v2
	v_mov_b32_e32 v48, v2
	v_mov_b32_e32 v49, v2
	v_mov_b32_e32 v54, v2
	v_mov_b32_e32 v55, v2
	v_mov_b32_e32 v56, v2
	v_mov_b32_e32 v57, v2
	v_mov_b32_e32 v58, v2
	v_mov_b32_e32 v59, v2
	v_mov_b32_e32 v60, v2
	v_mov_b32_e32 v61, v2
	v_mov_b32_e32 v62, v2
	v_mov_b32_e32 v63, v2
	v_mov_b32_e32 v64, v2
	v_mov_b32_e32 v65, v2
	v_mov_b32_e32 v66, v2
	v_mov_b32_e32 v67, v2
	v_mov_b32_e32 v68, v2
	v_mov_b32_e32 v69, v2
	v_mov_b32_e32 v70, v2
	v_mov_b32_e32 v71, v2
	v_mov_b32_e32 v72, v2
	v_mov_b32_e32 v73, v2
	v_mov_b32_e32 v74, v2
	v_mov_b32_e32 v75, v2
	v_mov_b32_e32 v76, v2
	v_mov_b32_e32 v77, v2
	v_mov_b32_e32 v82, v2
	v_mov_b32_e32 v83, v2
	v_mov_b32_e32 v84, v2
	v_mov_b32_e32 v85, v2
	v_mov_b32_e32 v90, v2
	v_mov_b32_e32 v91, v2
	v_mov_b32_e32 v92, v2
	v_mov_b32_e32 v93, v2
	v_mov_b32_e32 v98, v2
	v_mov_b32_e32 v99, v2
	v_mov_b32_e32 v100, v2
	v_mov_b32_e32 v101, v2
	v_mov_b32_e32 v106, v2
	v_mov_b32_e32 v107, v2
	v_mov_b32_e32 v108, v2
	v_mov_b32_e32 v109, v2
	v_mov_b32_e32 v114, v2
	v_mov_b32_e32 v115, v2
	v_mov_b32_e32 v116, v2
	v_mov_b32_e32 v117, v2
	v_mov_b32_e32 v78, v2
	v_mov_b32_e32 v79, v2
	v_mov_b32_e32 v80, v2
	v_mov_b32_e32 v81, v2
	v_mov_b32_e32 v86, v2
	v_mov_b32_e32 v87, v2
	v_mov_b32_e32 v88, v2
	v_mov_b32_e32 v89, v2
	v_mov_b32_e32 v94, v2
	v_mov_b32_e32 v95, v2
	v_mov_b32_e32 v96, v2
	v_mov_b32_e32 v97, v2
	v_mov_b32_e32 v102, v2
	v_mov_b32_e32 v103, v2
	v_mov_b32_e32 v104, v2
	v_mov_b32_e32 v105, v2
	v_mov_b32_e32 v110, v2
	v_mov_b32_e32 v111, v2
	v_mov_b32_e32 v112, v2
	v_mov_b32_e32 v113, v2
	v_mov_b32_e32 v118, v2
	v_mov_b32_e32 v119, v2
	v_mov_b32_e32 v120, v2
	v_mov_b32_e32 v121, v2
	v_mov_b32_e32 v122, v2
	v_mov_b32_e32 v123, v2
	v_mov_b32_e32 v124, v2
	v_mov_b32_e32 v125, v2
	v_mov_b32_e32 v126, v2
	v_mov_b32_e32 v127, v2
	v_mov_b32_e32 v128, v2
	v_mov_b32_e32 v129, v2
	s_branch .LBB0_1358

; #define PG8_STAGE(bufoff, gbase, voff) do { _Pragma("unroll") for (int _i = 0; _i < 2; ++_i) \
;         __builtin_amdgcn_global_load_lds((const unsigned*)((const char*)(gbase) + (voff)[_i]), (PG8_LAS unsigned*)(lds + (bufoff) + ldsw + _i * 8192), 16, 0, 0); } while (0)
; #define PG8_LDA(dst, b, h) do { _Pragma("unroll") for (int m = 0; m < 4; ++m) _Pragma("unroll") for (int k = 0; k < 2; ++k) dst[m][k] = *(const PG8_LAS bf16x8*)(lds + PG8_SA(b, h) + aoff + m * 2048 + k * 1024); } while (0)
; #define PG8_LDB(dst, b, h) do { _Pragma("unroll") for (int n = 0; n < 2; ++n) _Pragma("unroll") for (int k = 0; k < 2; ++k) dst[n][k] = *(const PG8_LAS bf16x8*)(lds + PG8_SB(b, h) + boff + n * 2048 + k * 1024); } while (0)
; #define PG8_WAIT_V(n) asm volatile("s_waitcnt vmcnt(" #n ")" ::: "memory")
; #define PG8_WAIT_L(n) asm volatile("s_waitcnt lgkmcnt(" #n ")" ::: "memory")
; #define PG8_BAR __builtin_amdgcn_s_barrier()
; #define PG8_SCHED __builtin_amdgcn_sched_barrier(0)
; template <class Epi, class Sched, bool ALIGN_EPI = false, bool SP2 = false, bool FP8 = false>
; __device__ __forceinline__ void gemm_phase(PG8_LAS unsigned char* lds, const Gemm g, const Sched& S, const Epi& E) {
;     ...
;             const bool last = (t == nt - 2);
;             const char* a1 = cA + (size_t)(t + 1) * kstep;
;             const char* a2 = last ? nA : cA + (size_t)(t + 2) * kstep; const char* b2 = last ? nB : cB + (size_t)(t + 2) * kstep;
;             const char* a3 = a2 + kstep; const char* b3 = b2 + kstep;
;             if (last && has_next) S.a_ready(nxt);
;             if constexpr (SP2) {
;             PG8_LDB(B0, 0, 0); PG8_LDB(B1, 0, 1); PG8_SCHED; PG8_LDA(At, 0, 0); PG8_STAGE(PG8_SA(1, 1), a1 + hstep, voffA);
;             PG8_WAIT_V(8); PG8_WAIT_L(0); PG8_BAR; PG8_MMA(0, 0, At, B0); PG8_MMA(0, 1, At, B1); PG8_BAR; PG8_SCHED;
;             PG8_LDA(At, 0, 1); PG8_STAGE(PG8_SB(0, 0), b2, voffB); PG8_STAGE(PG8_SB(0, 1), b2 + hstep, voffB); PG8_STAGE(PG8_SA(0, 0), a2, voffA);
.LBB0_1358:
	ds_read_b128 v[146:149], v152
	ds_read_b128 v[156:159], v152 offset:1024
	ds_read_b128 v[160:163], v152 offset:2048
	ds_read_b128 v[164:167], v152 offset:3072
	ds_read_b128 v[168:171], v153
	ds_read_b128 v[172:175], v153 offset:1024
	ds_read_b128 v[176:179], v153 offset:2048
	ds_read_b128 v[180:183], v153 offset:3072
	s_add_u32 s26, s24, 0xfff80080
	s_addc_u32 s27, s25, -1
	s_cmp_eq_u32 s62, 28
	s_cselect_b32 s29, s17, s27
	s_cselect_b32 s28, s56, s26
	s_cselect_b32 s27, s15, s61
	s_cselect_b32 s26, s57, s60
	v_lshl_add_u64 v[216:217], s[24:25], 0, v[138:139]
	s_add_i32 m0, s23, 0xc000
	ds_read_b128 v[184:187], v154
	ds_read_b128 v[188:191], v154 offset:1024
	ds_read_b128 v[192:195], v154 offset:2048
	ds_read_b128 v[196:199], v154 offset:3072
	ds_read_b128 v[200:203], v154 offset:4096
	ds_read_b128 v[204:207], v154 offset:5120
	ds_read_b128 v[208:211], v154 offset:6144
	ds_read_b128 v[212:215], v154 offset:7168
	global_load_lds_dwordx4 v[216:217], off
	v_lshl_add_u64 v[216:217], s[24:25], 0, v[140:141]
	s_add_i32 m0, s23, 0xe000
	s_nop 0
	global_load_lds_dwordx4 v[216:217], off
	s_waitcnt vmcnt(8)
	s_waitcnt lgkmcnt(0)
	s_barrier
	s_setprio 1
	s_waitcnt lgkmcnt(0)
	v_mfma_f32_16x16x32_bf16 v[126:129], v[146:149], v[184:187], v[126:129]
	v_mfma_f32_16x16x32_bf16 v[122:125], v[160:163], v[184:187], v[122:125]
	v_mfma_f32_16x16x32_bf16 v[118:121], v[146:149], v[192:195], v[118:121]
	v_mfma_f32_16x16x32_bf16 v[110:113], v[160:163], v[192:195], v[110:113]
	v_mfma_f32_16x16x32_bf16 v[102:105], v[146:149], v[200:203], v[102:105]
	v_mfma_f32_16x16x32_bf16 v[94:97], v[160:163], v[200:203], v[94:97]
	v_mfma_f32_16x16x32_bf16 v[86:89], v[146:149], v[208:211], v[86:89]
	v_mfma_f32_16x16x32_bf16 v[78:81], v[160:163], v[208:211], v[78:81]
	v_mfma_f32_16x16x32_bf16 v[126:129], v[156:159], v[188:191], v[126:129]
	v_mfma_f32_16x16x32_bf16 v[122:125], v[164:167], v[188:191], v[122:125]
	v_mfma_f32_16x16x32_bf16 v[118:121], v[156:159], v[196:199], v[118:121]
	v_mfma_f32_16x16x32_bf16 v[110:113], v[164:167], v[196:199], v[110:113]
	v_mfma_f32_16x16x32_bf16 v[102:105], v[156:159], v[204:207], v[102:105]
	v_mfma_f32_16x16x32_bf16 v[94:97], v[164:167], v[204:207], v[94:97]
	v_mfma_f32_16x16x32_bf16 v[86:89], v[156:159], v[212:215], v[86:89]
	v_mfma_f32_16x16x32_bf16 v[78:81], v[164:167], v[212:215], v[78:81]
	s_setprio 0
	s_setprio 1
	v_mfma_f32_16x16x32_bf16 v[114:117], v[168:171], v[184:187], v[114:117]
	v_mfma_f32_16x16x32_bf16 v[106:109], v[176:179], v[184:187], v[106:109]
	v_mfma_f32_16x16x32_bf16 v[98:101], v[168:171], v[192:195], v[98:101]
	v_mfma_f32_16x16x32_bf16 v[90:93], v[176:179], v[192:195], v[90:93]
	v_mfma_f32_16x16x32_bf16 v[82:85], v[168:171], v[200:203], v[82:85]
	v_mfma_f32_16x16x32_bf16 v[74:77], v[176:179], v[200:203], v[74:77]
	v_mfma_f32_16x16x32_bf16 v[70:73], v[168:171], v[208:211], v[70:73]
	v_mfma_f32_16x16x32_bf16 v[66:69], v[176:179], v[208:211], v[66:69]
	v_mfma_f32_16x16x32_bf16 v[114:117], v[172:175], v[188:191], v[114:117]
	v_mfma_f32_16x16x32_bf16 v[106:109], v[180:183], v[188:191], v[106:109]
	v_mfma_f32_16x16x32_bf16 v[98:101], v[172:175], v[196:199], v[98:101]
	v_mfma_f32_16x16x32_bf16 v[90:93], v[180:183], v[196:199], v[90:93]
	v_mfma_f32_16x16x32_bf16 v[82:85], v[172:175], v[204:207], v[82:85]
	v_mfma_f32_16x16x32_bf16 v[74:77], v[180:183], v[204:207], v[74:77]
	v_mfma_f32_16x16x32_bf16 v[70:73], v[172:175], v[212:215], v[70:73]
	v_mfma_f32_16x16x32_bf16 v[66:69], v[180:183], v[212:215], v[66:69]
	s_setprio 0
	s_barrier
	s_add_i32 s63, s46, s35
	v_lshl_add_u64 v[216:217], s[26:27], 0, v[134:135]
	s_mov_b32 m0, s63
	ds_read_b128 v[184:187], v154 offset:16384
	ds_read_b128 v[188:191], v154 offset:17408
	ds_read_b128 v[192:195], v154 offset:18432
	ds_read_b128 v[196:199], v154 offset:19456
	ds_read_b128 v[200:203], v154 offset:20480
	ds_read_b128 v[204:207], v154 offset:21504
	ds_read_b128 v[208:211], v154 offset:22528
	ds_read_b128 v[212:215], v154 offset:23552
	global_load_lds_dwordx4 v[216:217], off
	s_add_i32 m0, s63, 0x2000
	s_add_u32 s68, s26, 0x80000
	v_lshl_add_u64 v[218:219], s[26:27], 0, v[130:131]
	s_addc_u32 s69, s27, 0
	s_add_i32 s63, s47, s35
	global_load_lds_dwordx4 v[218:219], off
	v_lshl_add_u64 v[220:221], s[68:69], 0, v[134:135]
	s_mov_b32 m0, s63
	v_lshl_add_u64 v[222:223], s[28:29], 0, v[132:133]
	global_load_lds_dwordx4 v[220:221], off
	v_lshl_add_u64 v[220:221], s[68:69], 0, v[130:131]
	s_add_i32 m0, s63, 0x2000
	s_nop 0
	global_load_lds_dwordx4 v[220:221], off
	v_lshl_add_u64 v[220:221], s[28:29], 0, v[136:137]
	s_mov_b32 m0, s23
	s_nop 0
	global_load_lds_dwordx4 v[220:221], off
	s_mov_b32 m0, s38
	s_nop 0
	global_load_lds_dwordx4 v[222:223], off
	s_waitcnt vmcnt(8)
	s_waitcnt lgkmcnt(0)
	s_barrier
; #define PG8_STAGE(bufoff, gbase, voff) do { _Pragma("unroll") for (int _i = 0; _i < 2; ++_i) \
;         __builtin_amdgcn_global_load_lds((const unsigned*)((const char*)(gbase) + (voff)[_i]), (PG8_LAS unsigned*)(lds + (bufoff) + ldsw + _i * 8192), 16, 0, 0); } while (0)
; #define PG8_LDA(dst, b, h) do { _Pragma("unroll") for (int m = 0; m < 4; ++m) _Pragma("unroll") for (int k = 0; k < 2; ++k) dst[m][k] = *(const PG8_LAS bf16x8*)(lds + PG8_SA(b, h) + aoff + m * 2048 + k * 1024); } while (0)
; #define PG8_LDB(dst, b, h) do { _Pragma("unroll") for (int n = 0; n < 2; ++n) _Pragma("unroll") for (int k = 0; k < 2; ++k) dst[n][k] = *(const PG8_LAS bf16x8*)(lds + PG8_SB(b, h) + boff + n * 2048 + k * 1024); } while (0)
; #define PG8_WAIT_V(n) asm volatile("s_waitcnt vmcnt(" #n ")" ::: "memory")
; #define PG8_WAIT_L(n) asm volatile("s_waitcnt lgkmcnt(" #n ")" ::: "memory")
; #define PG8_BAR __builtin_amdgcn_s_barrier()
; #define PG8_SCHED __builtin_amdgcn_sched_barrier(0)
; template <class Epi, class Sched, bool ALIGN_EPI = false, bool SP2 = false, bool FP8 = false>
; __device__ __forceinline__ void gemm_phase(PG8_LAS unsigned char* lds, const Gemm g, const Sched& S, const Epi& E) {
;     ...
;             PG8_WAIT_V(8); PG8_WAIT_L(0); PG8_BAR; PG8_MMA(0, 0, At, B0); PG8_MMA(0, 1, At, B1); PG8_BAR; PG8_SCHED;
;             PG8_LDA(At, 0, 1); PG8_STAGE(PG8_SB(0, 0), b2, voffB); PG8_STAGE(PG8_SB(0, 1), b2 + hstep, voffB); PG8_STAGE(PG8_SA(0, 0), a2, voffA);
;             PG8_WAIT_V(8); PG8_WAIT_L(0); PG8_BAR; PG8_MMA(1, 0, At, B0); PG8_MMA(1, 1, At, B1); PG8_BAR; PG8_SCHED;
;             PG8_LDB(B0, 1, 0); PG8_LDB(B1, 1, 1); PG8_SCHED; PG8_LDA(At, 1, 0); PG8_STAGE(PG8_SA(0, 1), a2 + hstep, voffA);
;             PG8_WAIT_V(8); PG8_WAIT_L(0); PG8_BAR; PG8_MMA(0, 0, At, B0); PG8_MMA(0, 1, At, B1); PG8_BAR; PG8_SCHED;
	s_setprio 1
	s_waitcnt lgkmcnt(0)
	v_mfma_f32_16x16x32_bf16 v[62:65], v[146:149], v[184:187], v[62:65]
	v_mfma_f32_16x16x32_bf16 v[58:61], v[160:163], v[184:187], v[58:61]
	v_mfma_f32_16x16x32_bf16 v[54:57], v[146:149], v[192:195], v[54:57]
	v_mfma_f32_16x16x32_bf16 v[46:49], v[160:163], v[192:195], v[46:49]
	v_mfma_f32_16x16x32_bf16 v[38:41], v[146:149], v[200:203], v[38:41]
	v_mfma_f32_16x16x32_bf16 v[30:33], v[160:163], v[200:203], v[30:33]
	v_mfma_f32_16x16x32_bf16 v[22:25], v[146:149], v[208:211], v[22:25]
	v_mfma_f32_16x16x32_bf16 v[14:17], v[160:163], v[208:211], v[14:17]
	v_mfma_f32_16x16x32_bf16 v[62:65], v[156:159], v[188:191], v[62:65]
	v_mfma_f32_16x16x32_bf16 v[58:61], v[164:167], v[188:191], v[58:61]
	v_mfma_f32_16x16x32_bf16 v[54:57], v[156:159], v[196:199], v[54:57]
	v_mfma_f32_16x16x32_bf16 v[46:49], v[164:167], v[196:199], v[46:49]
	v_mfma_f32_16x16x32_bf16 v[38:41], v[156:159], v[204:207], v[38:41]
	v_mfma_f32_16x16x32_bf16 v[30:33], v[164:167], v[204:207], v[30:33]
	v_mfma_f32_16x16x32_bf16 v[22:25], v[156:159], v[212:215], v[22:25]
	v_mfma_f32_16x16x32_bf16 v[14:17], v[164:167], v[212:215], v[14:17]
	s_setprio 0
	s_setprio 1
	v_mfma_f32_16x16x32_bf16 v[50:53], v[168:171], v[184:187], v[50:53]
	v_mfma_f32_16x16x32_bf16 v[42:45], v[176:179], v[184:187], v[42:45]
	v_mfma_f32_16x16x32_bf16 v[34:37], v[168:171], v[192:195], v[34:37]
	v_mfma_f32_16x16x32_bf16 v[26:29], v[176:179], v[192:195], v[26:29]
	v_mfma_f32_16x16x32_bf16 v[18:21], v[168:171], v[200:203], v[18:21]
	v_mfma_f32_16x16x32_bf16 v[10:13], v[176:179], v[200:203], v[10:13]
	v_mfma_f32_16x16x32_bf16 v[6:9], v[168:171], v[208:211], v[6:9]
	v_mfma_f32_16x16x32_bf16 v[2:5], v[176:179], v[208:211], v[2:5]
	v_mfma_f32_16x16x32_bf16 v[50:53], v[172:175], v[188:191], v[50:53]
	v_mfma_f32_16x16x32_bf16 v[42:45], v[180:183], v[188:191], v[42:45]
	v_mfma_f32_16x16x32_bf16 v[34:37], v[172:175], v[196:199], v[34:37]
	v_mfma_f32_16x16x32_bf16 v[26:29], v[180:183], v[196:199], v[26:29]
	v_mfma_f32_16x16x32_bf16 v[18:21], v[172:175], v[204:207], v[18:21]
	v_mfma_f32_16x16x32_bf16 v[10:13], v[180:183], v[204:207], v[10:13]
	v_mfma_f32_16x16x32_bf16 v[6:9], v[172:175], v[212:215], v[6:9]
	v_mfma_f32_16x16x32_bf16 v[2:5], v[180:183], v[212:215], v[2:5]
	s_setprio 0
	s_barrier
	s_add_i32 s63, 0, 0x18000
	v_add_u32_e32 v155, s63, v150
	s_add_i32 s68, 0, 0x1c000
	ds_read_b128 v[146:149], v155
	ds_read_b128 v[156:159], v155 offset:1024
	ds_read_b128 v[160:163], v155 offset:2048
	ds_read_b128 v[164:167], v155 offset:3072
	v_add_u32_e32 v155, s68, v150
	ds_read_b128 v[168:171], v155
	ds_read_b128 v[172:175], v155 offset:1024
	ds_read_b128 v[176:179], v155 offset:2048
	ds_read_b128 v[180:183], v155 offset:3072
	s_add_u32 s28, s28, 0x80000
	s_addc_u32 s29, s29, 0
	s_mov_b32 m0, s39
	v_lshl_add_u64 v[224:225], s[28:29], 0, v[136:137]
	ds_read_b128 v[184:187], v154 offset:32768
	ds_read_b128 v[188:191], v154 offset:33792
	ds_read_b128 v[192:195], v154 offset:34816
	ds_read_b128 v[196:199], v154 offset:35840
	ds_read_b128 v[200:203], v154 offset:36864
	ds_read_b128 v[204:207], v154 offset:37888
	ds_read_b128 v[208:211], v154 offset:38912
	ds_read_b128 v[212:215], v154 offset:39936
	global_load_lds_dwordx4 v[224:225], off
	v_lshl_add_u64 v[224:225], s[28:29], 0, v[132:133]
	s_mov_b32 m0, s40
	s_nop 0
	global_load_lds_dwordx4 v[224:225], off
	s_waitcnt vmcnt(8)
	s_waitcnt lgkmcnt(0)
	s_barrier
	s_setprio 1
	s_waitcnt lgkmcnt(0)
	v_mfma_f32_16x16x32_bf16 v[126:129], v[146:149], v[184:187], v[126:129]
	v_mfma_f32_16x16x32_bf16 v[122:125], v[160:163], v[184:187], v[122:125]
	v_mfma_f32_16x16x32_bf16 v[118:121], v[146:149], v[192:195], v[118:121]
	v_mfma_f32_16x16x32_bf16 v[110:113], v[160:163], v[192:195], v[110:113]
	v_mfma_f32_16x16x32_bf16 v[102:105], v[146:149], v[200:203], v[102:105]
	v_mfma_f32_16x16x32_bf16 v[94:97], v[160:163], v[200:203], v[94:97]
	v_mfma_f32_16x16x32_bf16 v[86:89], v[146:149], v[208:211], v[86:89]
	v_mfma_f32_16x16x32_bf16 v[78:81], v[160:163], v[208:211], v[78:81]
	v_mfma_f32_16x16x32_bf16 v[126:129], v[156:159], v[188:191], v[126:129]
	v_mfma_f32_16x16x32_bf16 v[122:125], v[164:167], v[188:191], v[122:125]
	v_mfma_f32_16x16x32_bf16 v[118:121], v[156:159], v[196:199], v[118:121]
	v_mfma_f32_16x16x32_bf16 v[110:113], v[164:167], v[196:199], v[110:113]
	v_mfma_f32_16x16x32_bf16 v[102:105], v[156:159], v[204:207], v[102:105]
	v_mfma_f32_16x16x32_bf16 v[94:97], v[164:167], v[204:207], v[94:97]
	v_mfma_f32_16x16x32_bf16 v[86:89], v[156:159], v[212:215], v[86:89]
	v_mfma_f32_16x16x32_bf16 v[78:81], v[164:167], v[212:215], v[78:81]
	s_setprio 0
	s_setprio 1
	v_mfma_f32_16x16x32_bf16 v[114:117], v[168:171], v[184:187], v[114:117]
	v_mfma_f32_16x16x32_bf16 v[106:109], v[176:179], v[184:187], v[106:109]
	v_mfma_f32_16x16x32_bf16 v[98:101], v[168:171], v[192:195], v[98:101]
	v_mfma_f32_16x16x32_bf16 v[90:93], v[176:179], v[192:195], v[90:93]
	v_mfma_f32_16x16x32_bf16 v[82:85], v[168:171], v[200:203], v[82:85]
	v_mfma_f32_16x16x32_bf16 v[74:77], v[176:179], v[200:203], v[74:77]
	v_mfma_f32_16x16x32_bf16 v[70:73], v[168:171], v[208:211], v[70:73]
	v_mfma_f32_16x16x32_bf16 v[66:69], v[176:179], v[208:211], v[66:69]
	v_mfma_f32_16x16x32_bf16 v[114:117], v[172:175], v[188:191], v[114:117]
	v_mfma_f32_16x16x32_bf16 v[106:109], v[180:183], v[188:191], v[106:109]
	v_mfma_f32_16x16x32_bf16 v[98:101], v[172:175], v[196:199], v[98:101]
	v_mfma_f32_16x16x32_bf16 v[90:93], v[180:183], v[196:199], v[90:93]
	v_mfma_f32_16x16x32_bf16 v[82:85], v[172:175], v[204:207], v[82:85]
	v_mfma_f32_16x16x32_bf16 v[74:77], v[180:183], v[204:207], v[74:77]
	v_mfma_f32_16x16x32_bf16 v[70:73], v[172:175], v[212:215], v[70:73]
	v_mfma_f32_16x16x32_bf16 v[66:69], v[180:183], v[212:215], v[66:69]
	s_setprio 0
	s_barrier
; #define PG8_STAGE(bufoff, gbase, voff) do { _Pragma("unroll") for (int _i = 0; _i < 2; ++_i) \
;         __builtin_amdgcn_global_load_lds((const unsigned*)((const char*)(gbase) + (voff)[_i]), (PG8_LAS unsigned*)(lds + (bufoff) + ldsw + _i * 8192), 16, 0, 0); } while (0)
; #define PG8_LDA(dst, b, h) do { _Pragma("unroll") for (int m = 0; m < 4; ++m) _Pragma("unroll") for (int k = 0; k < 2; ++k) dst[m][k] = *(const PG8_LAS bf16x8*)(lds + PG8_SA(b, h) + aoff + m * 2048 + k * 1024); } while (0)
; #define PG8_WAIT_V(n) asm volatile("s_waitcnt vmcnt(" #n ")" ::: "memory")
; #define PG8_WAIT_L(n) asm volatile("s_waitcnt lgkmcnt(" #n ")" ::: "memory")
; #define PG8_BAR __builtin_amdgcn_s_barrier()
; #define PG8_SCHED __builtin_amdgcn_sched_barrier(0)
; template <class Epi, class Sched, bool ALIGN_EPI = false, bool SP2 = false, bool FP8 = false>
; __device__ __forceinline__ void gemm_phase(PG8_LAS unsigned char* lds, const Gemm g, const Sched& S, const Epi& E) {
;     ...
;         for (int t = 0; t < nt; t += 2) {
;     ...
;             PG8_WAIT_V(8); PG8_WAIT_L(0); PG8_BAR; PG8_MMA(0, 0, At, B0); PG8_MMA(0, 1, At, B1); PG8_BAR; PG8_SCHED;
;             PG8_LDA(At, 1, 1); PG8_STAGE(PG8_SB(1, 0), b3, voffB); PG8_STAGE(PG8_SB(1, 1), b3 + hstep, voffB); PG8_STAGE(PG8_SA(1, 0), a3, voffA);
;             PG8_WAIT_V(8); PG8_WAIT_L(0); PG8_BAR; PG8_MMA(1, 0, At, B0); PG8_MMA(1, 1, At, B1); PG8_BAR; PG8_SCHED;
	s_add_i32 s28, s63, s35
	v_lshl_add_u64 v[216:217], v[216:217], 0, s[10:11]
	s_mov_b32 m0, s28
	ds_read_b128 v[184:187], v154 offset:49152
	ds_read_b128 v[188:191], v154 offset:50176
	ds_read_b128 v[192:195], v154 offset:51200
	ds_read_b128 v[196:199], v154 offset:52224
	ds_read_b128 v[200:203], v154 offset:53248
	ds_read_b128 v[204:207], v154 offset:54272
	ds_read_b128 v[208:211], v154 offset:55296
	ds_read_b128 v[212:215], v154 offset:56320
	global_load_lds_dwordx4 v[216:217], off
	s_add_i32 m0, s28, 0x2000
	s_add_u32 s26, s26, 0x80080
	v_lshl_add_u64 v[216:217], v[218:219], 0, s[10:11]
	s_addc_u32 s27, s27, 0
	s_add_i32 s28, s68, s35
	global_load_lds_dwordx4 v[216:217], off
	v_lshl_add_u64 v[216:217], s[26:27], 0, v[134:135]
	s_mov_b32 m0, s28
	s_nop 0
	global_load_lds_dwordx4 v[216:217], off
	v_lshl_add_u64 v[216:217], s[26:27], 0, v[130:131]
	s_add_i32 m0, s28, 0x2000
	s_nop 0
	global_load_lds_dwordx4 v[216:217], off
	v_lshl_add_u64 v[216:217], v[220:221], 0, s[10:11]
	s_mov_b32 m0, s43
	s_nop 0
	global_load_lds_dwordx4 v[216:217], off
	v_lshl_add_u64 v[216:217], v[222:223], 0, s[10:11]
	s_mov_b32 m0, s44
	s_nop 0
	global_load_lds_dwordx4 v[216:217], off
	s_waitcnt vmcnt(8)
	s_waitcnt lgkmcnt(0)
	s_barrier
	s_setprio 1
	s_waitcnt lgkmcnt(0)
	v_mfma_f32_16x16x32_bf16 v[62:65], v[146:149], v[184:187], v[62:65]
	v_mfma_f32_16x16x32_bf16 v[58:61], v[160:163], v[184:187], v[58:61]
	v_mfma_f32_16x16x32_bf16 v[54:57], v[146:149], v[192:195], v[54:57]
	v_mfma_f32_16x16x32_bf16 v[46:49], v[160:163], v[192:195], v[46:49]
	v_mfma_f32_16x16x32_bf16 v[38:41], v[146:149], v[200:203], v[38:41]
	v_mfma_f32_16x16x32_bf16 v[30:33], v[160:163], v[200:203], v[30:33]
	v_mfma_f32_16x16x32_bf16 v[22:25], v[146:149], v[208:211], v[22:25]
	v_mfma_f32_16x16x32_bf16 v[14:17], v[160:163], v[208:211], v[14:17]
	v_mfma_f32_16x16x32_bf16 v[62:65], v[156:159], v[188:191], v[62:65]
	v_mfma_f32_16x16x32_bf16 v[58:61], v[164:167], v[188:191], v[58:61]
	v_mfma_f32_16x16x32_bf16 v[54:57], v[156:159], v[196:199], v[54:57]
	v_mfma_f32_16x16x32_bf16 v[46:49], v[164:167], v[196:199], v[46:49]
	v_mfma_f32_16x16x32_bf16 v[38:41], v[156:159], v[204:207], v[38:41]
	v_mfma_f32_16x16x32_bf16 v[30:33], v[164:167], v[204:207], v[30:33]
	v_mfma_f32_16x16x32_bf16 v[22:25], v[156:159], v[212:215], v[22:25]
	v_mfma_f32_16x16x32_bf16 v[14:17], v[164:167], v[212:215], v[14:17]
	s_setprio 0
	s_setprio 1
	v_mfma_f32_16x16x32_bf16 v[50:53], v[168:171], v[184:187], v[50:53]
	v_mfma_f32_16x16x32_bf16 v[42:45], v[176:179], v[184:187], v[42:45]
	v_mfma_f32_16x16x32_bf16 v[34:37], v[168:171], v[192:195], v[34:37]
	v_mfma_f32_16x16x32_bf16 v[26:29], v[176:179], v[192:195], v[26:29]
	v_mfma_f32_16x16x32_bf16 v[18:21], v[168:171], v[200:203], v[18:21]
	v_mfma_f32_16x16x32_bf16 v[10:13], v[176:179], v[200:203], v[10:13]
	v_mfma_f32_16x16x32_bf16 v[6:9], v[168:171], v[208:211], v[6:9]
	v_mfma_f32_16x16x32_bf16 v[2:5], v[176:179], v[208:211], v[2:5]
	v_mfma_f32_16x16x32_bf16 v[50:53], v[172:175], v[188:191], v[50:53]
	v_mfma_f32_16x16x32_bf16 v[42:45], v[180:183], v[188:191], v[42:45]
	v_mfma_f32_16x16x32_bf16 v[34:37], v[172:175], v[196:199], v[34:37]
	v_mfma_f32_16x16x32_bf16 v[26:29], v[180:183], v[196:199], v[26:29]
	v_mfma_f32_16x16x32_bf16 v[18:21], v[172:175], v[204:207], v[18:21]
	v_mfma_f32_16x16x32_bf16 v[10:13], v[180:183], v[204:207], v[10:13]
	v_mfma_f32_16x16x32_bf16 v[6:9], v[172:175], v[212:215], v[6:9]
	v_mfma_f32_16x16x32_bf16 v[2:5], v[180:183], v[212:215], v[2:5]
	s_setprio 0
	s_add_i32 s62, s62, 2
	s_add_u32 s24, s24, 0x100
	s_addc_u32 s25, s25, 0
	s_add_u32 s60, s60, 0x100
	s_addc_u32 s61, s61, 0
	s_cmp_gt_u32 s62, 29
	s_cbranch_scc0 .Lrot_head_1358
	s_barrier
	s_and_b64 vcc, exec, s[12:13]
	s_cbranch_vccz .LBB0_1361
	s_barrier

; template <class Epi, class Sched, bool ALIGN_EPI = false, bool SP2 = false, bool FP8 = false>
; __device__ __forceinline__ void gemm_phase(PG8_LAS unsigned char* lds, const Gemm g, const Sched& S, const Epi& E) {
;     ...
;         const bool has_next = S.next(ui + 1, nxt);
;         const char* nA = has_next ? (const char*)g.A + (size_t)nxt.pm * tstep : cA; const char* nB = has_next ? (const char*)g.Bt + (size_t)nxt.pb * tstep : cB;
;         for (int t = 0; t < nt; t += 2) {
;             const bool last = (t == nt - 2);
;             const char* a1 = cA + (size_t)(t + 1) * kstep;
;             const char* a2 = last ? nA : cA + (size_t)(t + 2) * kstep; const char* b2 = last ? nB : cB + (size_t)(t + 2) * kstep;
;             const char* a3 = a2 + kstep; const char* b3 = b2 + kstep;
;     ...
;         if (!has_next) break;
; #pragma unroll
;         for (int a = 0; a < 2; ++a)
; #pragma unroll
;             for (int b = 0; b < 2; ++b)
; #pragma unroll
;                 for (int m = 0; m < 4; ++m)
; #pragma unroll
;                     for (int n = 0; n < 2; ++n) acc[a][b][m][n] = (f32x4){0.f, 0.f, 0.f, 0.f};
;         cur = nxt; cA = nA; cB = nB; ++ui;
.LBB0_1951:
	s_ashr_i32 s25, s24, 31
	s_lshl_b64 s[26:27], s[24:25], 20
	s_add_u32 s26, s33, s26
	s_addc_u32 s27, s40, s27
	s_and_b64 s[28:29], s[6:7], exec
	s_cselect_b32 s25, s27, s35
	s_cselect_b32 s61, s26, s34
	s_ashr_i32 s23, s22, 31
	s_lshl_b64 s[28:29], s[22:23], 20
	s_add_u32 s28, s41, s28
	s_addc_u32 s29, s42, s29
	s_and_b64 s[38:39], s[6:7], exec
	s_cselect_b32 s23, s29, s37
	s_cselect_b32 s62, s28, s36
	s_add_u32 s34, s34, 0x80080
	s_addc_u32 s35, s35, 0
	s_add_u32 s63, s36, 0x100
	v_mov_b32_e32 v2, 0
	s_addc_u32 s68, s37, 0
	s_mov_b32 s69, -2
	v_mov_b32_e32 v3, v2
	v_mov_b32_e32 v4, v2
	v_mov_b32_e32 v5, v2
	v_mov_b32_e32 v6, v2
	v_mov_b32_e32 v7, v2
	v_mov_b32_e32 v8, v2
	v_mov_b32_e32 v9, v2
	v_mov_b32_e32 v18, v2
	v_mov_b32_e32 v19, v2
	v_mov_b32_e32 v20, v2
	v_mov_b32_e32 v21, v2
	v_mov_b32_e32 v22, v2
	v_mov_b32_e32 v23, v2
	v_mov_b32_e32 v24, v2
	v_mov_b32_e32 v25, v2
	v_mov_b32_e32 v34, v2
	v_mov_b32_e32 v35, v2
	v_mov_b32_e32 v36, v2
	v_mov_b32_e32 v37, v2
	v_mov_b32_e32 v38, v2
	v_mov_b32_e32 v39, v2
	v_mov_b32_e32 v40, v2
	v_mov_b32_e32 v41, v2
	v_mov_b32_e32 v50, v2
	v_mov_b32_e32 v51, v2
	v_mov_b32_e32 v52, v2
	v_mov_b32_e32 v53, v2
	v_mov_b32_e32 v54, v2
	v_mov_b32_e32 v55, v2
	v_mov_b32_e32 v56, v2
	v_mov_b32_e32 v57, v2
	v_mov_b32_e32 v10, v2
	v_mov_b32_e32 v11, v2
	v_mov_b32_e32 v12, v2
	v_mov_b32_e32 v13, v2
	v_mov_b32_e32 v14, v2
	v_mov_b32_e32 v15, v2
	v_mov_b32_e32 v16, v2
	v_mov_b32_e32 v17, v2
	v_mov_b32_e32 v26, v2
	v_mov_b32_e32 v27, v2
	v_mov_b32_e32 v28, v2
	v_mov_b32_e32 v29, v2
	v_mov_b32_e32 v30, v2
	v_mov_b32_e32 v31, v2
	v_mov_b32_e32 v32, v2
	v_mov_b32_e32 v33, v2
	v_mov_b32_e32 v42, v2
	v_mov_b32_e32 v43, v2
	v_mov_b32_e32 v44, v2
	v_mov_b32_e32 v45, v2
	v_mov_b32_e32 v46, v2
	v_mov_b32_e32 v47, v2
	v_mov_b32_e32 v48, v2
	v_mov_b32_e32 v49, v2
	v_mov_b32_e32 v58, v2
	v_mov_b32_e32 v59, v2
	v_mov_b32_e32 v60, v2
	v_mov_b32_e32 v61, v2
	v_mov_b32_e32 v62, v2
	v_mov_b32_e32 v63, v2
	v_mov_b32_e32 v64, v2
	v_mov_b32_e32 v65, v2
	v_mov_b32_e32 v66, v2
	v_mov_b32_e32 v67, v2
	v_mov_b32_e32 v68, v2
	v_mov_b32_e32 v69, v2
	v_mov_b32_e32 v70, v2
	v_mov_b32_e32 v71, v2
	v_mov_b32_e32 v72, v2
	v_mov_b32_e32 v73, v2
	v_mov_b32_e32 v82, v2
	v_mov_b32_e32 v83, v2
	v_mov_b32_e32 v84, v2
	v_mov_b32_e32 v85, v2
	v_mov_b32_e32 v86, v2
	v_mov_b32_e32 v87, v2
	v_mov_b32_e32 v88, v2
	v_mov_b32_e32 v89, v2
	v_mov_b32_e32 v98, v2
	v_mov_b32_e32 v99, v2
	v_mov_b32_e32 v100, v2
	v_mov_b32_e32 v101, v2
	v_mov_b32_e32 v102, v2
	v_mov_b32_e32 v103, v2
	v_mov_b32_e32 v104, v2
	v_mov_b32_e32 v105, v2
	v_mov_b32_e32 v114, v2
	v_mov_b32_e32 v115, v2
	v_mov_b32_e32 v116, v2
	v_mov_b32_e32 v117, v2
	v_mov_b32_e32 v118, v2
	v_mov_b32_e32 v119, v2
	v_mov_b32_e32 v120, v2
	v_mov_b32_e32 v121, v2
	v_mov_b32_e32 v74, v2
	v_mov_b32_e32 v75, v2
	v_mov_b32_e32 v76, v2
	v_mov_b32_e32 v77, v2
	v_mov_b32_e32 v78, v2
	v_mov_b32_e32 v79, v2
	v_mov_b32_e32 v80, v2
	v_mov_b32_e32 v81, v2
	v_mov_b32_e32 v90, v2
	v_mov_b32_e32 v91, v2
	v_mov_b32_e32 v92, v2
	v_mov_b32_e32 v93, v2
	v_mov_b32_e32 v94, v2
	v_mov_b32_e32 v95, v2
	v_mov_b32_e32 v96, v2
	v_mov_b32_e32 v97, v2
	v_mov_b32_e32 v106, v2
	v_mov_b32_e32 v107, v2
	v_mov_b32_e32 v108, v2
	v_mov_b32_e32 v109, v2
	v_mov_b32_e32 v110, v2
	v_mov_b32_e32 v111, v2
	v_mov_b32_e32 v112, v2
	v_mov_b32_e32 v113, v2
	v_mov_b32_e32 v122, v2
	v_mov_b32_e32 v123, v2
	v_mov_b32_e32 v124, v2
	v_mov_b32_e32 v125, v2
	v_mov_b32_e32 v126, v2
	v_mov_b32_e32 v127, v2
	v_mov_b32_e32 v128, v2
	v_mov_b32_e32 v129, v2
	s_branch .LBB0_1952

; #define PG8_STAGE(bufoff, gbase, voff) do { _Pragma("unroll") for (int _i = 0; _i < 2; ++_i) \
;         __builtin_amdgcn_global_load_lds((const unsigned*)((const char*)(gbase) + (voff)[_i]), (PG8_LAS unsigned*)(lds + (bufoff) + ldsw + _i * 8192), 16, 0, 0); } while (0)
; #define PG8_LDA(dst, b, h) do { _Pragma("unroll") for (int m = 0; m < 4; ++m) _Pragma("unroll") for (int k = 0; k < 2; ++k) dst[m][k] = *(const PG8_LAS bf16x8*)(lds + PG8_SA(b, h) + aoff + m * 2048 + k * 1024); } while (0)
; #define PG8_LDB(dst, b, h) do { _Pragma("unroll") for (int n = 0; n < 2; ++n) _Pragma("unroll") for (int k = 0; k < 2; ++k) dst[n][k] = *(const PG8_LAS bf16x8*)(lds + PG8_SB(b, h) + boff + n * 2048 + k * 1024); } while (0)
; #define PG8_WAIT_V(n) asm volatile("s_waitcnt vmcnt(" #n ")" ::: "memory")
; #define PG8_WAIT_L(n) asm volatile("s_waitcnt lgkmcnt(" #n ")" ::: "memory")
; #define PG8_BAR __builtin_amdgcn_s_barrier()
; #define PG8_SCHED __builtin_amdgcn_sched_barrier(0)
; template <class Epi, class Sched, bool ALIGN_EPI = false, bool SP2 = false, bool FP8 = false>
; __device__ __forceinline__ void gemm_phase(PG8_LAS unsigned char* lds, const Gemm g, const Sched& S, const Epi& E) {
;     ...
;             const bool last = (t == nt - 2);
;             const char* a1 = cA + (size_t)(t + 1) * kstep;
;             const char* a2 = last ? nA : cA + (size_t)(t + 2) * kstep; const char* b2 = last ? nB : cB + (size_t)(t + 2) * kstep;
;             const char* a3 = a2 + kstep; const char* b3 = b2 + kstep;
;             if (last && has_next) S.a_ready(nxt);
;             if constexpr (SP2) {
;             PG8_LDB(B0, 0, 0); PG8_LDB(B1, 0, 1); PG8_SCHED; PG8_LDA(At, 0, 0); PG8_STAGE(PG8_SA(1, 1), a1 + hstep, voffA);
;             PG8_WAIT_V(8); PG8_WAIT_L(0); PG8_BAR; PG8_MMA(0, 0, At, B0); PG8_MMA(0, 1, At, B1); PG8_BAR; PG8_SCHED;
;             PG8_LDA(At, 0, 1); PG8_STAGE(PG8_SB(0, 0), b2, voffB); PG8_STAGE(PG8_SB(0, 1), b2 + hstep, voffB); PG8_STAGE(PG8_SA(0, 0), a2, voffA);
.LBB0_1952:
	ds_read_b128 v[130:133], v190
	ds_read_b128 v[134:137], v190 offset:1024
	ds_read_b128 v[138:141], v190 offset:2048
	ds_read_b128 v[142:145], v190 offset:3072
	ds_read_b128 v[162:165], v191
	ds_read_b128 v[166:169], v191 offset:1024
	ds_read_b128 v[170:173], v191 offset:2048
	ds_read_b128 v[174:177], v191 offset:3072
	s_add_u32 s36, s34, 0xfff80080
	s_addc_u32 s37, s35, -1
	s_cmp_eq_u32 s69, 28
	s_cselect_b32 s39, s25, s37
	s_cselect_b32 s38, s61, s36
	s_cselect_b32 s37, s23, s68
	s_cselect_b32 s36, s62, s63
	v_lshl_add_u64 v[186:187], s[34:35], 0, v[154:155]
	s_add_i32 m0, s31, 0xc000
	ds_read_b128 v[178:181], v192
	ds_read_b128 v[182:185], v192 offset:1024
	ds_read_b128 v[194:197], v192 offset:2048
	ds_read_b128 v[198:201], v192 offset:3072
	ds_read_b128 v[202:205], v192 offset:4096
	ds_read_b128 v[206:209], v192 offset:5120
	ds_read_b128 v[210:213], v192 offset:6144
	ds_read_b128 v[214:217], v192 offset:7168
	global_load_lds_dwordx4 v[186:187], off
	v_lshl_add_u64 v[186:187], s[34:35], 0, v[156:157]
	s_add_i32 m0, s31, 0xe000
	s_nop 0
	global_load_lds_dwordx4 v[186:187], off
	s_waitcnt vmcnt(8)
	s_waitcnt lgkmcnt(0)
	s_barrier
	s_setprio 1
	s_waitcnt lgkmcnt(0)
	v_mfma_f32_16x16x32_bf16 v[126:129], v[130:133], v[178:181], v[126:129]
	v_mfma_f32_16x16x32_bf16 v[122:125], v[138:141], v[178:181], v[122:125]
	v_mfma_f32_16x16x32_bf16 v[110:113], v[130:133], v[194:197], v[110:113]
	v_mfma_f32_16x16x32_bf16 v[106:109], v[138:141], v[194:197], v[106:109]
	v_mfma_f32_16x16x32_bf16 v[94:97], v[130:133], v[202:205], v[94:97]
	v_mfma_f32_16x16x32_bf16 v[90:93], v[138:141], v[202:205], v[90:93]
	v_mfma_f32_16x16x32_bf16 v[78:81], v[130:133], v[210:213], v[78:81]
	v_mfma_f32_16x16x32_bf16 v[74:77], v[138:141], v[210:213], v[74:77]
	v_mfma_f32_16x16x32_bf16 v[126:129], v[134:137], v[182:185], v[126:129]
	v_mfma_f32_16x16x32_bf16 v[122:125], v[142:145], v[182:185], v[122:125]
	v_mfma_f32_16x16x32_bf16 v[110:113], v[134:137], v[198:201], v[110:113]
	v_mfma_f32_16x16x32_bf16 v[106:109], v[142:145], v[198:201], v[106:109]
	v_mfma_f32_16x16x32_bf16 v[94:97], v[134:137], v[206:209], v[94:97]
	v_mfma_f32_16x16x32_bf16 v[90:93], v[142:145], v[206:209], v[90:93]
	v_mfma_f32_16x16x32_bf16 v[78:81], v[134:137], v[214:217], v[78:81]
	v_mfma_f32_16x16x32_bf16 v[74:77], v[142:145], v[214:217], v[74:77]
	s_setprio 0
	s_setprio 1
	v_mfma_f32_16x16x32_bf16 v[118:121], v[162:165], v[178:181], v[118:121]
	v_mfma_f32_16x16x32_bf16 v[114:117], v[170:173], v[178:181], v[114:117]
	v_mfma_f32_16x16x32_bf16 v[102:105], v[162:165], v[194:197], v[102:105]
	v_mfma_f32_16x16x32_bf16 v[98:101], v[170:173], v[194:197], v[98:101]
	v_mfma_f32_16x16x32_bf16 v[86:89], v[162:165], v[202:205], v[86:89]
	v_mfma_f32_16x16x32_bf16 v[82:85], v[170:173], v[202:205], v[82:85]
	v_mfma_f32_16x16x32_bf16 v[70:73], v[162:165], v[210:213], v[70:73]
	v_mfma_f32_16x16x32_bf16 v[66:69], v[170:173], v[210:213], v[66:69]
	v_mfma_f32_16x16x32_bf16 v[118:121], v[166:169], v[182:185], v[118:121]
	v_mfma_f32_16x16x32_bf16 v[114:117], v[174:177], v[182:185], v[114:117]
	v_mfma_f32_16x16x32_bf16 v[102:105], v[166:169], v[198:201], v[102:105]
	v_mfma_f32_16x16x32_bf16 v[98:101], v[174:177], v[198:201], v[98:101]
	v_mfma_f32_16x16x32_bf16 v[86:89], v[166:169], v[206:209], v[86:89]
	v_mfma_f32_16x16x32_bf16 v[82:85], v[174:177], v[206:209], v[82:85]
	v_mfma_f32_16x16x32_bf16 v[70:73], v[166:169], v[214:217], v[70:73]
	v_mfma_f32_16x16x32_bf16 v[66:69], v[174:177], v[214:217], v[66:69]
	s_setprio 0
	s_barrier
	s_add_i32 s70, s54, s43
	v_lshl_add_u64 v[186:187], s[36:37], 0, v[148:149]
	s_mov_b32 m0, s70
	ds_read_b128 v[178:181], v192 offset:16384
	ds_read_b128 v[182:185], v192 offset:17408
	ds_read_b128 v[194:197], v192 offset:18432
	ds_read_b128 v[198:201], v192 offset:19456
	ds_read_b128 v[202:205], v192 offset:20480
	ds_read_b128 v[206:209], v192 offset:21504
	ds_read_b128 v[210:213], v192 offset:22528
	ds_read_b128 v[214:217], v192 offset:23552
	global_load_lds_dwordx4 v[186:187], off
	s_add_i32 m0, s70, 0x2000
	s_add_u32 s70, s36, 0x80000
	v_lshl_add_u64 v[218:219], s[36:37], 0, v[152:153]
	s_addc_u32 s71, s37, 0
	s_add_i32 s72, s55, s43
	global_load_lds_dwordx4 v[218:219], off
	v_lshl_add_u64 v[220:221], s[70:71], 0, v[148:149]
	s_mov_b32 m0, s72
	v_lshl_add_u64 v[222:223], s[38:39], 0, v[150:151]
	global_load_lds_dwordx4 v[220:221], off
	v_lshl_add_u64 v[220:221], s[70:71], 0, v[152:153]
	s_add_i32 m0, s72, 0x2000
	s_nop 0
	global_load_lds_dwordx4 v[220:221], off
	v_lshl_add_u64 v[220:221], s[38:39], 0, v[146:147]
	s_mov_b32 m0, s31
	s_nop 0
	global_load_lds_dwordx4 v[220:221], off
	s_mov_b32 m0, s44
	s_nop 0
	global_load_lds_dwordx4 v[222:223], off
	s_waitcnt vmcnt(8)
	s_waitcnt lgkmcnt(0)
	s_barrier
; #define PG8_STAGE(bufoff, gbase, voff) do { _Pragma("unroll") for (int _i = 0; _i < 2; ++_i) \
;         __builtin_amdgcn_global_load_lds((const unsigned*)((const char*)(gbase) + (voff)[_i]), (PG8_LAS unsigned*)(lds + (bufoff) + ldsw + _i * 8192), 16, 0, 0); } while (0)
; #define PG8_LDA(dst, b, h) do { _Pragma("unroll") for (int m = 0; m < 4; ++m) _Pragma("unroll") for (int k = 0; k < 2; ++k) dst[m][k] = *(const PG8_LAS bf16x8*)(lds + PG8_SA(b, h) + aoff + m * 2048 + k * 1024); } while (0)
; #define PG8_LDB(dst, b, h) do { _Pragma("unroll") for (int n = 0; n < 2; ++n) _Pragma("unroll") for (int k = 0; k < 2; ++k) dst[n][k] = *(const PG8_LAS bf16x8*)(lds + PG8_SB(b, h) + boff + n * 2048 + k * 1024); } while (0)
; #define PG8_WAIT_V(n) asm volatile("s_waitcnt vmcnt(" #n ")" ::: "memory")
; #define PG8_WAIT_L(n) asm volatile("s_waitcnt lgkmcnt(" #n ")" ::: "memory")
; #define PG8_BAR __builtin_amdgcn_s_barrier()
; #define PG8_SCHED __builtin_amdgcn_sched_barrier(0)
; template <class Epi, class Sched, bool ALIGN_EPI = false, bool SP2 = false, bool FP8 = false>
; __device__ __forceinline__ void gemm_phase(PG8_LAS unsigned char* lds, const Gemm g, const Sched& S, const Epi& E) {
;     ...
;             PG8_WAIT_V(8); PG8_WAIT_L(0); PG8_BAR; PG8_MMA(0, 0, At, B0); PG8_MMA(0, 1, At, B1); PG8_BAR; PG8_SCHED;
;             PG8_LDA(At, 0, 1); PG8_STAGE(PG8_SB(0, 0), b2, voffB); PG8_STAGE(PG8_SB(0, 1), b2 + hstep, voffB); PG8_STAGE(PG8_SA(0, 0), a2, voffA);
;             PG8_WAIT_V(8); PG8_WAIT_L(0); PG8_BAR; PG8_MMA(1, 0, At, B0); PG8_MMA(1, 1, At, B1); PG8_BAR; PG8_SCHED;
;             PG8_LDB(B0, 1, 0); PG8_LDB(B1, 1, 1); PG8_SCHED; PG8_LDA(At, 1, 0); PG8_STAGE(PG8_SA(0, 1), a2 + hstep, voffA);
;             PG8_WAIT_V(8); PG8_WAIT_L(0); PG8_BAR; PG8_MMA(0, 0, At, B0); PG8_MMA(0, 1, At, B1); PG8_BAR; PG8_SCHED;
	s_setprio 1
	s_waitcnt lgkmcnt(0)
	v_mfma_f32_16x16x32_bf16 v[62:65], v[130:133], v[178:181], v[62:65]
	v_mfma_f32_16x16x32_bf16 v[58:61], v[138:141], v[178:181], v[58:61]
	v_mfma_f32_16x16x32_bf16 v[46:49], v[130:133], v[194:197], v[46:49]
	v_mfma_f32_16x16x32_bf16 v[42:45], v[138:141], v[194:197], v[42:45]
	v_mfma_f32_16x16x32_bf16 v[30:33], v[130:133], v[202:205], v[30:33]
	v_mfma_f32_16x16x32_bf16 v[26:29], v[138:141], v[202:205], v[26:29]
	v_mfma_f32_16x16x32_bf16 v[14:17], v[130:133], v[210:213], v[14:17]
	v_mfma_f32_16x16x32_bf16 v[10:13], v[138:141], v[210:213], v[10:13]
	v_mfma_f32_16x16x32_bf16 v[62:65], v[134:137], v[182:185], v[62:65]
	v_mfma_f32_16x16x32_bf16 v[58:61], v[142:145], v[182:185], v[58:61]
	v_mfma_f32_16x16x32_bf16 v[46:49], v[134:137], v[198:201], v[46:49]
	v_mfma_f32_16x16x32_bf16 v[42:45], v[142:145], v[198:201], v[42:45]
	v_mfma_f32_16x16x32_bf16 v[30:33], v[134:137], v[206:209], v[30:33]
	v_mfma_f32_16x16x32_bf16 v[26:29], v[142:145], v[206:209], v[26:29]
	v_mfma_f32_16x16x32_bf16 v[14:17], v[134:137], v[214:217], v[14:17]
	v_mfma_f32_16x16x32_bf16 v[10:13], v[142:145], v[214:217], v[10:13]
	s_setprio 0
	s_setprio 1
	v_mfma_f32_16x16x32_bf16 v[54:57], v[162:165], v[178:181], v[54:57]
	v_mfma_f32_16x16x32_bf16 v[50:53], v[170:173], v[178:181], v[50:53]
	v_mfma_f32_16x16x32_bf16 v[38:41], v[162:165], v[194:197], v[38:41]
	v_mfma_f32_16x16x32_bf16 v[34:37], v[170:173], v[194:197], v[34:37]
	v_mfma_f32_16x16x32_bf16 v[22:25], v[162:165], v[202:205], v[22:25]
	v_mfma_f32_16x16x32_bf16 v[18:21], v[170:173], v[202:205], v[18:21]
	v_mfma_f32_16x16x32_bf16 v[6:9], v[162:165], v[210:213], v[6:9]
	v_mfma_f32_16x16x32_bf16 v[2:5], v[170:173], v[210:213], v[2:5]
	v_mfma_f32_16x16x32_bf16 v[54:57], v[166:169], v[182:185], v[54:57]
	v_mfma_f32_16x16x32_bf16 v[50:53], v[174:177], v[182:185], v[50:53]
	v_mfma_f32_16x16x32_bf16 v[38:41], v[166:169], v[198:201], v[38:41]
	v_mfma_f32_16x16x32_bf16 v[34:37], v[174:177], v[198:201], v[34:37]
	v_mfma_f32_16x16x32_bf16 v[22:25], v[166:169], v[206:209], v[22:25]
	v_mfma_f32_16x16x32_bf16 v[18:21], v[174:177], v[206:209], v[18:21]
	v_mfma_f32_16x16x32_bf16 v[6:9], v[166:169], v[214:217], v[6:9]
	v_mfma_f32_16x16x32_bf16 v[2:5], v[174:177], v[214:217], v[2:5]
	s_setprio 0
	s_barrier
	s_add_i32 s70, 0, 0x18000
	s_add_i32 s71, 0, 0x1c000
	v_add_u32_e32 v142, s70, v188
	v_add_u32_e32 v174, s71, v188
	ds_read_b128 v[130:133], v142
	ds_read_b128 v[134:137], v142 offset:1024
	ds_read_b128 v[138:141], v142 offset:2048
	ds_read_b128 v[142:145], v142 offset:3072
	ds_read_b128 v[162:165], v174
	ds_read_b128 v[166:169], v174 offset:1024
	ds_read_b128 v[170:173], v174 offset:2048
	ds_read_b128 v[174:177], v174 offset:3072
	s_add_u32 s38, s38, 0x80000
	s_addc_u32 s39, s39, 0
	s_mov_b32 m0, s45
	v_lshl_add_u64 v[224:225], s[38:39], 0, v[146:147]
	ds_read_b128 v[178:181], v192 offset:32768
	ds_read_b128 v[182:185], v192 offset:33792
	ds_read_b128 v[194:197], v192 offset:34816
	ds_read_b128 v[198:201], v192 offset:35840
	ds_read_b128 v[202:205], v192 offset:36864
	ds_read_b128 v[206:209], v192 offset:37888
	ds_read_b128 v[210:213], v192 offset:38912
	ds_read_b128 v[214:217], v192 offset:39936
	global_load_lds_dwordx4 v[224:225], off
	v_lshl_add_u64 v[224:225], s[38:39], 0, v[150:151]
	s_mov_b32 m0, s46
	s_nop 0
	global_load_lds_dwordx4 v[224:225], off
	s_waitcnt vmcnt(8)
	s_waitcnt lgkmcnt(0)
	s_barrier
	s_setprio 1
	s_waitcnt lgkmcnt(0)
	v_mfma_f32_16x16x32_bf16 v[126:129], v[130:133], v[178:181], v[126:129]
	v_mfma_f32_16x16x32_bf16 v[122:125], v[138:141], v[178:181], v[122:125]
	v_mfma_f32_16x16x32_bf16 v[110:113], v[130:133], v[194:197], v[110:113]
	v_mfma_f32_16x16x32_bf16 v[106:109], v[138:141], v[194:197], v[106:109]
	v_mfma_f32_16x16x32_bf16 v[94:97], v[130:133], v[202:205], v[94:97]
	v_mfma_f32_16x16x32_bf16 v[90:93], v[138:141], v[202:205], v[90:93]
	v_mfma_f32_16x16x32_bf16 v[78:81], v[130:133], v[210:213], v[78:81]
	v_mfma_f32_16x16x32_bf16 v[74:77], v[138:141], v[210:213], v[74:77]
	v_mfma_f32_16x16x32_bf16 v[126:129], v[134:137], v[182:185], v[126:129]
	v_mfma_f32_16x16x32_bf16 v[122:125], v[142:145], v[182:185], v[122:125]
	v_mfma_f32_16x16x32_bf16 v[110:113], v[134:137], v[198:201], v[110:113]
	v_mfma_f32_16x16x32_bf16 v[106:109], v[142:145], v[198:201], v[106:109]
	v_mfma_f32_16x16x32_bf16 v[94:97], v[134:137], v[206:209], v[94:97]
	v_mfma_f32_16x16x32_bf16 v[90:93], v[142:145], v[206:209], v[90:93]
	v_mfma_f32_16x16x32_bf16 v[78:81], v[134:137], v[214:217], v[78:81]
	v_mfma_f32_16x16x32_bf16 v[74:77], v[142:145], v[214:217], v[74:77]
	s_setprio 0
	s_setprio 1
	v_mfma_f32_16x16x32_bf16 v[118:121], v[162:165], v[178:181], v[118:121]
	v_mfma_f32_16x16x32_bf16 v[114:117], v[170:173], v[178:181], v[114:117]
	v_mfma_f32_16x16x32_bf16 v[102:105], v[162:165], v[194:197], v[102:105]
	v_mfma_f32_16x16x32_bf16 v[98:101], v[170:173], v[194:197], v[98:101]
	v_mfma_f32_16x16x32_bf16 v[86:89], v[162:165], v[202:205], v[86:89]
	v_mfma_f32_16x16x32_bf16 v[82:85], v[170:173], v[202:205], v[82:85]
	v_mfma_f32_16x16x32_bf16 v[70:73], v[162:165], v[210:213], v[70:73]
	v_mfma_f32_16x16x32_bf16 v[66:69], v[170:173], v[210:213], v[66:69]
	v_mfma_f32_16x16x32_bf16 v[118:121], v[166:169], v[182:185], v[118:121]
	v_mfma_f32_16x16x32_bf16 v[114:117], v[174:177], v[182:185], v[114:117]
	v_mfma_f32_16x16x32_bf16 v[102:105], v[166:169], v[198:201], v[102:105]
	v_mfma_f32_16x16x32_bf16 v[98:101], v[174:177], v[198:201], v[98:101]
	v_mfma_f32_16x16x32_bf16 v[86:89], v[166:169], v[206:209], v[86:89]
	v_mfma_f32_16x16x32_bf16 v[82:85], v[174:177], v[206:209], v[82:85]
	v_mfma_f32_16x16x32_bf16 v[70:73], v[166:169], v[214:217], v[70:73]
	v_mfma_f32_16x16x32_bf16 v[66:69], v[174:177], v[214:217], v[66:69]
	s_setprio 0
	s_barrier
; #define PG8_STAGE(bufoff, gbase, voff) do { _Pragma("unroll") for (int _i = 0; _i < 2; ++_i) \
;         __builtin_amdgcn_global_load_lds((const unsigned*)((const char*)(gbase) + (voff)[_i]), (PG8_LAS unsigned*)(lds + (bufoff) + ldsw + _i * 8192), 16, 0, 0); } while (0)
; #define PG8_LDA(dst, b, h) do { _Pragma("unroll") for (int m = 0; m < 4; ++m) _Pragma("unroll") for (int k = 0; k < 2; ++k) dst[m][k] = *(const PG8_LAS bf16x8*)(lds + PG8_SA(b, h) + aoff + m * 2048 + k * 1024); } while (0)
; #define PG8_WAIT_V(n) asm volatile("s_waitcnt vmcnt(" #n ")" ::: "memory")
; #define PG8_WAIT_L(n) asm volatile("s_waitcnt lgkmcnt(" #n ")" ::: "memory")
; #define PG8_BAR __builtin_amdgcn_s_barrier()
; #define PG8_SCHED __builtin_amdgcn_sched_barrier(0)
; template <class Epi, class Sched, bool ALIGN_EPI = false, bool SP2 = false, bool FP8 = false>
; __device__ __forceinline__ void gemm_phase(PG8_LAS unsigned char* lds, const Gemm g, const Sched& S, const Epi& E) {
;     ...
;         for (int t = 0; t < nt; t += 2) {
;     ...
;             PG8_WAIT_V(8); PG8_WAIT_L(0); PG8_BAR; PG8_MMA(0, 0, At, B0); PG8_MMA(0, 1, At, B1); PG8_BAR; PG8_SCHED;
;             PG8_LDA(At, 1, 1); PG8_STAGE(PG8_SB(1, 0), b3, voffB); PG8_STAGE(PG8_SB(1, 1), b3 + hstep, voffB); PG8_STAGE(PG8_SA(1, 0), a3, voffA);
;             PG8_WAIT_V(8); PG8_WAIT_L(0); PG8_BAR; PG8_MMA(1, 0, At, B0); PG8_MMA(1, 1, At, B1); PG8_BAR; PG8_SCHED;
	s_add_i32 s38, s70, s43
	v_lshl_add_u64 v[186:187], v[186:187], 0, s[10:11]
	s_mov_b32 m0, s38
	ds_read_b128 v[178:181], v192 offset:49152
	ds_read_b128 v[182:185], v192 offset:50176
	ds_read_b128 v[194:197], v192 offset:51200
	ds_read_b128 v[198:201], v192 offset:52224
	ds_read_b128 v[202:205], v192 offset:53248
	ds_read_b128 v[206:209], v192 offset:54272
	ds_read_b128 v[210:213], v192 offset:55296
	ds_read_b128 v[214:217], v192 offset:56320
	global_load_lds_dwordx4 v[186:187], off
	s_add_i32 m0, s38, 0x2000
	s_add_u32 s36, s36, 0x80080
	v_lshl_add_u64 v[186:187], v[218:219], 0, s[10:11]
	s_addc_u32 s37, s37, 0
	s_add_i32 s38, s71, s43
	global_load_lds_dwordx4 v[186:187], off
	v_lshl_add_u64 v[186:187], s[36:37], 0, v[148:149]
	s_mov_b32 m0, s38
	s_nop 0
	global_load_lds_dwordx4 v[186:187], off
	v_lshl_add_u64 v[186:187], s[36:37], 0, v[152:153]
	s_add_i32 m0, s38, 0x2000
	s_nop 0
	global_load_lds_dwordx4 v[186:187], off
	v_lshl_add_u64 v[186:187], v[220:221], 0, s[10:11]
	s_mov_b32 m0, s51
	s_nop 0
	global_load_lds_dwordx4 v[186:187], off
	v_lshl_add_u64 v[186:187], v[222:223], 0, s[10:11]
	s_mov_b32 m0, s52
	s_nop 0
	global_load_lds_dwordx4 v[186:187], off
	s_waitcnt vmcnt(8)
	s_waitcnt lgkmcnt(0)
	s_barrier
	s_setprio 1
	s_waitcnt lgkmcnt(0)
	v_mfma_f32_16x16x32_bf16 v[62:65], v[130:133], v[178:181], v[62:65]
	v_mfma_f32_16x16x32_bf16 v[58:61], v[138:141], v[178:181], v[58:61]
	v_mfma_f32_16x16x32_bf16 v[46:49], v[130:133], v[194:197], v[46:49]
	v_mfma_f32_16x16x32_bf16 v[42:45], v[138:141], v[194:197], v[42:45]
	v_mfma_f32_16x16x32_bf16 v[30:33], v[130:133], v[202:205], v[30:33]
	v_mfma_f32_16x16x32_bf16 v[26:29], v[138:141], v[202:205], v[26:29]
	v_mfma_f32_16x16x32_bf16 v[14:17], v[130:133], v[210:213], v[14:17]
	v_mfma_f32_16x16x32_bf16 v[10:13], v[138:141], v[210:213], v[10:13]
	v_mfma_f32_16x16x32_bf16 v[62:65], v[134:137], v[182:185], v[62:65]
	v_mfma_f32_16x16x32_bf16 v[58:61], v[142:145], v[182:185], v[58:61]
	v_mfma_f32_16x16x32_bf16 v[46:49], v[134:137], v[198:201], v[46:49]
	v_mfma_f32_16x16x32_bf16 v[42:45], v[142:145], v[198:201], v[42:45]
	v_mfma_f32_16x16x32_bf16 v[30:33], v[134:137], v[206:209], v[30:33]
	v_mfma_f32_16x16x32_bf16 v[26:29], v[142:145], v[206:209], v[26:29]
	v_mfma_f32_16x16x32_bf16 v[14:17], v[134:137], v[214:217], v[14:17]
	v_mfma_f32_16x16x32_bf16 v[10:13], v[142:145], v[214:217], v[10:13]
	s_setprio 0
	s_setprio 1
	v_mfma_f32_16x16x32_bf16 v[54:57], v[162:165], v[178:181], v[54:57]
	v_mfma_f32_16x16x32_bf16 v[50:53], v[170:173], v[178:181], v[50:53]
	v_mfma_f32_16x16x32_bf16 v[38:41], v[162:165], v[194:197], v[38:41]
	v_mfma_f32_16x16x32_bf16 v[34:37], v[170:173], v[194:197], v[34:37]
	v_mfma_f32_16x16x32_bf16 v[22:25], v[162:165], v[202:205], v[22:25]
	v_mfma_f32_16x16x32_bf16 v[18:21], v[170:173], v[202:205], v[18:21]
	v_mfma_f32_16x16x32_bf16 v[6:9], v[162:165], v[210:213], v[6:9]
	v_mfma_f32_16x16x32_bf16 v[2:5], v[170:173], v[210:213], v[2:5]
	v_mfma_f32_16x16x32_bf16 v[54:57], v[166:169], v[182:185], v[54:57]
	v_mfma_f32_16x16x32_bf16 v[50:53], v[174:177], v[182:185], v[50:53]
	v_mfma_f32_16x16x32_bf16 v[38:41], v[166:169], v[198:201], v[38:41]
	v_mfma_f32_16x16x32_bf16 v[34:37], v[174:177], v[198:201], v[34:37]
	v_mfma_f32_16x16x32_bf16 v[22:25], v[166:169], v[206:209], v[22:25]
	v_mfma_f32_16x16x32_bf16 v[18:21], v[174:177], v[206:209], v[18:21]
	v_mfma_f32_16x16x32_bf16 v[6:9], v[166:169], v[214:217], v[6:9]
	v_mfma_f32_16x16x32_bf16 v[2:5], v[174:177], v[214:217], v[2:5]
	s_setprio 0
	s_add_i32 s69, s69, 2
	s_add_u32 s34, s34, 0x100
	s_addc_u32 s35, s35, 0
	s_add_u32 s63, s63, 0x100
	s_addc_u32 s68, s68, 0
	s_cmp_gt_u32 s69, 29
	s_cbranch_scc0 .Lrot_head_1952
	s_barrier
	s_and_b64 vcc, exec, s[12:13]
	s_cbranch_vccz .LBB0_1955
	s_barrier

; template <class Epi, class Sched, bool ALIGN_EPI = false, bool SP2 = false, bool FP8 = false>
; __device__ __forceinline__ void gemm_phase(PG8_LAS unsigned char* lds, const Gemm g, const Sched& S, const Epi& E) {
;     ...
;         const bool has_next = S.next(ui + 1, nxt);
;         const char* nA = has_next ? (const char*)g.A + (size_t)nxt.pm * tstep : cA; const char* nB = has_next ? (const char*)g.Bt + (size_t)nxt.pb * tstep : cB;
;         for (int t = 0; t < nt; t += 2) {
;             const bool last = (t == nt - 2);
;             const char* a1 = cA + (size_t)(t + 1) * kstep;
;             const char* a2 = last ? nA : cA + (size_t)(t + 2) * kstep; const char* b2 = last ? nB : cB + (size_t)(t + 2) * kstep;
;             const char* a3 = a2 + kstep; const char* b3 = b2 + kstep;
;     ...
;         if (!has_next) break;
; #pragma unroll
;         for (int a = 0; a < 2; ++a)
; #pragma unroll
;             for (int b = 0; b < 2; ++b)
; #pragma unroll
;                 for (int m = 0; m < 4; ++m)
; #pragma unroll
;                     for (int n = 0; n < 2; ++n) acc[a][b][m][n] = (f32x4){0.f, 0.f, 0.f, 0.f};
;         cur = nxt; cA = nA; cB = nB; ++ui;
.LBB0_2183:
	s_ashr_i32 s13, s12, 31
	s_lshl_b64 s[18:19], s[12:13], 19
	s_add_u32 s18, s39, s18
	s_addc_u32 s19, s40, s19
	s_and_b64 s[20:21], s[14:15], exec
	s_cselect_b32 s13, s19, s25
	s_cselect_b32 s56, s18, s24
	s_ashr_i32 s17, s16, 31
	s_lshl_b64 s[20:21], s[16:17], 19
	s_add_u32 s20, s41, s20
	s_addc_u32 s21, s42, s21
	s_and_b64 s[28:29], s[14:15], exec
	s_cselect_b32 s17, s21, s27
	s_cselect_b32 s57, s20, s26
	s_add_u32 s24, s24, 0x40080
	s_addc_u32 s25, s25, 0
	s_add_u32 s58, s26, 0x100
	v_mov_b32_e32 v34, 0
	s_addc_u32 s59, s27, 0
	s_mov_b32 s60, -2
	v_mov_b32_e32 v35, v34
	v_mov_b32_e32 v36, v34
	v_mov_b32_e32 v37, v34
	v_mov_b32_e32 v42, v34
	v_mov_b32_e32 v43, v34
	v_mov_b32_e32 v44, v34
	v_mov_b32_e32 v45, v34
	v_mov_b32_e32 v50, v34
	v_mov_b32_e32 v51, v34
	v_mov_b32_e32 v52, v34
	v_mov_b32_e32 v53, v34
	v_mov_b32_e32 v58, v34
	v_mov_b32_e32 v59, v34
	v_mov_b32_e32 v60, v34
	v_mov_b32_e32 v61, v34
	v_mov_b32_e32 v66, v34
	v_mov_b32_e32 v67, v34
	v_mov_b32_e32 v68, v34
	v_mov_b32_e32 v69, v34
	v_mov_b32_e32 v74, v34
	v_mov_b32_e32 v75, v34
	v_mov_b32_e32 v76, v34
	v_mov_b32_e32 v77, v34
	v_mov_b32_e32 v82, v34
	v_mov_b32_e32 v83, v34
	v_mov_b32_e32 v84, v34
	v_mov_b32_e32 v85, v34
	v_mov_b32_e32 v90, v34
	v_mov_b32_e32 v91, v34
	v_mov_b32_e32 v92, v34
	v_mov_b32_e32 v93, v34
	v_mov_b32_e32 v38, v34
	v_mov_b32_e32 v39, v34
	v_mov_b32_e32 v40, v34
	v_mov_b32_e32 v41, v34
	v_mov_b32_e32 v46, v34
	v_mov_b32_e32 v47, v34
	v_mov_b32_e32 v48, v34
	v_mov_b32_e32 v49, v34
	v_mov_b32_e32 v54, v34
	v_mov_b32_e32 v55, v34
	v_mov_b32_e32 v56, v34
	v_mov_b32_e32 v57, v34
	v_mov_b32_e32 v62, v34
	v_mov_b32_e32 v63, v34
	v_mov_b32_e32 v64, v34
	v_mov_b32_e32 v65, v34
	v_mov_b32_e32 v70, v34
	v_mov_b32_e32 v71, v34
	v_mov_b32_e32 v72, v34
	v_mov_b32_e32 v73, v34
	v_mov_b32_e32 v78, v34
	v_mov_b32_e32 v79, v34
	v_mov_b32_e32 v80, v34
	v_mov_b32_e32 v81, v34
	v_mov_b32_e32 v86, v34
	v_mov_b32_e32 v87, v34
	v_mov_b32_e32 v88, v34
	v_mov_b32_e32 v89, v34
	v_mov_b32_e32 v94, v34
	v_mov_b32_e32 v95, v34
	v_mov_b32_e32 v96, v34
	v_mov_b32_e32 v97, v34
	v_mov_b32_e32 v98, v34
	v_mov_b32_e32 v99, v34
	v_mov_b32_e32 v100, v34
	v_mov_b32_e32 v101, v34
	v_mov_b32_e32 v106, v34
	v_mov_b32_e32 v107, v34
	v_mov_b32_e32 v108, v34
	v_mov_b32_e32 v109, v34
	v_mov_b32_e32 v114, v34
	v_mov_b32_e32 v115, v34
	v_mov_b32_e32 v116, v34
	v_mov_b32_e32 v117, v34
	v_mov_b32_e32 v122, v34
	v_mov_b32_e32 v123, v34
	v_mov_b32_e32 v124, v34
	v_mov_b32_e32 v125, v34
	v_mov_b32_e32 v130, v34
	v_mov_b32_e32 v131, v34
	v_mov_b32_e32 v132, v34
	v_mov_b32_e32 v133, v34
	v_mov_b32_e32 v138, v34
	v_mov_b32_e32 v139, v34
	v_mov_b32_e32 v140, v34
	v_mov_b32_e32 v141, v34
	v_mov_b32_e32 v146, v34
	v_mov_b32_e32 v147, v34
	v_mov_b32_e32 v148, v34
	v_mov_b32_e32 v149, v34
	v_mov_b32_e32 v154, v34
	v_mov_b32_e32 v155, v34
	v_mov_b32_e32 v156, v34
	v_mov_b32_e32 v157, v34
	v_mov_b32_e32 v102, v34
	v_mov_b32_e32 v103, v34
	v_mov_b32_e32 v104, v34
	v_mov_b32_e32 v105, v34
	v_mov_b32_e32 v110, v34
	v_mov_b32_e32 v111, v34
	v_mov_b32_e32 v112, v34
	v_mov_b32_e32 v113, v34
	v_mov_b32_e32 v118, v34
	v_mov_b32_e32 v119, v34
	v_mov_b32_e32 v120, v34
	v_mov_b32_e32 v121, v34
	v_mov_b32_e32 v126, v34
	v_mov_b32_e32 v127, v34
	v_mov_b32_e32 v128, v34
	v_mov_b32_e32 v129, v34
	v_mov_b32_e32 v134, v34
	v_mov_b32_e32 v135, v34
	v_mov_b32_e32 v136, v34
	v_mov_b32_e32 v137, v34
	v_mov_b32_e32 v142, v34
	v_mov_b32_e32 v143, v34
	v_mov_b32_e32 v144, v34
	v_mov_b32_e32 v145, v34
	v_mov_b32_e32 v150, v34
	v_mov_b32_e32 v151, v34
	v_mov_b32_e32 v152, v34
	v_mov_b32_e32 v153, v34
	v_mov_b32_e32 v158, v34
	v_mov_b32_e32 v159, v34
	v_mov_b32_e32 v160, v34
	v_mov_b32_e32 v161, v34
	s_branch .LBB0_2184

; #define PG8_STAGE(bufoff, gbase, voff) do { _Pragma("unroll") for (int _i = 0; _i < 2; ++_i) \
;         __builtin_amdgcn_global_load_lds((const unsigned*)((const char*)(gbase) + (voff)[_i]), (PG8_LAS unsigned*)(lds + (bufoff) + ldsw + _i * 8192), 16, 0, 0); } while (0)
; #define PG8_LDA(dst, b, h) do { _Pragma("unroll") for (int m = 0; m < 4; ++m) _Pragma("unroll") for (int k = 0; k < 2; ++k) dst[m][k] = *(const PG8_LAS bf16x8*)(lds + PG8_SA(b, h) + aoff + m * 2048 + k * 1024); } while (0)
; #define PG8_LDB(dst, b, h) do { _Pragma("unroll") for (int n = 0; n < 2; ++n) _Pragma("unroll") for (int k = 0; k < 2; ++k) dst[n][k] = *(const PG8_LAS bf16x8*)(lds + PG8_SB(b, h) + boff + n * 2048 + k * 1024); } while (0)
; #define PG8_WAIT_V(n) asm volatile("s_waitcnt vmcnt(" #n ")" ::: "memory")
; #define PG8_WAIT_L(n) asm volatile("s_waitcnt lgkmcnt(" #n ")" ::: "memory")
; #define PG8_BAR __builtin_amdgcn_s_barrier()
; #define PG8_SCHED __builtin_amdgcn_sched_barrier(0)
; template <class Epi, class Sched, bool ALIGN_EPI = false, bool SP2 = false, bool FP8 = false>
; __device__ __forceinline__ void gemm_phase(PG8_LAS unsigned char* lds, const Gemm g, const Sched& S, const Epi& E) {
;     ...
;             PG8_LDB(B0, 0, 0); PG8_LDB(B1, 0, 1); PG8_SCHED; PG8_LDA(At, 0, 0); PG8_STAGE(PG8_SA(1, 1), a1 + hstep, voffA);
;             PG8_WAIT_V(8); PG8_WAIT_L(0); PG8_BAR; PG8_MMA(0, 0, At, B0); PG8_MMA(0, 1, At, B1); PG8_BAR; PG8_SCHED;
;             PG8_LDA(At, 0, 1); PG8_STAGE(PG8_SB(0, 0), b2, voffB); PG8_STAGE(PG8_SB(0, 1), b2 + hstep, voffB); PG8_STAGE(PG8_SA(0, 0), a2, voffA);
;             PG8_WAIT_V(8); PG8_WAIT_L(0); PG8_BAR; PG8_MMA(1, 0, At, B0); PG8_MMA(1, 1, At, B1); PG8_BAR; PG8_SCHED;
.LBB0_2184:
	ds_read_b128 v[26:29], v184
	ds_read_b128 v[30:33], v184 offset:1024
	ds_read_b128 v[18:21], v184 offset:2048
	ds_read_b128 v[22:25], v184 offset:3072
	ds_read_b128 v[10:13], v185
	ds_read_b128 v[14:17], v185 offset:1024
	ds_read_b128 v[2:5], v185 offset:2048
	ds_read_b128 v[6:9], v185 offset:3072
	s_add_u32 s26, s24, 0xfffc0080
	s_addc_u32 s27, s25, -1
	s_cmp_eq_u32 s60, 12
	s_cselect_b32 s29, s13, s27
	s_cselect_b32 s28, s56, s26
	s_cselect_b32 s27, s17, s59
	s_cselect_b32 s26, s57, s58
	v_lshl_add_u64 v[212:213], s[24:25], 0, v[170:171]
	s_add_i32 m0, s23, 0xc000
	ds_read_b128 v[174:177], v186
	ds_read_b128 v[178:181], v186 offset:1024
	ds_read_b128 v[188:191], v186 offset:2048
	ds_read_b128 v[192:195], v186 offset:3072
	ds_read_b128 v[196:199], v186 offset:4096
	ds_read_b128 v[200:203], v186 offset:5120
	ds_read_b128 v[204:207], v186 offset:6144
	ds_read_b128 v[208:211], v186 offset:7168
	global_load_lds_dwordx4 v[212:213], off
	v_lshl_add_u64 v[212:213], s[24:25], 0, v[172:173]
	s_add_i32 m0, s23, 0xe000
	s_nop 0
	global_load_lds_dwordx4 v[212:213], off
	s_waitcnt vmcnt(8)
	s_waitcnt lgkmcnt(0)
	s_barrier
	s_setprio 1
	s_waitcnt lgkmcnt(0)
	v_mfma_f32_16x16x128_f8f6f4 v[158:161], v[26:33], v[174:181], v[158:161]
	v_mfma_f32_16x16x128_f8f6f4 v[150:153], v[18:25], v[174:181], v[150:153]
	v_mfma_f32_16x16x128_f8f6f4 v[142:145], v[26:33], v[188:195], v[142:145]
	v_mfma_f32_16x16x128_f8f6f4 v[134:137], v[18:25], v[188:195], v[134:137]
	v_mfma_f32_16x16x128_f8f6f4 v[126:129], v[26:33], v[196:203], v[126:129]
	v_mfma_f32_16x16x128_f8f6f4 v[118:121], v[18:25], v[196:203], v[118:121]
	v_mfma_f32_16x16x128_f8f6f4 v[110:113], v[26:33], v[204:211], v[110:113]
	v_mfma_f32_16x16x128_f8f6f4 v[102:105], v[18:25], v[204:211], v[102:105]
	s_setprio 0
	s_setprio 1
	v_mfma_f32_16x16x128_f8f6f4 v[154:157], v[10:17], v[174:181], v[154:157]
	v_mfma_f32_16x16x128_f8f6f4 v[146:149], v[2:9], v[174:181], v[146:149]
	v_mfma_f32_16x16x128_f8f6f4 v[138:141], v[10:17], v[188:195], v[138:141]
	v_mfma_f32_16x16x128_f8f6f4 v[130:133], v[2:9], v[188:195], v[130:133]
	v_mfma_f32_16x16x128_f8f6f4 v[122:125], v[10:17], v[196:203], v[122:125]
	v_mfma_f32_16x16x128_f8f6f4 v[114:117], v[2:9], v[196:203], v[114:117]
	v_mfma_f32_16x16x128_f8f6f4 v[106:109], v[10:17], v[204:211], v[106:109]
	v_mfma_f32_16x16x128_f8f6f4 v[98:101], v[2:9], v[204:211], v[98:101]
	s_setprio 0
	s_barrier
	s_add_i32 s61, s51, s43
	v_lshl_add_u64 v[174:175], s[26:27], 0, v[162:163]
	s_mov_b32 m0, s61
	ds_read_b128 v[188:191], v186 offset:16384
	ds_read_b128 v[192:195], v186 offset:17408
	ds_read_b128 v[196:199], v186 offset:18432
	ds_read_b128 v[200:203], v186 offset:19456
	ds_read_b128 v[204:207], v186 offset:20480
	ds_read_b128 v[208:211], v186 offset:21504
	ds_read_b128 v[212:215], v186 offset:22528
	ds_read_b128 v[216:219], v186 offset:23552
	global_load_lds_dwordx4 v[174:175], off
	s_add_i32 m0, s61, 0x2000
	s_add_u32 s62, s26, 0x40000
	v_lshl_add_u64 v[176:177], s[26:27], 0, v[164:165]
	s_addc_u32 s63, s27, 0
	s_add_i32 s61, s52, s43
	global_load_lds_dwordx4 v[176:177], off
	v_lshl_add_u64 v[178:179], s[62:63], 0, v[162:163]
	s_mov_b32 m0, s61
	v_lshl_add_u64 v[180:181], s[28:29], 0, v[166:167]
	global_load_lds_dwordx4 v[178:179], off
	v_lshl_add_u64 v[178:179], s[62:63], 0, v[164:165]
	s_add_i32 m0, s61, 0x2000
	s_nop 0
	global_load_lds_dwordx4 v[178:179], off
	v_lshl_add_u64 v[178:179], s[28:29], 0, v[168:169]
	s_mov_b32 m0, s23
	s_nop 0
	global_load_lds_dwordx4 v[178:179], off
	s_mov_b32 m0, s44
	s_nop 0
	global_load_lds_dwordx4 v[180:181], off
	s_waitcnt vmcnt(8)
	s_waitcnt lgkmcnt(0)
	s_barrier
	s_setprio 1
	s_waitcnt lgkmcnt(0)
	v_mfma_f32_16x16x128_f8f6f4 v[94:97], v[26:33], v[188:195], v[94:97]
	v_mfma_f32_16x16x128_f8f6f4 v[86:89], v[18:25], v[188:195], v[86:89]
	v_mfma_f32_16x16x128_f8f6f4 v[78:81], v[26:33], v[196:203], v[78:81]
	v_mfma_f32_16x16x128_f8f6f4 v[70:73], v[18:25], v[196:203], v[70:73]
	v_mfma_f32_16x16x128_f8f6f4 v[62:65], v[26:33], v[204:211], v[62:65]
	v_mfma_f32_16x16x128_f8f6f4 v[54:57], v[18:25], v[204:211], v[54:57]
	v_mfma_f32_16x16x128_f8f6f4 v[46:49], v[26:33], v[212:219], v[46:49]
	v_mfma_f32_16x16x128_f8f6f4 v[38:41], v[18:25], v[212:219], v[38:41]
	s_setprio 0
	s_setprio 1
	v_mfma_f32_16x16x128_f8f6f4 v[90:93], v[10:17], v[188:195], v[90:93]
	v_mfma_f32_16x16x128_f8f6f4 v[82:85], v[2:9], v[188:195], v[82:85]
	v_mfma_f32_16x16x128_f8f6f4 v[74:77], v[10:17], v[196:203], v[74:77]
	v_mfma_f32_16x16x128_f8f6f4 v[66:69], v[2:9], v[196:203], v[66:69]
	v_mfma_f32_16x16x128_f8f6f4 v[58:61], v[10:17], v[204:211], v[58:61]
	v_mfma_f32_16x16x128_f8f6f4 v[50:53], v[2:9], v[204:211], v[50:53]
	v_mfma_f32_16x16x128_f8f6f4 v[42:45], v[10:17], v[212:219], v[42:45]
	v_mfma_f32_16x16x128_f8f6f4 v[34:37], v[2:9], v[212:219], v[34:37]
	s_setprio 0
	s_barrier
; #define PG8_STAGE(bufoff, gbase, voff) do { _Pragma("unroll") for (int _i = 0; _i < 2; ++_i) \
;         __builtin_amdgcn_global_load_lds((const unsigned*)((const char*)(gbase) + (voff)[_i]), (PG8_LAS unsigned*)(lds + (bufoff) + ldsw + _i * 8192), 16, 0, 0); } while (0)
; #define PG8_LDA(dst, b, h) do { _Pragma("unroll") for (int m = 0; m < 4; ++m) _Pragma("unroll") for (int k = 0; k < 2; ++k) dst[m][k] = *(const PG8_LAS bf16x8*)(lds + PG8_SA(b, h) + aoff + m * 2048 + k * 1024); } while (0)
; #define PG8_LDB(dst, b, h) do { _Pragma("unroll") for (int n = 0; n < 2; ++n) _Pragma("unroll") for (int k = 0; k < 2; ++k) dst[n][k] = *(const PG8_LAS bf16x8*)(lds + PG8_SB(b, h) + boff + n * 2048 + k * 1024); } while (0)
; #define PG8_WAIT_V(n) asm volatile("s_waitcnt vmcnt(" #n ")" ::: "memory")
; #define PG8_WAIT_L(n) asm volatile("s_waitcnt lgkmcnt(" #n ")" ::: "memory")
; #define PG8_BAR __builtin_amdgcn_s_barrier()
; #define PG8_SCHED __builtin_amdgcn_sched_barrier(0)
; template <class Epi, class Sched, bool ALIGN_EPI = false, bool SP2 = false, bool FP8 = false>
; __device__ __forceinline__ void gemm_phase(PG8_LAS unsigned char* lds, const Gemm g, const Sched& S, const Epi& E) {
;     ...
;             PG8_WAIT_V(8); PG8_WAIT_L(0); PG8_BAR; PG8_MMA(1, 0, At, B0); PG8_MMA(1, 1, At, B1); PG8_BAR; PG8_SCHED;
;             PG8_LDB(B0, 1, 0); PG8_LDB(B1, 1, 1); PG8_SCHED; PG8_LDA(At, 1, 0); PG8_STAGE(PG8_SA(0, 1), a2 + hstep, voffA);
;             PG8_WAIT_V(8); PG8_WAIT_L(0); PG8_BAR; PG8_MMA(0, 0, At, B0); PG8_MMA(0, 1, At, B1); PG8_BAR; PG8_SCHED;
;             PG8_LDA(At, 1, 1); PG8_STAGE(PG8_SB(1, 0), b3, voffB); PG8_STAGE(PG8_SB(1, 1), b3 + hstep, voffB); PG8_STAGE(PG8_SA(1, 0), a3, voffA);
;             PG8_WAIT_V(8); PG8_WAIT_L(0); PG8_BAR; PG8_MMA(1, 0, At, B0); PG8_MMA(1, 1, At, B1); PG8_BAR; PG8_SCHED;
;     ...
;         if constexpr (FP8) asm volatile("s_nop 15\n\ts_nop 15\n\ts_nop 15\n\ts_nop 15" ::: "memory");
;         if constexpr (ALIGN_EPI) { if (wr == 0) PG8_BAR; }
	s_add_i32 s61, 0, 0x18000
	s_add_i32 s62, 0, 0x1c000
	v_add_u32_e32 v14, s61, v182
	v_add_u32_e32 v30, s62, v182
	ds_read_b128 v[2:5], v14
	ds_read_b128 v[6:9], v14 offset:1024
	ds_read_b128 v[10:13], v14 offset:2048
	ds_read_b128 v[14:17], v14 offset:3072
	ds_read_b128 v[18:21], v30
	ds_read_b128 v[22:25], v30 offset:1024
	ds_read_b128 v[26:29], v30 offset:2048
	ds_read_b128 v[30:33], v30 offset:3072
	s_add_u32 s28, s28, 0x40000
	s_addc_u32 s29, s29, 0
	s_mov_b32 m0, s45
	v_lshl_add_u64 v[220:221], s[28:29], 0, v[168:169]
	ds_read_b128 v[188:191], v186 offset:32768
	ds_read_b128 v[192:195], v186 offset:33792
	ds_read_b128 v[196:199], v186 offset:34816
	ds_read_b128 v[200:203], v186 offset:35840
	ds_read_b128 v[204:207], v186 offset:36864
	ds_read_b128 v[208:211], v186 offset:37888
	ds_read_b128 v[212:215], v186 offset:38912
	ds_read_b128 v[216:219], v186 offset:39936
	global_load_lds_dwordx4 v[220:221], off
	v_lshl_add_u64 v[220:221], s[28:29], 0, v[166:167]
	s_mov_b32 m0, s46
	s_nop 0
	global_load_lds_dwordx4 v[220:221], off
	s_waitcnt vmcnt(8)
	s_waitcnt lgkmcnt(0)
	s_barrier
	s_setprio 1
	s_waitcnt lgkmcnt(0)
	v_mfma_f32_16x16x128_f8f6f4 v[158:161], v[2:9], v[188:195], v[158:161]
	v_mfma_f32_16x16x128_f8f6f4 v[150:153], v[10:17], v[188:195], v[150:153]
	v_mfma_f32_16x16x128_f8f6f4 v[142:145], v[2:9], v[196:203], v[142:145]
	v_mfma_f32_16x16x128_f8f6f4 v[134:137], v[10:17], v[196:203], v[134:137]
	v_mfma_f32_16x16x128_f8f6f4 v[126:129], v[2:9], v[204:211], v[126:129]
	v_mfma_f32_16x16x128_f8f6f4 v[118:121], v[10:17], v[204:211], v[118:121]
	v_mfma_f32_16x16x128_f8f6f4 v[110:113], v[2:9], v[212:219], v[110:113]
	v_mfma_f32_16x16x128_f8f6f4 v[102:105], v[10:17], v[212:219], v[102:105]
	s_setprio 0
	s_setprio 1
	v_mfma_f32_16x16x128_f8f6f4 v[154:157], v[18:25], v[188:195], v[154:157]
	v_mfma_f32_16x16x128_f8f6f4 v[146:149], v[26:33], v[188:195], v[146:149]
	v_mfma_f32_16x16x128_f8f6f4 v[138:141], v[18:25], v[196:203], v[138:141]
	v_mfma_f32_16x16x128_f8f6f4 v[130:133], v[26:33], v[196:203], v[130:133]
	v_mfma_f32_16x16x128_f8f6f4 v[122:125], v[18:25], v[204:211], v[122:125]
	v_mfma_f32_16x16x128_f8f6f4 v[114:117], v[26:33], v[204:211], v[114:117]
	v_mfma_f32_16x16x128_f8f6f4 v[106:109], v[18:25], v[212:219], v[106:109]
	v_mfma_f32_16x16x128_f8f6f4 v[98:101], v[26:33], v[212:219], v[98:101]
	s_setprio 0
	s_barrier
	s_add_i32 s28, s61, s43
	v_lshl_add_u64 v[174:175], v[174:175], 0, s[6:7]
	s_mov_b32 m0, s28
	ds_read_b128 v[188:191], v186 offset:49152
	ds_read_b128 v[192:195], v186 offset:50176
	ds_read_b128 v[196:199], v186 offset:51200
	ds_read_b128 v[200:203], v186 offset:52224
	ds_read_b128 v[204:207], v186 offset:53248
	ds_read_b128 v[208:211], v186 offset:54272
	ds_read_b128 v[212:215], v186 offset:55296
	ds_read_b128 v[216:219], v186 offset:56320
	global_load_lds_dwordx4 v[174:175], off
	s_add_i32 m0, s28, 0x2000
	s_add_u32 s26, s26, 0x40080
	v_lshl_add_u64 v[174:175], v[176:177], 0, s[6:7]
	s_addc_u32 s27, s27, 0
	s_add_i32 s28, s62, s43
	global_load_lds_dwordx4 v[174:175], off
	v_lshl_add_u64 v[174:175], s[26:27], 0, v[162:163]
	s_mov_b32 m0, s28
	s_nop 0
	global_load_lds_dwordx4 v[174:175], off
	v_lshl_add_u64 v[174:175], s[26:27], 0, v[164:165]
	s_add_i32 m0, s28, 0x2000
	s_nop 0
	global_load_lds_dwordx4 v[174:175], off
	v_lshl_add_u64 v[174:175], v[178:179], 0, s[6:7]
	s_mov_b32 m0, s49
	s_nop 0
	global_load_lds_dwordx4 v[174:175], off
	v_lshl_add_u64 v[174:175], v[180:181], 0, s[6:7]
	s_mov_b32 m0, s50
	s_nop 0
	global_load_lds_dwordx4 v[174:175], off
	s_waitcnt vmcnt(8)
	s_waitcnt lgkmcnt(0)
	s_barrier
	s_setprio 1
	s_waitcnt lgkmcnt(0)
	v_mfma_f32_16x16x128_f8f6f4 v[94:97], v[2:9], v[188:195], v[94:97]
	v_mfma_f32_16x16x128_f8f6f4 v[86:89], v[10:17], v[188:195], v[86:89]
	v_mfma_f32_16x16x128_f8f6f4 v[78:81], v[2:9], v[196:203], v[78:81]
	v_mfma_f32_16x16x128_f8f6f4 v[70:73], v[10:17], v[196:203], v[70:73]
	v_mfma_f32_16x16x128_f8f6f4 v[62:65], v[2:9], v[204:211], v[62:65]
	v_mfma_f32_16x16x128_f8f6f4 v[54:57], v[10:17], v[204:211], v[54:57]
	v_mfma_f32_16x16x128_f8f6f4 v[46:49], v[2:9], v[212:219], v[46:49]
	v_mfma_f32_16x16x128_f8f6f4 v[38:41], v[10:17], v[212:219], v[38:41]
	s_setprio 0
	s_setprio 1
	v_mfma_f32_16x16x128_f8f6f4 v[90:93], v[18:25], v[188:195], v[90:93]
	v_mfma_f32_16x16x128_f8f6f4 v[82:85], v[26:33], v[188:195], v[82:85]
	v_mfma_f32_16x16x128_f8f6f4 v[74:77], v[18:25], v[196:203], v[74:77]
	v_mfma_f32_16x16x128_f8f6f4 v[66:69], v[26:33], v[196:203], v[66:69]
	v_mfma_f32_16x16x128_f8f6f4 v[58:61], v[18:25], v[204:211], v[58:61]
	v_mfma_f32_16x16x128_f8f6f4 v[50:53], v[26:33], v[204:211], v[50:53]
	v_mfma_f32_16x16x128_f8f6f4 v[42:45], v[18:25], v[212:219], v[42:45]
	v_mfma_f32_16x16x128_f8f6f4 v[34:37], v[26:33], v[212:219], v[34:37]
	s_setprio 0
	s_add_i32 s60, s60, 2
	s_add_u32 s24, s24, 0x100
	s_addc_u32 s25, s25, 0
	s_add_u32 s58, s58, 0x100
	s_addc_u32 s59, s59, 0
	s_cmp_gt_u32 s60, 13
	s_cbranch_scc0 .Lrot_head_2184
	s_barrier
	s_nop 15
	s_nop 15
	s_nop 15
	s_nop 15
	s_and_b64 vcc, exec, s[8:9]
	s_cbranch_vccz .LBB0_2187
	s_barrier

; template <class Epi, class Sched, bool ALIGN_EPI = false, bool SP2 = false, bool FP8 = false>
; __device__ __forceinline__ void gemm_phase(PG8_LAS unsigned char* lds, const Gemm g, const Sched& S, const Epi& E) {
;     ...
;         if (!has_next) break;
; #pragma unroll
;         for (int a = 0; a < 2; ++a)
; #pragma unroll
;             for (int b = 0; b < 2; ++b)
; #pragma unroll
;                 for (int m = 0; m < 4; ++m)
; #pragma unroll
;                     for (int n = 0; n < 2; ++n) acc[a][b][m][n] = (f32x4){0.f, 0.f, 0.f, 0.f};
;         cur = nxt; cA = nA; cB = nB; ++ui;
.LBB0_2258:
	s_add_u32 s34, s34, 0xe0080
	v_mov_b32_e32 v34, 0
	s_addc_u32 s35, s35, 0
	v_lshl_add_u64 v[172:173], v[2:3], 0, s[18:19]
	s_mov_b32 s71, -2
	v_mov_b32_e32 v35, v34
	v_mov_b32_e32 v36, v34
	v_mov_b32_e32 v37, v34
	v_mov_b32_e32 v38, v34
	v_mov_b32_e32 v39, v34
	v_mov_b32_e32 v40, v34
	v_mov_b32_e32 v41, v34
	v_mov_b32_e32 v46, v34
	v_mov_b32_e32 v47, v34
	v_mov_b32_e32 v48, v34
	v_mov_b32_e32 v49, v34
	v_mov_b32_e32 v54, v34
	v_mov_b32_e32 v55, v34
	v_mov_b32_e32 v56, v34
	v_mov_b32_e32 v57, v34
	v_mov_b32_e32 v62, v34
	v_mov_b32_e32 v63, v34
	v_mov_b32_e32 v64, v34
	v_mov_b32_e32 v65, v34
	v_mov_b32_e32 v70, v34
	v_mov_b32_e32 v71, v34
	v_mov_b32_e32 v72, v34
	v_mov_b32_e32 v73, v34
	v_mov_b32_e32 v78, v34
	v_mov_b32_e32 v79, v34
	v_mov_b32_e32 v80, v34
	v_mov_b32_e32 v81, v34
	v_mov_b32_e32 v86, v34
	v_mov_b32_e32 v87, v34
	v_mov_b32_e32 v88, v34
	v_mov_b32_e32 v89, v34
	v_mov_b32_e32 v42, v34
	v_mov_b32_e32 v43, v34
	v_mov_b32_e32 v44, v34
	v_mov_b32_e32 v45, v34
	v_mov_b32_e32 v50, v34
	v_mov_b32_e32 v51, v34
	v_mov_b32_e32 v52, v34
	v_mov_b32_e32 v53, v34
	v_mov_b32_e32 v58, v34
	v_mov_b32_e32 v59, v34
	v_mov_b32_e32 v60, v34
	v_mov_b32_e32 v61, v34
	v_mov_b32_e32 v66, v34
	v_mov_b32_e32 v67, v34
	v_mov_b32_e32 v68, v34
	v_mov_b32_e32 v69, v34
	v_mov_b32_e32 v74, v34
	v_mov_b32_e32 v75, v34
	v_mov_b32_e32 v76, v34
	v_mov_b32_e32 v77, v34
	v_mov_b32_e32 v82, v34
	v_mov_b32_e32 v83, v34
	v_mov_b32_e32 v84, v34
	v_mov_b32_e32 v85, v34
	v_mov_b32_e32 v90, v34
	v_mov_b32_e32 v91, v34
	v_mov_b32_e32 v92, v34
	v_mov_b32_e32 v93, v34
	v_mov_b32_e32 v94, v34
	v_mov_b32_e32 v95, v34
	v_mov_b32_e32 v96, v34
	v_mov_b32_e32 v97, v34
	v_mov_b32_e32 v98, v34
	v_mov_b32_e32 v99, v34
	v_mov_b32_e32 v100, v34
	v_mov_b32_e32 v101, v34
	v_mov_b32_e32 v102, v34
	v_mov_b32_e32 v103, v34
	v_mov_b32_e32 v104, v34
	v_mov_b32_e32 v105, v34
	v_mov_b32_e32 v110, v34
	v_mov_b32_e32 v111, v34
	v_mov_b32_e32 v112, v34
	v_mov_b32_e32 v113, v34
	v_mov_b32_e32 v118, v34
	v_mov_b32_e32 v119, v34
	v_mov_b32_e32 v120, v34
	v_mov_b32_e32 v121, v34
	v_mov_b32_e32 v126, v34
	v_mov_b32_e32 v127, v34
	v_mov_b32_e32 v128, v34
	v_mov_b32_e32 v129, v34
	v_mov_b32_e32 v134, v34
	v_mov_b32_e32 v135, v34
	v_mov_b32_e32 v136, v34
	v_mov_b32_e32 v137, v34
	v_mov_b32_e32 v142, v34
	v_mov_b32_e32 v143, v34
	v_mov_b32_e32 v144, v34
	v_mov_b32_e32 v145, v34
	v_mov_b32_e32 v150, v34
	v_mov_b32_e32 v151, v34
	v_mov_b32_e32 v152, v34
	v_mov_b32_e32 v153, v34
	v_mov_b32_e32 v106, v34
	v_mov_b32_e32 v107, v34
	v_mov_b32_e32 v108, v34
	v_mov_b32_e32 v109, v34
	v_mov_b32_e32 v114, v34
	v_mov_b32_e32 v115, v34
	v_mov_b32_e32 v116, v34
	v_mov_b32_e32 v117, v34
	v_mov_b32_e32 v122, v34
	v_mov_b32_e32 v123, v34
	v_mov_b32_e32 v124, v34
	v_mov_b32_e32 v125, v34
	v_mov_b32_e32 v130, v34
	v_mov_b32_e32 v131, v34
	v_mov_b32_e32 v132, v34
	v_mov_b32_e32 v133, v34
	v_mov_b32_e32 v138, v34
	v_mov_b32_e32 v139, v34
	v_mov_b32_e32 v140, v34
	v_mov_b32_e32 v141, v34
	v_mov_b32_e32 v146, v34
	v_mov_b32_e32 v147, v34
	v_mov_b32_e32 v148, v34
	v_mov_b32_e32 v149, v34
	v_mov_b32_e32 v154, v34
	v_mov_b32_e32 v155, v34
	v_mov_b32_e32 v156, v34
	v_mov_b32_e32 v157, v34
	v_mov_b32_e32 v158, v34
	v_mov_b32_e32 v159, v34
	v_mov_b32_e32 v160, v34
	v_mov_b32_e32 v161, v34
	s_branch .LBB0_2259

; #define PG8_STAGE(bufoff, gbase, voff) do { _Pragma("unroll") for (int _i = 0; _i < 2; ++_i) \
;         __builtin_amdgcn_global_load_lds((const unsigned*)((const char*)(gbase) + (voff)[_i]), (PG8_LAS unsigned*)(lds + (bufoff) + ldsw + _i * 8192), 16, 0, 0); } while (0)
; #define PG8_LDA(dst, b, h) do { _Pragma("unroll") for (int m = 0; m < 4; ++m) _Pragma("unroll") for (int k = 0; k < 2; ++k) dst[m][k] = *(const PG8_LAS bf16x8*)(lds + PG8_SA(b, h) + aoff + m * 2048 + k * 1024); } while (0)
; #define PG8_LDB(dst, b, h) do { _Pragma("unroll") for (int n = 0; n < 2; ++n) _Pragma("unroll") for (int k = 0; k < 2; ++k) dst[n][k] = *(const PG8_LAS bf16x8*)(lds + PG8_SB(b, h) + boff + n * 2048 + k * 1024); } while (0)
; #define PG8_WAIT_V(n) asm volatile("s_waitcnt vmcnt(" #n ")" ::: "memory")
; #define PG8_WAIT_L(n) asm volatile("s_waitcnt lgkmcnt(" #n ")" ::: "memory")
; #define PG8_BAR __builtin_amdgcn_s_barrier()
; #define PG8_SCHED __builtin_amdgcn_sched_barrier(0)
; template <class Epi, class Sched, bool ALIGN_EPI = false, bool SP2 = false, bool FP8 = false>
; __device__ __forceinline__ void gemm_phase(PG8_LAS unsigned char* lds, const Gemm g, const Sched& S, const Epi& E) {
;     ...
;             PG8_LDB(B0, 0, 0); PG8_LDB(B1, 0, 1); PG8_SCHED; PG8_LDA(At, 0, 0); PG8_STAGE(PG8_SA(1, 1), a1 + hstep, voffA);
;             PG8_WAIT_V(8); PG8_WAIT_L(0); PG8_BAR; PG8_MMA(0, 0, At, B0); PG8_MMA(0, 1, At, B1); PG8_BAR; PG8_SCHED;
;             PG8_LDA(At, 0, 1); PG8_STAGE(PG8_SB(0, 0), b2, voffB); PG8_STAGE(PG8_SB(0, 1), b2 + hstep, voffB); PG8_STAGE(PG8_SA(0, 0), a2, voffA);
;             PG8_WAIT_V(8); PG8_WAIT_L(0); PG8_BAR; PG8_MMA(1, 0, At, B0); PG8_MMA(1, 1, At, B1); PG8_BAR; PG8_SCHED;
.LBB0_2259:
	ds_read_b128 v[26:29], v186
	ds_read_b128 v[30:33], v186 offset:1024
	ds_read_b128 v[18:21], v186 offset:2048
	ds_read_b128 v[22:25], v186 offset:3072
	ds_read_b128 v[10:13], v187
	ds_read_b128 v[14:17], v187 offset:1024
	ds_read_b128 v[2:5], v187 offset:2048
	ds_read_b128 v[6:9], v187 offset:3072
	s_add_u32 s36, s34, 0xfff20080
	s_addc_u32 s37, s35, -1
	s_cmp_eq_u32 s71, 52
	s_cselect_b64 vcc, -1, 0
	s_cselect_b32 s37, s31, s37
	s_cselect_b32 s36, s30, s36
	v_cndmask_b32_e32 v175, v173, v171, vcc
	v_cndmask_b32_e32 v174, v172, v170, vcc
	v_lshl_add_u64 v[214:215], s[34:35], 0, v[166:167]
	s_add_i32 m0, s48, 0xc000
	ds_read_b128 v[176:179], v188
	ds_read_b128 v[180:183], v188 offset:1024
	ds_read_b128 v[190:193], v188 offset:2048
	ds_read_b128 v[194:197], v188 offset:3072
	ds_read_b128 v[198:201], v188 offset:4096
	ds_read_b128 v[202:205], v188 offset:5120
	ds_read_b128 v[206:209], v188 offset:6144
	ds_read_b128 v[210:213], v188 offset:7168
	global_load_lds_dwordx4 v[214:215], off
	v_lshl_add_u64 v[214:215], s[34:35], 0, v[168:169]
	s_add_i32 m0, s48, 0xe000
	s_nop 0
	global_load_lds_dwordx4 v[214:215], off
	s_waitcnt vmcnt(8)
	s_waitcnt lgkmcnt(0)
	s_barrier
	s_setprio 1
	s_waitcnt lgkmcnt(0)
	v_mfma_f32_16x16x128_f8f6f4 v[158:161], v[26:33], v[176:183], v[158:161]
	v_mfma_f32_16x16x128_f8f6f4 v[154:157], v[18:25], v[176:183], v[154:157]
	v_mfma_f32_16x16x128_f8f6f4 v[146:149], v[26:33], v[190:197], v[146:149]
	v_mfma_f32_16x16x128_f8f6f4 v[138:141], v[18:25], v[190:197], v[138:141]
	v_mfma_f32_16x16x128_f8f6f4 v[130:133], v[26:33], v[198:205], v[130:133]
	v_mfma_f32_16x16x128_f8f6f4 v[122:125], v[18:25], v[198:205], v[122:125]
	v_mfma_f32_16x16x128_f8f6f4 v[114:117], v[26:33], v[206:213], v[114:117]
	v_mfma_f32_16x16x128_f8f6f4 v[106:109], v[18:25], v[206:213], v[106:109]
	s_setprio 0
	s_setprio 1
	v_mfma_f32_16x16x128_f8f6f4 v[150:153], v[10:17], v[176:183], v[150:153]
	v_mfma_f32_16x16x128_f8f6f4 v[142:145], v[2:9], v[176:183], v[142:145]
	v_mfma_f32_16x16x128_f8f6f4 v[134:137], v[10:17], v[190:197], v[134:137]
	v_mfma_f32_16x16x128_f8f6f4 v[126:129], v[2:9], v[190:197], v[126:129]
	v_mfma_f32_16x16x128_f8f6f4 v[118:121], v[10:17], v[198:205], v[118:121]
	v_mfma_f32_16x16x128_f8f6f4 v[110:113], v[2:9], v[198:205], v[110:113]
	v_mfma_f32_16x16x128_f8f6f4 v[102:105], v[10:17], v[206:213], v[102:105]
	v_mfma_f32_16x16x128_f8f6f4 v[98:101], v[2:9], v[206:213], v[98:101]
	s_setprio 0
	s_barrier
	s_add_i32 s72, s57, s47
	v_lshl_add_u64 v[176:177], v[174:175], 0, v[162:163]
	s_mov_b32 m0, s72
	ds_read_b128 v[190:193], v188 offset:16384
	ds_read_b128 v[194:197], v188 offset:17408
	ds_read_b128 v[198:201], v188 offset:18432
	ds_read_b128 v[202:205], v188 offset:19456
	ds_read_b128 v[206:209], v188 offset:20480
	ds_read_b128 v[210:213], v188 offset:21504
	ds_read_b128 v[214:217], v188 offset:22528
	ds_read_b128 v[218:221], v188 offset:23552
	global_load_lds_dwordx4 v[176:177], off
	v_lshl_add_u64 v[178:179], v[174:175], 0, v[164:165]
	s_add_i32 m0, s72, 0x2000
	v_lshl_add_u64 v[180:181], v[174:175], 0, s[6:7]
	s_add_i32 s72, s58, s47
	global_load_lds_dwordx4 v[178:179], off
	v_lshl_add_u64 v[182:183], v[180:181], 0, v[162:163]
	s_mov_b32 m0, s72
	v_lshl_add_u64 v[180:181], v[180:181], 0, v[164:165]
	global_load_lds_dwordx4 v[182:183], off
	s_add_i32 m0, s72, 0x2000
	v_lshl_add_u64 v[182:183], s[36:37], 0, v[164:165]
	global_load_lds_dwordx4 v[180:181], off
	v_lshl_add_u64 v[180:181], s[36:37], 0, v[162:163]
	s_mov_b32 m0, s48
	s_nop 0
	global_load_lds_dwordx4 v[180:181], off
	s_mov_b32 m0, s49
	s_nop 0
	global_load_lds_dwordx4 v[182:183], off
	s_waitcnt vmcnt(8)
	s_waitcnt lgkmcnt(0)
	s_barrier
	s_setprio 1
	s_waitcnt lgkmcnt(0)
	v_mfma_f32_16x16x128_f8f6f4 v[94:97], v[26:33], v[190:197], v[94:97]
	v_mfma_f32_16x16x128_f8f6f4 v[90:93], v[18:25], v[190:197], v[90:93]
	v_mfma_f32_16x16x128_f8f6f4 v[82:85], v[26:33], v[198:205], v[82:85]
	v_mfma_f32_16x16x128_f8f6f4 v[74:77], v[18:25], v[198:205], v[74:77]
	v_mfma_f32_16x16x128_f8f6f4 v[66:69], v[26:33], v[206:213], v[66:69]
	v_mfma_f32_16x16x128_f8f6f4 v[58:61], v[18:25], v[206:213], v[58:61]
	v_mfma_f32_16x16x128_f8f6f4 v[50:53], v[26:33], v[214:221], v[50:53]
	v_mfma_f32_16x16x128_f8f6f4 v[42:45], v[18:25], v[214:221], v[42:45]
	s_setprio 0
	s_setprio 1
	v_mfma_f32_16x16x128_f8f6f4 v[86:89], v[10:17], v[190:197], v[86:89]
	v_mfma_f32_16x16x128_f8f6f4 v[78:81], v[2:9], v[190:197], v[78:81]
	v_mfma_f32_16x16x128_f8f6f4 v[70:73], v[10:17], v[198:205], v[70:73]
	v_mfma_f32_16x16x128_f8f6f4 v[62:65], v[2:9], v[198:205], v[62:65]
	v_mfma_f32_16x16x128_f8f6f4 v[54:57], v[10:17], v[206:213], v[54:57]
	v_mfma_f32_16x16x128_f8f6f4 v[46:49], v[2:9], v[206:213], v[46:49]
	v_mfma_f32_16x16x128_f8f6f4 v[38:41], v[10:17], v[214:221], v[38:41]
	v_mfma_f32_16x16x128_f8f6f4 v[34:37], v[2:9], v[214:221], v[34:37]
	s_setprio 0
	s_barrier
; #define PG8_STAGE(bufoff, gbase, voff) do { _Pragma("unroll") for (int _i = 0; _i < 2; ++_i) \
;         __builtin_amdgcn_global_load_lds((const unsigned*)((const char*)(gbase) + (voff)[_i]), (PG8_LAS unsigned*)(lds + (bufoff) + ldsw + _i * 8192), 16, 0, 0); } while (0)
; #define PG8_LDA(dst, b, h) do { _Pragma("unroll") for (int m = 0; m < 4; ++m) _Pragma("unroll") for (int k = 0; k < 2; ++k) dst[m][k] = *(const PG8_LAS bf16x8*)(lds + PG8_SA(b, h) + aoff + m * 2048 + k * 1024); } while (0)
; #define PG8_LDB(dst, b, h) do { _Pragma("unroll") for (int n = 0; n < 2; ++n) _Pragma("unroll") for (int k = 0; k < 2; ++k) dst[n][k] = *(const PG8_LAS bf16x8*)(lds + PG8_SB(b, h) + boff + n * 2048 + k * 1024); } while (0)
; #define PG8_WAIT_V(n) asm volatile("s_waitcnt vmcnt(" #n ")" ::: "memory")
; #define PG8_WAIT_L(n) asm volatile("s_waitcnt lgkmcnt(" #n ")" ::: "memory")
; #define PG8_BAR __builtin_amdgcn_s_barrier()
; #define PG8_SCHED __builtin_amdgcn_sched_barrier(0)
; template <class Epi, class Sched, bool ALIGN_EPI = false, bool SP2 = false, bool FP8 = false>
; __device__ __forceinline__ void gemm_phase(PG8_LAS unsigned char* lds, const Gemm g, const Sched& S, const Epi& E) {
;     ...
;             PG8_WAIT_V(8); PG8_WAIT_L(0); PG8_BAR; PG8_MMA(1, 0, At, B0); PG8_MMA(1, 1, At, B1); PG8_BAR; PG8_SCHED;
;             PG8_LDB(B0, 1, 0); PG8_LDB(B1, 1, 1); PG8_SCHED; PG8_LDA(At, 1, 0); PG8_STAGE(PG8_SA(0, 1), a2 + hstep, voffA);
;             PG8_WAIT_V(8); PG8_WAIT_L(0); PG8_BAR; PG8_MMA(0, 0, At, B0); PG8_MMA(0, 1, At, B1); PG8_BAR; PG8_SCHED;
;             PG8_LDA(At, 1, 1); PG8_STAGE(PG8_SB(1, 0), b3, voffB); PG8_STAGE(PG8_SB(1, 1), b3 + hstep, voffB); PG8_STAGE(PG8_SA(1, 0), a3, voffA);
;             PG8_WAIT_V(8); PG8_WAIT_L(0); PG8_BAR; PG8_MMA(1, 0, At, B0); PG8_MMA(1, 1, At, B1); PG8_BAR; PG8_SCHED;
;     ...
;         if constexpr (FP8) asm volatile("s_nop 15\n\ts_nop 15\n\ts_nop 15\n\ts_nop 15" ::: "memory");
;         if constexpr (ALIGN_EPI) { if (wr == 0) PG8_BAR; }
	s_add_i32 s72, 0, 0x18000
	s_add_i32 s73, 0, 0x1c000
	v_add_u32_e32 v14, s72, v184
	v_add_u32_e32 v30, s73, v184
	ds_read_b128 v[2:5], v14
	ds_read_b128 v[6:9], v14 offset:1024
	ds_read_b128 v[10:13], v14 offset:2048
	ds_read_b128 v[14:17], v14 offset:3072
	ds_read_b128 v[18:21], v30
	ds_read_b128 v[22:25], v30 offset:1024
	ds_read_b128 v[26:29], v30 offset:2048
	ds_read_b128 v[30:33], v30 offset:3072
	s_add_u32 s36, s36, 0xe0000
	s_addc_u32 s37, s37, 0
	s_mov_b32 m0, s50
	v_lshl_add_u64 v[222:223], s[36:37], 0, v[162:163]
	ds_read_b128 v[190:193], v188 offset:32768
	ds_read_b128 v[194:197], v188 offset:33792
	ds_read_b128 v[198:201], v188 offset:34816
	ds_read_b128 v[202:205], v188 offset:35840
	ds_read_b128 v[206:209], v188 offset:36864
	ds_read_b128 v[210:213], v188 offset:37888
	ds_read_b128 v[214:217], v188 offset:38912
	ds_read_b128 v[218:221], v188 offset:39936
	global_load_lds_dwordx4 v[222:223], off
	v_lshl_add_u64 v[222:223], s[36:37], 0, v[164:165]
	s_mov_b32 m0, s51
	s_nop 0
	global_load_lds_dwordx4 v[222:223], off
	s_waitcnt vmcnt(8)
	s_waitcnt lgkmcnt(0)
	s_barrier
	s_setprio 1
	s_waitcnt lgkmcnt(0)
	v_mfma_f32_16x16x128_f8f6f4 v[158:161], v[2:9], v[190:197], v[158:161]
	v_mfma_f32_16x16x128_f8f6f4 v[154:157], v[10:17], v[190:197], v[154:157]
	v_mfma_f32_16x16x128_f8f6f4 v[146:149], v[2:9], v[198:205], v[146:149]
	v_mfma_f32_16x16x128_f8f6f4 v[138:141], v[10:17], v[198:205], v[138:141]
	v_mfma_f32_16x16x128_f8f6f4 v[130:133], v[2:9], v[206:213], v[130:133]
	v_mfma_f32_16x16x128_f8f6f4 v[122:125], v[10:17], v[206:213], v[122:125]
	v_mfma_f32_16x16x128_f8f6f4 v[114:117], v[2:9], v[214:221], v[114:117]
	v_mfma_f32_16x16x128_f8f6f4 v[106:109], v[10:17], v[214:221], v[106:109]
	s_setprio 0
	s_setprio 1
	v_mfma_f32_16x16x128_f8f6f4 v[150:153], v[18:25], v[190:197], v[150:153]
	v_mfma_f32_16x16x128_f8f6f4 v[142:145], v[26:33], v[190:197], v[142:145]
	v_mfma_f32_16x16x128_f8f6f4 v[134:137], v[18:25], v[198:205], v[134:137]
	v_mfma_f32_16x16x128_f8f6f4 v[126:129], v[26:33], v[198:205], v[126:129]
	v_mfma_f32_16x16x128_f8f6f4 v[118:121], v[18:25], v[206:213], v[118:121]
	v_mfma_f32_16x16x128_f8f6f4 v[110:113], v[26:33], v[206:213], v[110:113]
	v_mfma_f32_16x16x128_f8f6f4 v[102:105], v[18:25], v[214:221], v[102:105]
	v_mfma_f32_16x16x128_f8f6f4 v[98:101], v[26:33], v[214:221], v[98:101]
	s_setprio 0
	s_barrier
	s_add_i32 s36, s72, s47
	v_lshl_add_u64 v[176:177], v[176:177], 0, s[12:13]
	s_mov_b32 m0, s36
	ds_read_b128 v[190:193], v188 offset:49152
	ds_read_b128 v[194:197], v188 offset:50176
	ds_read_b128 v[198:201], v188 offset:51200
	ds_read_b128 v[202:205], v188 offset:52224
	ds_read_b128 v[206:209], v188 offset:53248
	ds_read_b128 v[210:213], v188 offset:54272
	ds_read_b128 v[214:217], v188 offset:55296
	ds_read_b128 v[218:221], v188 offset:56320
	global_load_lds_dwordx4 v[176:177], off
	v_lshl_add_u64 v[176:177], v[178:179], 0, s[12:13]
	s_add_i32 m0, s36, 0x2000
	v_lshl_add_u64 v[174:175], v[174:175], 0, s[14:15]
	s_add_i32 s36, s73, s47
	global_load_lds_dwordx4 v[176:177], off
	v_lshl_add_u64 v[176:177], v[174:175], 0, v[162:163]
	s_mov_b32 m0, s36
	v_lshl_add_u64 v[174:175], v[174:175], 0, v[164:165]
	global_load_lds_dwordx4 v[176:177], off
	s_add_i32 m0, s36, 0x2000
	s_nop 0
	global_load_lds_dwordx4 v[174:175], off
	v_lshl_add_u64 v[174:175], v[180:181], 0, s[12:13]
	s_mov_b32 m0, s55
	s_nop 0
	global_load_lds_dwordx4 v[174:175], off
	v_lshl_add_u64 v[174:175], v[182:183], 0, s[12:13]
	s_mov_b32 m0, s56
	s_nop 0
	global_load_lds_dwordx4 v[174:175], off
	s_waitcnt vmcnt(8)
	s_waitcnt lgkmcnt(0)
	s_barrier
	s_setprio 1
	s_waitcnt lgkmcnt(0)
	v_mfma_f32_16x16x128_f8f6f4 v[94:97], v[2:9], v[190:197], v[94:97]
	v_mfma_f32_16x16x128_f8f6f4 v[90:93], v[10:17], v[190:197], v[90:93]
	v_mfma_f32_16x16x128_f8f6f4 v[82:85], v[2:9], v[198:205], v[82:85]
	v_mfma_f32_16x16x128_f8f6f4 v[74:77], v[10:17], v[198:205], v[74:77]
	v_mfma_f32_16x16x128_f8f6f4 v[66:69], v[2:9], v[206:213], v[66:69]
	v_mfma_f32_16x16x128_f8f6f4 v[58:61], v[10:17], v[206:213], v[58:61]
	v_mfma_f32_16x16x128_f8f6f4 v[50:53], v[2:9], v[214:221], v[50:53]
	v_mfma_f32_16x16x128_f8f6f4 v[42:45], v[10:17], v[214:221], v[42:45]
	s_setprio 0
	s_setprio 1
	v_mfma_f32_16x16x128_f8f6f4 v[86:89], v[18:25], v[190:197], v[86:89]
	v_mfma_f32_16x16x128_f8f6f4 v[78:81], v[26:33], v[190:197], v[78:81]
	v_mfma_f32_16x16x128_f8f6f4 v[70:73], v[18:25], v[198:205], v[70:73]
	v_mfma_f32_16x16x128_f8f6f4 v[62:65], v[26:33], v[198:205], v[62:65]
	v_mfma_f32_16x16x128_f8f6f4 v[54:57], v[18:25], v[206:213], v[54:57]
	v_mfma_f32_16x16x128_f8f6f4 v[46:49], v[26:33], v[206:213], v[46:49]
	v_mfma_f32_16x16x128_f8f6f4 v[38:41], v[18:25], v[214:221], v[38:41]
	v_mfma_f32_16x16x128_f8f6f4 v[34:37], v[26:33], v[214:221], v[34:37]
	s_setprio 0
	s_add_i32 s71, s71, 2
	s_add_u32 s34, s34, 0x100
	s_addc_u32 s35, s35, 0
	s_cmp_gt_u32 s71, 53
	v_lshl_add_u64 v[172:173], v[172:173], 0, s[18:19]
	s_cbranch_scc0 .Lrot_head_2259
	s_barrier
	s_nop 15
	s_nop 15
	s_nop 15
	s_nop 15
	s_and_b64 vcc, exec, s[16:17]
	s_cbranch_vccz .LBB0_2262
	s_barrier
